# v_P with the 8-MFMA groups of all int8/fp8 K-loops reordered so consecutive MFMAs share one operand register block (snake order)
# speedup vs baseline: 1.0135x; 1.0034x over previous
.LBB0_216:
	v_add_u32_e32 v130, s88, v196
	v_add_u32_e32 v134, s89, v196
	ds_read_b128 v[158:161], v130
	ds_read_b128 v[150:153], v130 offset:1024
	ds_read_b128 v[154:157], v130 offset:2048
	ds_read_b128 v[146:149], v130 offset:3072
	ds_read_b128 v[142:145], v134
	ds_read_b128 v[130:133], v134 offset:1024
	ds_read_b128 v[138:141], v134 offset:2048
	ds_read_b128 v[134:137], v134 offset:3072
	s_add_u32 s25, s50, 0xfff80080
	s_addc_u32 s56, s51, -1
	s_and_b64 s[18:19], s[18:19], exec
	s_cselect_b32 s59, s31, s56
	s_cselect_b32 s58, s4, s25
	s_cselect_b32 s57, s5, s64
	s_cselect_b32 s56, s29, s92
	s_add_i32 m0, s39, 0xc000
	ds_read_b128 v[186:189], v198
	ds_read_b128 v[190:193], v198 offset:1024
	ds_read_b128 v[200:203], v198 offset:2048
	ds_read_b128 v[204:207], v198 offset:3072
	ds_read_b128 v[208:211], v198 offset:4096
	ds_read_b128 v[212:215], v198 offset:5120
	ds_read_b128 v[216:219], v198 offset:6144
	ds_read_b128 v[220:223], v198 offset:7168
	global_load_lds_dwordx4 v170, s[50:51]
	s_add_i32 m0, s39, 0xe000
	s_nop 0
	global_load_lds_dwordx4 v172, s[50:51]
	s_waitcnt vmcnt(8)
	s_waitcnt lgkmcnt(0)
	s_barrier
	s_setprio 1
	s_waitcnt lgkmcnt(0)
	v_mfma_i32_16x16x64_i8 v[126:129], v[158:161], v[186:189], v[126:129]
	v_mfma_i32_16x16x64_i8 v[122:125], v[154:157], v[186:189], v[122:125]
	v_mfma_i32_16x16x64_i8 v[106:109], v[154:157], v[200:203], v[106:109]
	v_mfma_i32_16x16x64_i8 v[110:113], v[158:161], v[200:203], v[110:113]
	v_mfma_i32_16x16x64_i8 v[94:97], v[158:161], v[208:211], v[94:97]
	v_mfma_i32_16x16x64_i8 v[90:93], v[154:157], v[208:211], v[90:93]
	v_mfma_i32_16x16x64_i8 v[74:77], v[154:157], v[216:219], v[74:77]
	v_mfma_i32_16x16x64_i8 v[78:81], v[158:161], v[216:219], v[78:81]
	s_nop 0
	v_mfma_i32_16x16x64_i8 v[126:129], v[150:153], v[190:193], v[126:129]
	v_mfma_i32_16x16x64_i8 v[122:125], v[146:149], v[190:193], v[122:125]
	v_mfma_i32_16x16x64_i8 v[106:109], v[146:149], v[204:207], v[106:109]
	v_mfma_i32_16x16x64_i8 v[110:113], v[150:153], v[204:207], v[110:113]
	v_mfma_i32_16x16x64_i8 v[94:97], v[150:153], v[212:215], v[94:97]
	v_mfma_i32_16x16x64_i8 v[90:93], v[146:149], v[212:215], v[90:93]
	v_mfma_i32_16x16x64_i8 v[74:77], v[146:149], v[220:223], v[74:77]
	v_mfma_i32_16x16x64_i8 v[78:81], v[150:153], v[220:223], v[78:81]
	s_setprio 0
	s_setprio 1
	v_mfma_i32_16x16x64_i8 v[118:121], v[142:145], v[186:189], v[118:121]
	v_mfma_i32_16x16x64_i8 v[114:117], v[138:141], v[186:189], v[114:117]
	v_mfma_i32_16x16x64_i8 v[98:101], v[138:141], v[200:203], v[98:101]
	v_mfma_i32_16x16x64_i8 v[102:105], v[142:145], v[200:203], v[102:105]
	v_mfma_i32_16x16x64_i8 v[86:89], v[142:145], v[208:211], v[86:89]
	v_mfma_i32_16x16x64_i8 v[82:85], v[138:141], v[208:211], v[82:85]
	v_mfma_i32_16x16x64_i8 v[66:69], v[138:141], v[216:219], v[66:69]
	v_mfma_i32_16x16x64_i8 v[70:73], v[142:145], v[216:219], v[70:73]
	s_nop 0
	v_mfma_i32_16x16x64_i8 v[118:121], v[130:133], v[190:193], v[118:121]
	v_mfma_i32_16x16x64_i8 v[114:117], v[134:137], v[190:193], v[114:117]
	v_mfma_i32_16x16x64_i8 v[98:101], v[134:137], v[204:207], v[98:101]
	v_mfma_i32_16x16x64_i8 v[102:105], v[130:133], v[204:207], v[102:105]
	v_mfma_i32_16x16x64_i8 v[86:89], v[130:133], v[212:215], v[86:89]
	v_mfma_i32_16x16x64_i8 v[82:85], v[134:137], v[212:215], v[82:85]
	v_mfma_i32_16x16x64_i8 v[66:69], v[134:137], v[220:223], v[66:69]
	v_mfma_i32_16x16x64_i8 v[70:73], v[130:133], v[220:223], v[70:73]
	s_setprio 0
	s_barrier
	s_add_i32 s18, s88, s7
	s_mov_b32 m0, s18
	ds_read_b128 v[200:203], v198 offset:16384
	ds_read_b128 v[204:207], v198 offset:17408
	ds_read_b128 v[208:211], v198 offset:18432
	ds_read_b128 v[212:215], v198 offset:19456
	ds_read_b128 v[216:219], v198 offset:20480
	ds_read_b128 v[220:223], v198 offset:21504
	ds_read_b128 v[224:227], v198 offset:22528
	ds_read_b128 v[228:231], v198 offset:23552
	global_load_lds_dwordx4 v164, s[56:57]
	s_add_i32 m0, s18, 0x2000
	s_add_u32 s18, s56, 0x80000
	s_addc_u32 s19, s57, 0
	s_add_i32 s25, s89, s7
	global_load_lds_dwordx4 v168, s[56:57]
	s_mov_b32 m0, s25
	s_nop 0
	global_load_lds_dwordx4 v164, s[18:19]
	s_add_i32 m0, s25, 0x2000
	s_nop 0
	global_load_lds_dwordx4 v168, s[18:19]
	s_mov_b32 m0, s39
	s_nop 0
	global_load_lds_dwordx4 v162, s[58:59]
	s_mov_b32 m0, s43
	s_nop 0
	global_load_lds_dwordx4 v166, s[58:59]
	s_waitcnt vmcnt(8)
	s_waitcnt lgkmcnt(0)
	s_barrier
	s_setprio 1
	s_waitcnt lgkmcnt(0)
	v_mfma_i32_16x16x64_i8 v[62:65], v[158:161], v[200:203], v[62:65]
	v_mfma_i32_16x16x64_i8 v[58:61], v[154:157], v[200:203], v[58:61]
	v_mfma_i32_16x16x64_i8 v[42:45], v[154:157], v[208:211], v[42:45]
	v_mfma_i32_16x16x64_i8 v[46:49], v[158:161], v[208:211], v[46:49]
	v_mfma_i32_16x16x64_i8 v[30:33], v[158:161], v[216:219], v[30:33]
	v_mfma_i32_16x16x64_i8 v[26:29], v[154:157], v[216:219], v[26:29]
	v_mfma_i32_16x16x64_i8 v[10:13], v[154:157], v[224:227], v[10:13]
	v_mfma_i32_16x16x64_i8 v[14:17], v[158:161], v[224:227], v[14:17]
	s_nop 0
	v_mfma_i32_16x16x64_i8 v[62:65], v[150:153], v[204:207], v[62:65]
	v_mfma_i32_16x16x64_i8 v[58:61], v[146:149], v[204:207], v[58:61]
	v_mfma_i32_16x16x64_i8 v[42:45], v[146:149], v[212:215], v[42:45]
	v_mfma_i32_16x16x64_i8 v[46:49], v[150:153], v[212:215], v[46:49]
	v_mfma_i32_16x16x64_i8 v[30:33], v[150:153], v[220:223], v[30:33]
	v_mfma_i32_16x16x64_i8 v[26:29], v[146:149], v[220:223], v[26:29]
	v_mfma_i32_16x16x64_i8 v[10:13], v[146:149], v[228:231], v[10:13]
	v_mfma_i32_16x16x64_i8 v[14:17], v[150:153], v[228:231], v[14:17]
	s_setprio 0
	s_setprio 1
	v_mfma_i32_16x16x64_i8 v[54:57], v[142:145], v[200:203], v[54:57]
	v_mfma_i32_16x16x64_i8 v[50:53], v[138:141], v[200:203], v[50:53]
	v_mfma_i32_16x16x64_i8 v[34:37], v[138:141], v[208:211], v[34:37]
	v_mfma_i32_16x16x64_i8 v[38:41], v[142:145], v[208:211], v[38:41]
	v_mfma_i32_16x16x64_i8 v[22:25], v[142:145], v[216:219], v[22:25]
	v_mfma_i32_16x16x64_i8 v[18:21], v[138:141], v[216:219], v[18:21]
	v_mfma_i32_16x16x64_i8 v[2:5], v[138:141], v[224:227], v[2:5]
	v_mfma_i32_16x16x64_i8 v[6:9], v[142:145], v[224:227], v[6:9]
	s_nop 0
	v_mfma_i32_16x16x64_i8 v[54:57], v[130:133], v[204:207], v[54:57]
	v_mfma_i32_16x16x64_i8 v[50:53], v[134:137], v[204:207], v[50:53]
	v_mfma_i32_16x16x64_i8 v[34:37], v[134:137], v[212:215], v[34:37]
	v_mfma_i32_16x16x64_i8 v[38:41], v[130:133], v[212:215], v[38:41]
	v_mfma_i32_16x16x64_i8 v[22:25], v[130:133], v[220:223], v[22:25]
	v_mfma_i32_16x16x64_i8 v[18:21], v[134:137], v[220:223], v[18:21]
	v_mfma_i32_16x16x64_i8 v[2:5], v[134:137], v[228:231], v[2:5]
	v_mfma_i32_16x16x64_i8 v[6:9], v[130:133], v[228:231], v[6:9]
	s_setprio 0
	s_barrier
	s_add_i32 s25, 0, 0x18000
	s_add_i32 vcc_lo, 0, 0x1c000
	v_add_u32_e32 v142, s25, v196
	v_add_u32_e32 v158, vcc_lo, v196
	ds_read_b128 v[130:133], v142
	ds_read_b128 v[134:137], v142 offset:1024
	ds_read_b128 v[138:141], v142 offset:2048
	ds_read_b128 v[142:145], v142 offset:3072
	ds_read_b128 v[146:149], v158
	ds_read_b128 v[150:153], v158 offset:1024
	ds_read_b128 v[154:157], v158 offset:2048
	ds_read_b128 v[158:161], v158 offset:3072
	s_add_u32 s18, s58, 0x80000
	s_addc_u32 s19, s59, 0
	s_mov_b32 m0, s61
	ds_read_b128 v[200:203], v198 offset:32768
	ds_read_b128 v[204:207], v198 offset:33792
	ds_read_b128 v[208:211], v198 offset:34816
	ds_read_b128 v[212:215], v198 offset:35840
	ds_read_b128 v[216:219], v198 offset:36864
	ds_read_b128 v[220:223], v198 offset:37888
	ds_read_b128 v[224:227], v198 offset:38912
	ds_read_b128 v[228:231], v198 offset:39936
	global_load_lds_dwordx4 v162, s[18:19]
	s_mov_b32 m0, s62
	s_nop 0
	global_load_lds_dwordx4 v166, s[18:19]
	s_waitcnt vmcnt(8)
	s_waitcnt lgkmcnt(0)
	s_barrier
	s_setprio 1
	s_waitcnt lgkmcnt(0)
	v_mfma_i32_16x16x64_i8 v[126:129], v[130:133], v[200:203], v[126:129]
	v_mfma_i32_16x16x64_i8 v[122:125], v[138:141], v[200:203], v[122:125]
	v_mfma_i32_16x16x64_i8 v[106:109], v[138:141], v[208:211], v[106:109]
	v_mfma_i32_16x16x64_i8 v[110:113], v[130:133], v[208:211], v[110:113]
	v_mfma_i32_16x16x64_i8 v[94:97], v[130:133], v[216:219], v[94:97]
	v_mfma_i32_16x16x64_i8 v[90:93], v[138:141], v[216:219], v[90:93]
	v_mfma_i32_16x16x64_i8 v[74:77], v[138:141], v[224:227], v[74:77]
	v_mfma_i32_16x16x64_i8 v[78:81], v[130:133], v[224:227], v[78:81]
	s_nop 0
	v_mfma_i32_16x16x64_i8 v[126:129], v[134:137], v[204:207], v[126:129]
	v_mfma_i32_16x16x64_i8 v[122:125], v[142:145], v[204:207], v[122:125]
	v_mfma_i32_16x16x64_i8 v[106:109], v[142:145], v[212:215], v[106:109]
	v_mfma_i32_16x16x64_i8 v[110:113], v[134:137], v[212:215], v[110:113]
	v_mfma_i32_16x16x64_i8 v[94:97], v[134:137], v[220:223], v[94:97]
	v_mfma_i32_16x16x64_i8 v[90:93], v[142:145], v[220:223], v[90:93]
	v_mfma_i32_16x16x64_i8 v[74:77], v[142:145], v[228:231], v[74:77]
	v_mfma_i32_16x16x64_i8 v[78:81], v[134:137], v[228:231], v[78:81]
	s_setprio 0
	s_setprio 1
	v_mfma_i32_16x16x64_i8 v[118:121], v[146:149], v[200:203], v[118:121]
	v_mfma_i32_16x16x64_i8 v[114:117], v[154:157], v[200:203], v[114:117]
	v_mfma_i32_16x16x64_i8 v[98:101], v[154:157], v[208:211], v[98:101]
	v_mfma_i32_16x16x64_i8 v[102:105], v[146:149], v[208:211], v[102:105]
	v_mfma_i32_16x16x64_i8 v[86:89], v[146:149], v[216:219], v[86:89]
	v_mfma_i32_16x16x64_i8 v[82:85], v[154:157], v[216:219], v[82:85]
	v_mfma_i32_16x16x64_i8 v[66:69], v[154:157], v[224:227], v[66:69]
	v_mfma_i32_16x16x64_i8 v[70:73], v[146:149], v[224:227], v[70:73]
	s_nop 0
	v_mfma_i32_16x16x64_i8 v[118:121], v[150:153], v[204:207], v[118:121]
	v_mfma_i32_16x16x64_i8 v[114:117], v[158:161], v[204:207], v[114:117]
	v_mfma_i32_16x16x64_i8 v[98:101], v[158:161], v[212:215], v[98:101]
	v_mfma_i32_16x16x64_i8 v[102:105], v[150:153], v[212:215], v[102:105]
	v_mfma_i32_16x16x64_i8 v[86:89], v[150:153], v[220:223], v[86:89]
	v_mfma_i32_16x16x64_i8 v[82:85], v[158:161], v[220:223], v[82:85]
	v_mfma_i32_16x16x64_i8 v[66:69], v[158:161], v[228:231], v[66:69]
	v_mfma_i32_16x16x64_i8 v[70:73], v[150:153], v[228:231], v[70:73]
	s_setprio 0
	s_barrier
	s_add_i32 s18, s25, s7
	s_mov_b32 m0, s18
	s_add_u32 s98, s56, 0x80
	s_addc_u32 s99, s57, 0
	s_add_u32 s100, s58, 0x80
	s_addc_u32 s101, s59, 0
	ds_read_b128 v[200:203], v198 offset:49152
	ds_read_b128 v[204:207], v198 offset:50176
	ds_read_b128 v[208:211], v198 offset:51200
	ds_read_b128 v[212:215], v198 offset:52224
	ds_read_b128 v[216:219], v198 offset:53248
	ds_read_b128 v[220:223], v198 offset:54272
	ds_read_b128 v[224:227], v198 offset:55296
	ds_read_b128 v[228:231], v198 offset:56320
	global_load_lds_dwordx4 v164, s[98:99]
	s_add_i32 m0, s18, 0x2000
	s_add_u32 s18, s56, 0x80080
	s_addc_u32 s19, s57, 0
	s_add_i32 s25, vcc_lo, s7
	global_load_lds_dwordx4 v168, s[98:99]
	s_mov_b32 m0, s25
	s_nop 0
	global_load_lds_dwordx4 v164, s[18:19]
	s_add_i32 m0, s25, 0x2000
	s_nop 0
	global_load_lds_dwordx4 v168, s[18:19]
	s_mov_b32 m0, s67
	s_nop 0
	global_load_lds_dwordx4 v162, s[100:101]
	s_mov_b32 m0, s68
	s_nop 0
	global_load_lds_dwordx4 v166, s[100:101]
	s_waitcnt vmcnt(8)
	s_waitcnt lgkmcnt(0)
	s_barrier
	s_setprio 1
	s_waitcnt lgkmcnt(0)
	v_mfma_i32_16x16x64_i8 v[62:65], v[130:133], v[200:203], v[62:65]
	v_mfma_i32_16x16x64_i8 v[58:61], v[138:141], v[200:203], v[58:61]
	v_mfma_i32_16x16x64_i8 v[42:45], v[138:141], v[208:211], v[42:45]
	v_mfma_i32_16x16x64_i8 v[46:49], v[130:133], v[208:211], v[46:49]
	v_mfma_i32_16x16x64_i8 v[30:33], v[130:133], v[216:219], v[30:33]
	v_mfma_i32_16x16x64_i8 v[26:29], v[138:141], v[216:219], v[26:29]
	v_mfma_i32_16x16x64_i8 v[10:13], v[138:141], v[224:227], v[10:13]
	v_mfma_i32_16x16x64_i8 v[14:17], v[130:133], v[224:227], v[14:17]
	s_nop 0
	v_mfma_i32_16x16x64_i8 v[62:65], v[134:137], v[204:207], v[62:65]
	v_mfma_i32_16x16x64_i8 v[58:61], v[142:145], v[204:207], v[58:61]
	v_mfma_i32_16x16x64_i8 v[42:45], v[142:145], v[212:215], v[42:45]
	v_mfma_i32_16x16x64_i8 v[46:49], v[134:137], v[212:215], v[46:49]
	v_mfma_i32_16x16x64_i8 v[30:33], v[134:137], v[220:223], v[30:33]
	v_mfma_i32_16x16x64_i8 v[26:29], v[142:145], v[220:223], v[26:29]
	v_mfma_i32_16x16x64_i8 v[10:13], v[142:145], v[228:231], v[10:13]
	v_mfma_i32_16x16x64_i8 v[14:17], v[134:137], v[228:231], v[14:17]
	s_setprio 0
	s_setprio 1
	v_mfma_i32_16x16x64_i8 v[54:57], v[146:149], v[200:203], v[54:57]
	v_mfma_i32_16x16x64_i8 v[50:53], v[154:157], v[200:203], v[50:53]
	v_mfma_i32_16x16x64_i8 v[34:37], v[154:157], v[208:211], v[34:37]
	v_mfma_i32_16x16x64_i8 v[38:41], v[146:149], v[208:211], v[38:41]
	v_mfma_i32_16x16x64_i8 v[22:25], v[146:149], v[216:219], v[22:25]
	v_mfma_i32_16x16x64_i8 v[18:21], v[154:157], v[216:219], v[18:21]
	v_mfma_i32_16x16x64_i8 v[2:5], v[154:157], v[224:227], v[2:5]
	v_mfma_i32_16x16x64_i8 v[6:9], v[146:149], v[224:227], v[6:9]
	s_nop 0
	v_mfma_i32_16x16x64_i8 v[54:57], v[150:153], v[204:207], v[54:57]
	v_mfma_i32_16x16x64_i8 v[50:53], v[158:161], v[204:207], v[50:53]
	v_mfma_i32_16x16x64_i8 v[34:37], v[158:161], v[212:215], v[34:37]
	v_mfma_i32_16x16x64_i8 v[38:41], v[150:153], v[212:215], v[38:41]
	v_mfma_i32_16x16x64_i8 v[22:25], v[150:153], v[220:223], v[22:25]
	v_mfma_i32_16x16x64_i8 v[18:21], v[158:161], v[220:223], v[18:21]
	v_mfma_i32_16x16x64_i8 v[2:5], v[158:161], v[228:231], v[2:5]
	v_mfma_i32_16x16x64_i8 v[6:9], v[150:153], v[228:231], v[6:9]
	s_setprio 0
	s_barrier
	s_add_i32 s65, s65, 2
	s_add_u32 s50, s50, 0x100
	s_addc_u32 s51, s51, 0
	s_add_u32 s92, s92, 0x100
	s_addc_u32 s64, s64, 0
	s_cmp_gt_u32 s65, 29
	s_cbranch_scc1 .LBB0_219

.LBB0_318:
	ds_read_b128 v[26:29], v185
	ds_read_b128 v[30:33], v185 offset:1024
	ds_read_b128 v[18:21], v185 offset:2048
	ds_read_b128 v[22:25], v185 offset:3072
	ds_read_b128 v[10:13], v186
	ds_read_b128 v[14:17], v186 offset:1024
	ds_read_b128 v[2:5], v186 offset:2048
	ds_read_b128 v[6:9], v186 offset:3072
	s_add_u32 s24, s26, 0xffea8080
	s_addc_u32 s25, s27, -1
	s_cmpk_eq_i32 s58, 0x52
	s_cselect_b32 s31, s5, s25
	s_cselect_b32 s30, s4, s24
	s_cselect_b32 s29, s21, s51
	s_cselect_b32 s28, s20, s50
	v_lshl_add_u64 v[212:213], s[26:27], 0, v[166:167]
	s_add_i32 m0, s7, 0xc000
	ds_read_b128 v[174:177], v187
	ds_read_b128 v[178:181], v187 offset:1024
	ds_read_b128 v[188:191], v187 offset:2048
	ds_read_b128 v[192:195], v187 offset:3072
	ds_read_b128 v[196:199], v187 offset:4096
	ds_read_b128 v[200:203], v187 offset:5120
	ds_read_b128 v[204:207], v187 offset:6144
	ds_read_b128 v[208:211], v187 offset:7168
	global_load_lds_dwordx4 v[212:213], off
	v_lshl_add_u64 v[212:213], s[26:27], 0, v[168:169]
	s_add_i32 m0, s7, 0xe000
	s_nop 0
	global_load_lds_dwordx4 v[212:213], off
	s_waitcnt vmcnt(8)
	s_waitcnt lgkmcnt(0)
	s_barrier
	s_setprio 1
	s_waitcnt lgkmcnt(0)
	v_mfma_scale_f32_16x16x128_f8f6f4 v[158:161], v[26:33], v[174:181], v[158:161], v1, v1 op_sel_hi:[0,0,0]
	v_mfma_scale_f32_16x16x128_f8f6f4 v[154:157], v[18:25], v[174:181], v[154:157], v1, v1 op_sel_hi:[0,0,0]
	v_mfma_scale_f32_16x16x128_f8f6f4 v[138:141], v[18:25], v[188:195], v[138:141], v1, v1 op_sel_hi:[0,0,0]
	v_mfma_scale_f32_16x16x128_f8f6f4 v[142:145], v[26:33], v[188:195], v[142:145], v1, v1 op_sel_hi:[0,0,0]
	v_mfma_scale_f32_16x16x128_f8f6f4 v[126:129], v[26:33], v[196:203], v[126:129], v1, v1 op_sel_hi:[0,0,0]
	v_mfma_scale_f32_16x16x128_f8f6f4 v[122:125], v[18:25], v[196:203], v[122:125], v1, v1 op_sel_hi:[0,0,0]
	v_mfma_scale_f32_16x16x128_f8f6f4 v[106:109], v[18:25], v[204:211], v[106:109], v1, v1 op_sel_hi:[0,0,0]
	v_mfma_scale_f32_16x16x128_f8f6f4 v[110:113], v[26:33], v[204:211], v[110:113], v1, v1 op_sel_hi:[0,0,0]
	s_setprio 0
	s_setprio 1
	v_mfma_scale_f32_16x16x128_f8f6f4 v[150:153], v[10:17], v[174:181], v[150:153], v1, v1 op_sel_hi:[0,0,0]
	v_mfma_scale_f32_16x16x128_f8f6f4 v[146:149], v[2:9], v[174:181], v[146:149], v1, v1 op_sel_hi:[0,0,0]
	v_mfma_scale_f32_16x16x128_f8f6f4 v[130:133], v[2:9], v[188:195], v[130:133], v1, v1 op_sel_hi:[0,0,0]
	v_mfma_scale_f32_16x16x128_f8f6f4 v[134:137], v[10:17], v[188:195], v[134:137], v1, v1 op_sel_hi:[0,0,0]
	v_mfma_scale_f32_16x16x128_f8f6f4 v[118:121], v[10:17], v[196:203], v[118:121], v1, v1 op_sel_hi:[0,0,0]
	v_mfma_scale_f32_16x16x128_f8f6f4 v[114:117], v[2:9], v[196:203], v[114:117], v1, v1 op_sel_hi:[0,0,0]
	v_mfma_scale_f32_16x16x128_f8f6f4 v[98:101], v[2:9], v[204:211], v[98:101], v1, v1 op_sel_hi:[0,0,0]
	v_mfma_scale_f32_16x16x128_f8f6f4 v[102:105], v[10:17], v[204:211], v[102:105], v1, v1 op_sel_hi:[0,0,0]
	s_setprio 0
	s_barrier
	s_add_i32 s24, s42, s3
	v_lshl_add_u64 v[174:175], s[28:29], 0, v[164:165]
	s_mov_b32 m0, s24
	ds_read_b128 v[188:191], v187 offset:16384
	ds_read_b128 v[192:195], v187 offset:17408
	ds_read_b128 v[196:199], v187 offset:18432
	ds_read_b128 v[200:203], v187 offset:19456
	ds_read_b128 v[204:207], v187 offset:20480
	ds_read_b128 v[208:211], v187 offset:21504
	ds_read_b128 v[212:215], v187 offset:22528
	ds_read_b128 v[216:219], v187 offset:23552
	global_load_lds_dwordx4 v[174:175], off
	s_add_i32 m0, s24, 0x2000
	s_add_u32 s24, s28, 0x158000
	v_lshl_add_u64 v[176:177], s[28:29], 0, v[162:163]
	s_addc_u32 s25, s29, 0
	s_add_i32 s59, s43, s3
	global_load_lds_dwordx4 v[176:177], off
	v_lshl_add_u64 v[178:179], s[24:25], 0, v[164:165]
	s_mov_b32 m0, s59
	v_lshl_add_u64 v[180:181], s[30:31], 0, v[162:163]
	global_load_lds_dwordx4 v[178:179], off
	v_lshl_add_u64 v[178:179], s[24:25], 0, v[162:163]
	s_add_i32 m0, s59, 0x2000
	s_nop 0
	global_load_lds_dwordx4 v[178:179], off
	v_lshl_add_u64 v[178:179], s[30:31], 0, v[164:165]
	s_mov_b32 m0, s7
	s_nop 0
	global_load_lds_dwordx4 v[178:179], off
	s_mov_b32 m0, s17
	s_nop 0
	global_load_lds_dwordx4 v[180:181], off
	s_waitcnt vmcnt(8)
	s_waitcnt lgkmcnt(0)
	s_barrier
	s_setprio 1
	s_waitcnt lgkmcnt(0)
	v_mfma_scale_f32_16x16x128_f8f6f4 v[94:97], v[26:33], v[188:195], v[94:97], v1, v1 op_sel_hi:[0,0,0]
	v_mfma_scale_f32_16x16x128_f8f6f4 v[90:93], v[18:25], v[188:195], v[90:93], v1, v1 op_sel_hi:[0,0,0]
	v_mfma_scale_f32_16x16x128_f8f6f4 v[74:77], v[18:25], v[196:203], v[74:77], v1, v1 op_sel_hi:[0,0,0]
	v_mfma_scale_f32_16x16x128_f8f6f4 v[78:81], v[26:33], v[196:203], v[78:81], v1, v1 op_sel_hi:[0,0,0]
	v_mfma_scale_f32_16x16x128_f8f6f4 v[62:65], v[26:33], v[204:211], v[62:65], v1, v1 op_sel_hi:[0,0,0]
	v_mfma_scale_f32_16x16x128_f8f6f4 v[58:61], v[18:25], v[204:211], v[58:61], v1, v1 op_sel_hi:[0,0,0]
	v_mfma_scale_f32_16x16x128_f8f6f4 v[42:45], v[18:25], v[212:219], v[42:45], v1, v1 op_sel_hi:[0,0,0]
	v_mfma_scale_f32_16x16x128_f8f6f4 v[46:49], v[26:33], v[212:219], v[46:49], v1, v1 op_sel_hi:[0,0,0]
	s_setprio 0
	s_setprio 1
	v_mfma_scale_f32_16x16x128_f8f6f4 v[86:89], v[10:17], v[188:195], v[86:89], v1, v1 op_sel_hi:[0,0,0]
	v_mfma_scale_f32_16x16x128_f8f6f4 v[82:85], v[2:9], v[188:195], v[82:85], v1, v1 op_sel_hi:[0,0,0]
	v_mfma_scale_f32_16x16x128_f8f6f4 v[66:69], v[2:9], v[196:203], v[66:69], v1, v1 op_sel_hi:[0,0,0]
	v_mfma_scale_f32_16x16x128_f8f6f4 v[70:73], v[10:17], v[196:203], v[70:73], v1, v1 op_sel_hi:[0,0,0]
	v_mfma_scale_f32_16x16x128_f8f6f4 v[54:57], v[10:17], v[204:211], v[54:57], v1, v1 op_sel_hi:[0,0,0]
	v_mfma_scale_f32_16x16x128_f8f6f4 v[50:53], v[2:9], v[204:211], v[50:53], v1, v1 op_sel_hi:[0,0,0]
	v_mfma_scale_f32_16x16x128_f8f6f4 v[34:37], v[2:9], v[212:219], v[34:37], v1, v1 op_sel_hi:[0,0,0]
	v_mfma_scale_f32_16x16x128_f8f6f4 v[38:41], v[10:17], v[212:219], v[38:41], v1, v1 op_sel_hi:[0,0,0]
	s_setprio 0
	s_barrier
	s_add_i32 s59, 0, 0x18000
	s_add_i32 s60, 0, 0x1c000
	v_add_u32_e32 v14, s59, v183
	v_add_u32_e32 v30, s60, v183
	ds_read_b128 v[2:5], v14
	ds_read_b128 v[6:9], v14 offset:1024
	ds_read_b128 v[10:13], v14 offset:2048
	ds_read_b128 v[14:17], v14 offset:3072
	ds_read_b128 v[18:21], v30
	ds_read_b128 v[22:25], v30 offset:1024
	ds_read_b128 v[26:29], v30 offset:2048
	ds_read_b128 v[30:33], v30 offset:3072
	s_add_u32 s24, s30, 0x158000
	s_addc_u32 s25, s31, 0
	s_mov_b32 m0, s34
	v_lshl_add_u64 v[220:221], s[24:25], 0, v[164:165]
	ds_read_b128 v[188:191], v187 offset:32768
	ds_read_b128 v[192:195], v187 offset:33792
	ds_read_b128 v[196:199], v187 offset:34816
	ds_read_b128 v[200:203], v187 offset:35840
	ds_read_b128 v[204:207], v187 offset:36864
	ds_read_b128 v[208:211], v187 offset:37888
	ds_read_b128 v[212:215], v187 offset:38912
	ds_read_b128 v[216:219], v187 offset:39936
	global_load_lds_dwordx4 v[220:221], off
	v_lshl_add_u64 v[220:221], s[24:25], 0, v[162:163]
	s_mov_b32 m0, s35
	s_nop 0
	global_load_lds_dwordx4 v[220:221], off
	s_waitcnt vmcnt(8)
	s_waitcnt lgkmcnt(0)
	s_barrier
	s_setprio 1
	s_waitcnt lgkmcnt(0)
	v_mfma_scale_f32_16x16x128_f8f6f4 v[158:161], v[2:9], v[188:195], v[158:161], v1, v1 op_sel_hi:[0,0,0]
	v_mfma_scale_f32_16x16x128_f8f6f4 v[154:157], v[10:17], v[188:195], v[154:157], v1, v1 op_sel_hi:[0,0,0]
	v_mfma_scale_f32_16x16x128_f8f6f4 v[138:141], v[10:17], v[196:203], v[138:141], v1, v1 op_sel_hi:[0,0,0]
	v_mfma_scale_f32_16x16x128_f8f6f4 v[142:145], v[2:9], v[196:203], v[142:145], v1, v1 op_sel_hi:[0,0,0]
	v_mfma_scale_f32_16x16x128_f8f6f4 v[126:129], v[2:9], v[204:211], v[126:129], v1, v1 op_sel_hi:[0,0,0]
	v_mfma_scale_f32_16x16x128_f8f6f4 v[122:125], v[10:17], v[204:211], v[122:125], v1, v1 op_sel_hi:[0,0,0]
	v_mfma_scale_f32_16x16x128_f8f6f4 v[106:109], v[10:17], v[212:219], v[106:109], v1, v1 op_sel_hi:[0,0,0]
	v_mfma_scale_f32_16x16x128_f8f6f4 v[110:113], v[2:9], v[212:219], v[110:113], v1, v1 op_sel_hi:[0,0,0]
	s_setprio 0
	s_setprio 1
	v_mfma_scale_f32_16x16x128_f8f6f4 v[150:153], v[18:25], v[188:195], v[150:153], v1, v1 op_sel_hi:[0,0,0]
	v_mfma_scale_f32_16x16x128_f8f6f4 v[146:149], v[26:33], v[188:195], v[146:149], v1, v1 op_sel_hi:[0,0,0]
	v_mfma_scale_f32_16x16x128_f8f6f4 v[130:133], v[26:33], v[196:203], v[130:133], v1, v1 op_sel_hi:[0,0,0]
	v_mfma_scale_f32_16x16x128_f8f6f4 v[134:137], v[18:25], v[196:203], v[134:137], v1, v1 op_sel_hi:[0,0,0]
	v_mfma_scale_f32_16x16x128_f8f6f4 v[118:121], v[18:25], v[204:211], v[118:121], v1, v1 op_sel_hi:[0,0,0]
	v_mfma_scale_f32_16x16x128_f8f6f4 v[114:117], v[26:33], v[204:211], v[114:117], v1, v1 op_sel_hi:[0,0,0]
	v_mfma_scale_f32_16x16x128_f8f6f4 v[98:101], v[26:33], v[212:219], v[98:101], v1, v1 op_sel_hi:[0,0,0]
	v_mfma_scale_f32_16x16x128_f8f6f4 v[102:105], v[18:25], v[212:219], v[102:105], v1, v1 op_sel_hi:[0,0,0]
	s_setprio 0
	s_barrier
	s_add_i32 s24, s59, s3
	v_lshl_add_u64 v[174:175], v[174:175], 0, s[12:13]
	s_mov_b32 m0, s24
	ds_read_b128 v[188:191], v187 offset:49152
	ds_read_b128 v[192:195], v187 offset:50176
	ds_read_b128 v[196:199], v187 offset:51200
	ds_read_b128 v[200:203], v187 offset:52224
	ds_read_b128 v[204:207], v187 offset:53248
	ds_read_b128 v[208:211], v187 offset:54272
	ds_read_b128 v[212:215], v187 offset:55296
	ds_read_b128 v[216:219], v187 offset:56320
	global_load_lds_dwordx4 v[174:175], off
	s_add_i32 m0, s24, 0x2000
	s_add_u32 s24, s28, 0x158080
	v_lshl_add_u64 v[174:175], v[176:177], 0, s[12:13]
	s_addc_u32 s25, s29, 0
	s_add_i32 s28, s60, s3
	global_load_lds_dwordx4 v[174:175], off
	v_lshl_add_u64 v[174:175], s[24:25], 0, v[164:165]
	s_mov_b32 m0, s28
	s_nop 0
	global_load_lds_dwordx4 v[174:175], off
	v_lshl_add_u64 v[174:175], s[24:25], 0, v[162:163]
	s_add_i32 m0, s28, 0x2000
	s_nop 0
	global_load_lds_dwordx4 v[174:175], off
	v_lshl_add_u64 v[174:175], v[178:179], 0, s[12:13]
	s_mov_b32 m0, s38
	s_nop 0
	global_load_lds_dwordx4 v[174:175], off
	v_lshl_add_u64 v[174:175], v[180:181], 0, s[12:13]
	s_mov_b32 m0, s39
	s_nop 0
	global_load_lds_dwordx4 v[174:175], off
	s_waitcnt vmcnt(8)
	s_waitcnt lgkmcnt(0)
	s_barrier
	s_setprio 1
	s_waitcnt lgkmcnt(0)
	v_mfma_scale_f32_16x16x128_f8f6f4 v[94:97], v[2:9], v[188:195], v[94:97], v1, v1 op_sel_hi:[0,0,0]
	v_mfma_scale_f32_16x16x128_f8f6f4 v[90:93], v[10:17], v[188:195], v[90:93], v1, v1 op_sel_hi:[0,0,0]
	v_mfma_scale_f32_16x16x128_f8f6f4 v[74:77], v[10:17], v[196:203], v[74:77], v1, v1 op_sel_hi:[0,0,0]
	v_mfma_scale_f32_16x16x128_f8f6f4 v[78:81], v[2:9], v[196:203], v[78:81], v1, v1 op_sel_hi:[0,0,0]
	v_mfma_scale_f32_16x16x128_f8f6f4 v[62:65], v[2:9], v[204:211], v[62:65], v1, v1 op_sel_hi:[0,0,0]
	v_mfma_scale_f32_16x16x128_f8f6f4 v[58:61], v[10:17], v[204:211], v[58:61], v1, v1 op_sel_hi:[0,0,0]
	v_mfma_scale_f32_16x16x128_f8f6f4 v[42:45], v[10:17], v[212:219], v[42:45], v1, v1 op_sel_hi:[0,0,0]
	v_mfma_scale_f32_16x16x128_f8f6f4 v[46:49], v[2:9], v[212:219], v[46:49], v1, v1 op_sel_hi:[0,0,0]
	s_setprio 0
	s_setprio 1
	v_mfma_scale_f32_16x16x128_f8f6f4 v[86:89], v[18:25], v[188:195], v[86:89], v1, v1 op_sel_hi:[0,0,0]
	v_mfma_scale_f32_16x16x128_f8f6f4 v[82:85], v[26:33], v[188:195], v[82:85], v1, v1 op_sel_hi:[0,0,0]
	v_mfma_scale_f32_16x16x128_f8f6f4 v[66:69], v[26:33], v[196:203], v[66:69], v1, v1 op_sel_hi:[0,0,0]
	v_mfma_scale_f32_16x16x128_f8f6f4 v[70:73], v[18:25], v[196:203], v[70:73], v1, v1 op_sel_hi:[0,0,0]
	v_mfma_scale_f32_16x16x128_f8f6f4 v[54:57], v[18:25], v[204:211], v[54:57], v1, v1 op_sel_hi:[0,0,0]
	v_mfma_scale_f32_16x16x128_f8f6f4 v[50:53], v[26:33], v[204:211], v[50:53], v1, v1 op_sel_hi:[0,0,0]
	v_mfma_scale_f32_16x16x128_f8f6f4 v[34:37], v[26:33], v[212:219], v[34:37], v1, v1 op_sel_hi:[0,0,0]
	v_mfma_scale_f32_16x16x128_f8f6f4 v[38:41], v[18:25], v[212:219], v[38:41], v1, v1 op_sel_hi:[0,0,0]
	s_setprio 0
	s_barrier
	s_add_i32 s58, s58, 2
	s_add_u32 s26, s26, 0x100
	s_addc_u32 s27, s27, 0
	s_add_u32 s50, s50, 0x100
	s_addc_u32 s51, s51, 0
	s_cmpk_gt_u32 s58, 0x53
	s_cbranch_scc0 .LBB0_318
	s_and_b64 vcc, exec, s[14:15]
	s_cbranch_vccz .LBB0_321
	s_barrier

.LBB0_332:
	s_add_u32 s6, s61, s4
	s_addc_u32 s7, s62, s5
	s_add_u32 s6, s6, 0x32800100
	s_addc_u32 s7, s7, 0
	s_add_u32 s24, s63, s4
	s_addc_u32 s25, s68, s5
	s_add_i32 s64, 0, 0x10000
	s_cmpk_eq_i32 s4, 0x2a00
	s_cselect_b32 s13, s1, s7
	s_cselect_b32 s12, s0, s6
	s_cselect_b32 s7, s29, s25
	s_cselect_b32 s6, s28, s24
	s_add_i32 s65, 0, 0x14000
	v_add_u32_e32 v2, s64, v188
	v_add_u32_e32 v6, s65, v188
	ds_read_b128 v[26:29], v2
	ds_read_b128 v[30:33], v2 offset:1024
	ds_read_b128 v[18:21], v2 offset:2048
	ds_read_b128 v[22:25], v2 offset:3072
	ds_read_b128 v[10:13], v6
	ds_read_b128 v[14:17], v6 offset:1024
	ds_read_b128 v[2:5], v6 offset:2048
	ds_read_b128 v[6:9], v6 offset:3072
	v_lshl_add_u64 v[214:215], v[168:169], 0, s[4:5]
	s_add_i32 m0, s18, 0xc000
	ds_read_b128 v[172:175], v189
	ds_read_b128 v[176:179], v189 offset:1024
	ds_read_b128 v[190:193], v189 offset:2048
	ds_read_b128 v[194:197], v189 offset:3072
	ds_read_b128 v[198:201], v189 offset:4096
	ds_read_b128 v[202:205], v189 offset:5120
	ds_read_b128 v[206:209], v189 offset:6144
	ds_read_b128 v[210:213], v189 offset:7168
	global_load_lds_dwordx4 v[214:215], off
	v_lshl_add_u64 v[214:215], v[170:171], 0, s[4:5]
	s_add_i32 m0, s18, 0xe000
	s_nop 0
	global_load_lds_dwordx4 v[214:215], off
	s_waitcnt vmcnt(8)
	s_waitcnt lgkmcnt(0)
	s_barrier
	s_setprio 1
	s_waitcnt lgkmcnt(0)
	v_mfma_scale_f32_16x16x128_f8f6f4 v[70:73], v[26:33], v[172:179], v[70:73], v187, v187 op_sel_hi:[0,0,0]
	v_mfma_scale_f32_16x16x128_f8f6f4 v[66:69], v[18:25], v[172:179], v[66:69], v187, v187 op_sel_hi:[0,0,0]
	v_mfma_scale_f32_16x16x128_f8f6f4 v[74:77], v[18:25], v[190:197], v[74:77], v187, v187 op_sel_hi:[0,0,0]
	v_mfma_scale_f32_16x16x128_f8f6f4 v[78:81], v[26:33], v[190:197], v[78:81], v187, v187 op_sel_hi:[0,0,0]
	v_mfma_scale_f32_16x16x128_f8f6f4 v[86:89], v[26:33], v[198:205], v[86:89], v187, v187 op_sel_hi:[0,0,0]
	v_mfma_scale_f32_16x16x128_f8f6f4 v[82:85], v[18:25], v[198:205], v[82:85], v187, v187 op_sel_hi:[0,0,0]
	v_mfma_scale_f32_16x16x128_f8f6f4 v[90:93], v[18:25], v[206:213], v[90:93], v187, v187 op_sel_hi:[0,0,0]
	v_mfma_scale_f32_16x16x128_f8f6f4 v[94:97], v[26:33], v[206:213], v[94:97], v187, v187 op_sel_hi:[0,0,0]
	s_setprio 0
	s_setprio 1
	v_mfma_scale_f32_16x16x128_f8f6f4 v[158:161], v[10:17], v[172:179], v[158:161], v187, v187 op_sel_hi:[0,0,0]
	v_mfma_scale_f32_16x16x128_f8f6f4 v[154:157], v[2:9], v[172:179], v[154:157], v187, v187 op_sel_hi:[0,0,0]
	v_mfma_scale_f32_16x16x128_f8f6f4 v[146:149], v[2:9], v[190:197], v[146:149], v187, v187 op_sel_hi:[0,0,0]
	v_mfma_scale_f32_16x16x128_f8f6f4 v[150:153], v[10:17], v[190:197], v[150:153], v187, v187 op_sel_hi:[0,0,0]
	v_mfma_scale_f32_16x16x128_f8f6f4 v[142:145], v[10:17], v[198:205], v[142:145], v187, v187 op_sel_hi:[0,0,0]
	v_mfma_scale_f32_16x16x128_f8f6f4 v[138:141], v[2:9], v[198:205], v[138:141], v187, v187 op_sel_hi:[0,0,0]
	v_mfma_scale_f32_16x16x128_f8f6f4 v[130:133], v[2:9], v[206:213], v[130:133], v187, v187 op_sel_hi:[0,0,0]
	v_mfma_scale_f32_16x16x128_f8f6f4 v[134:137], v[10:17], v[206:213], v[134:137], v187, v187 op_sel_hi:[0,0,0]
	s_setprio 0
	s_barrier
	s_add_i32 s24, s64, s17
	v_lshl_add_u64 v[172:173], s[6:7], 0, v[162:163]
	s_mov_b32 m0, s24
	ds_read_b128 v[190:193], v189 offset:16384
	ds_read_b128 v[194:197], v189 offset:17408
	ds_read_b128 v[198:201], v189 offset:18432
	ds_read_b128 v[202:205], v189 offset:19456
	ds_read_b128 v[206:209], v189 offset:20480
	ds_read_b128 v[210:213], v189 offset:21504
	ds_read_b128 v[214:217], v189 offset:22528
	ds_read_b128 v[218:221], v189 offset:23552
	global_load_lds_dwordx4 v[172:173], off
	s_add_i32 m0, s24, 0x2000
	s_add_u32 s24, s6, 0x158000
	v_lshl_add_u64 v[174:175], s[6:7], 0, v[166:167]
	s_addc_u32 s25, s7, 0
	s_add_i32 s64, s65, s17
	global_load_lds_dwordx4 v[174:175], off
	v_lshl_add_u64 v[176:177], s[24:25], 0, v[162:163]
	s_mov_b32 m0, s64
	v_lshl_add_u64 v[178:179], s[12:13], 0, v[166:167]
	global_load_lds_dwordx4 v[176:177], off
	v_lshl_add_u64 v[176:177], s[24:25], 0, v[166:167]
	s_add_i32 m0, s64, 0x2000
	s_nop 0
	global_load_lds_dwordx4 v[176:177], off
	v_lshl_add_u64 v[176:177], s[12:13], 0, v[162:163]
	s_mov_b32 m0, s18
	s_nop 0
	global_load_lds_dwordx4 v[176:177], off
	s_mov_b32 m0, s19
	s_nop 0
	global_load_lds_dwordx4 v[178:179], off
	s_waitcnt vmcnt(8)
	s_waitcnt lgkmcnt(0)
	s_barrier
	s_setprio 1
	s_waitcnt lgkmcnt(0)
	v_mfma_scale_f32_16x16x128_f8f6f4 v[102:105], v[26:33], v[190:197], v[102:105], v187, v187 op_sel_hi:[0,0,0]
	v_mfma_scale_f32_16x16x128_f8f6f4 v[98:101], v[18:25], v[190:197], v[98:101], v187, v187 op_sel_hi:[0,0,0]
	v_mfma_scale_f32_16x16x128_f8f6f4 v[106:109], v[18:25], v[198:205], v[106:109], v187, v187 op_sel_hi:[0,0,0]
	v_mfma_scale_f32_16x16x128_f8f6f4 v[110:113], v[26:33], v[198:205], v[110:113], v187, v187 op_sel_hi:[0,0,0]
	v_mfma_scale_f32_16x16x128_f8f6f4 v[118:121], v[26:33], v[206:213], v[118:121], v187, v187 op_sel_hi:[0,0,0]
	v_mfma_scale_f32_16x16x128_f8f6f4 v[114:117], v[18:25], v[206:213], v[114:117], v187, v187 op_sel_hi:[0,0,0]
	v_mfma_scale_f32_16x16x128_f8f6f4 v[122:125], v[18:25], v[214:221], v[122:125], v187, v187 op_sel_hi:[0,0,0]
	v_mfma_scale_f32_16x16x128_f8f6f4 v[126:129], v[26:33], v[214:221], v[126:129], v187, v187 op_sel_hi:[0,0,0]
	s_setprio 0
	s_setprio 1
	v_mfma_scale_f32_16x16x128_f8f6f4 v[38:41], v[10:17], v[190:197], v[38:41], v187, v187 op_sel_hi:[0,0,0]
	v_mfma_scale_f32_16x16x128_f8f6f4 v[34:37], v[2:9], v[190:197], v[34:37], v187, v187 op_sel_hi:[0,0,0]
	v_mfma_scale_f32_16x16x128_f8f6f4 v[42:45], v[2:9], v[198:205], v[42:45], v187, v187 op_sel_hi:[0,0,0]
	v_mfma_scale_f32_16x16x128_f8f6f4 v[46:49], v[10:17], v[198:205], v[46:49], v187, v187 op_sel_hi:[0,0,0]
	v_mfma_scale_f32_16x16x128_f8f6f4 v[54:57], v[10:17], v[206:213], v[54:57], v187, v187 op_sel_hi:[0,0,0]
	v_mfma_scale_f32_16x16x128_f8f6f4 v[50:53], v[2:9], v[206:213], v[50:53], v187, v187 op_sel_hi:[0,0,0]
	v_mfma_scale_f32_16x16x128_f8f6f4 v[58:61], v[2:9], v[214:221], v[58:61], v187, v187 op_sel_hi:[0,0,0]
	v_mfma_scale_f32_16x16x128_f8f6f4 v[62:65], v[10:17], v[214:221], v[62:65], v187, v187 op_sel_hi:[0,0,0]
	s_setprio 0
	s_barrier
	s_add_i32 s24, 0, 0x18000
	s_add_i32 s25, 0, 0x1c000
	v_add_u32_e32 v14, s24, v188
	v_add_u32_e32 v30, s25, v188
	ds_read_b128 v[2:5], v14
	ds_read_b128 v[6:9], v14 offset:1024
	ds_read_b128 v[10:13], v14 offset:2048
	ds_read_b128 v[14:17], v14 offset:3072
	ds_read_b128 v[18:21], v30
	ds_read_b128 v[22:25], v30 offset:1024
	ds_read_b128 v[26:29], v30 offset:2048
	ds_read_b128 v[30:33], v30 offset:3072
	s_add_u32 s12, s12, 0x158000
	s_addc_u32 s13, s13, 0
	s_mov_b32 m0, s93
	v_lshl_add_u64 v[222:223], s[12:13], 0, v[162:163]
	ds_read_b128 v[190:193], v189 offset:32768
	ds_read_b128 v[194:197], v189 offset:33792
	ds_read_b128 v[198:201], v189 offset:34816
	ds_read_b128 v[202:205], v189 offset:35840
	ds_read_b128 v[206:209], v189 offset:36864
	ds_read_b128 v[210:213], v189 offset:37888
	ds_read_b128 v[214:217], v189 offset:38912
	ds_read_b128 v[218:221], v189 offset:39936
	global_load_lds_dwordx4 v[222:223], off
	v_lshl_add_u64 v[222:223], s[12:13], 0, v[166:167]
	s_mov_b32 m0, s94
	s_nop 0
	global_load_lds_dwordx4 v[222:223], off
	s_waitcnt vmcnt(8)
	s_waitcnt lgkmcnt(0)
	s_barrier
	s_setprio 1
	s_waitcnt lgkmcnt(0)
	v_mfma_scale_f32_16x16x128_f8f6f4 v[70:73], v[2:9], v[190:197], v[70:73], v187, v187 op_sel_hi:[0,0,0]
	v_mfma_scale_f32_16x16x128_f8f6f4 v[66:69], v[10:17], v[190:197], v[66:69], v187, v187 op_sel_hi:[0,0,0]
	v_mfma_scale_f32_16x16x128_f8f6f4 v[74:77], v[10:17], v[198:205], v[74:77], v187, v187 op_sel_hi:[0,0,0]
	v_mfma_scale_f32_16x16x128_f8f6f4 v[78:81], v[2:9], v[198:205], v[78:81], v187, v187 op_sel_hi:[0,0,0]
	v_mfma_scale_f32_16x16x128_f8f6f4 v[86:89], v[2:9], v[206:213], v[86:89], v187, v187 op_sel_hi:[0,0,0]
	v_mfma_scale_f32_16x16x128_f8f6f4 v[82:85], v[10:17], v[206:213], v[82:85], v187, v187 op_sel_hi:[0,0,0]
	v_mfma_scale_f32_16x16x128_f8f6f4 v[90:93], v[10:17], v[214:221], v[90:93], v187, v187 op_sel_hi:[0,0,0]
	v_mfma_scale_f32_16x16x128_f8f6f4 v[94:97], v[2:9], v[214:221], v[94:97], v187, v187 op_sel_hi:[0,0,0]
	s_setprio 0
	s_setprio 1
	v_mfma_scale_f32_16x16x128_f8f6f4 v[158:161], v[18:25], v[190:197], v[158:161], v187, v187 op_sel_hi:[0,0,0]
	v_mfma_scale_f32_16x16x128_f8f6f4 v[154:157], v[26:33], v[190:197], v[154:157], v187, v187 op_sel_hi:[0,0,0]
	v_mfma_scale_f32_16x16x128_f8f6f4 v[146:149], v[26:33], v[198:205], v[146:149], v187, v187 op_sel_hi:[0,0,0]
	v_mfma_scale_f32_16x16x128_f8f6f4 v[150:153], v[18:25], v[198:205], v[150:153], v187, v187 op_sel_hi:[0,0,0]
	v_mfma_scale_f32_16x16x128_f8f6f4 v[142:145], v[18:25], v[206:213], v[142:145], v187, v187 op_sel_hi:[0,0,0]
	v_mfma_scale_f32_16x16x128_f8f6f4 v[138:141], v[26:33], v[206:213], v[138:141], v187, v187 op_sel_hi:[0,0,0]
	v_mfma_scale_f32_16x16x128_f8f6f4 v[130:133], v[26:33], v[214:221], v[130:133], v187, v187 op_sel_hi:[0,0,0]
	v_mfma_scale_f32_16x16x128_f8f6f4 v[134:137], v[18:25], v[214:221], v[134:137], v187, v187 op_sel_hi:[0,0,0]
	s_setprio 0
	s_barrier
	s_add_i32 s12, s24, s17
	v_lshl_add_u64 v[172:173], v[172:173], 0, s[76:77]
	s_mov_b32 m0, s12
	ds_read_b128 v[190:193], v189 offset:49152
	ds_read_b128 v[194:197], v189 offset:50176
	ds_read_b128 v[198:201], v189 offset:51200
	ds_read_b128 v[202:205], v189 offset:52224
	ds_read_b128 v[206:209], v189 offset:53248
	ds_read_b128 v[210:213], v189 offset:54272
	ds_read_b128 v[214:217], v189 offset:55296
	ds_read_b128 v[218:221], v189 offset:56320
	global_load_lds_dwordx4 v[172:173], off
	s_add_i32 m0, s12, 0x2000
	s_add_u32 s6, s6, 0x158080
	v_lshl_add_u64 v[172:173], v[174:175], 0, s[76:77]
	s_addc_u32 s7, s7, 0
	s_add_i32 s12, s25, s17
	global_load_lds_dwordx4 v[172:173], off
	v_lshl_add_u64 v[172:173], s[6:7], 0, v[162:163]
	s_mov_b32 m0, s12
	s_nop 0
	global_load_lds_dwordx4 v[172:173], off
	v_lshl_add_u64 v[172:173], s[6:7], 0, v[166:167]
	s_add_i32 m0, s12, 0x2000
	s_nop 0
	global_load_lds_dwordx4 v[172:173], off
	v_lshl_add_u64 v[172:173], v[176:177], 0, s[76:77]
	s_mov_b32 m0, s95
	s_nop 0
	global_load_lds_dwordx4 v[172:173], off
	v_lshl_add_u64 v[172:173], v[178:179], 0, s[76:77]
	s_mov_b32 m0, vcc_lo
	s_nop 0
	global_load_lds_dwordx4 v[172:173], off
	s_waitcnt vmcnt(8)
	s_waitcnt lgkmcnt(0)
	s_barrier
	s_setprio 1
	s_waitcnt lgkmcnt(0)
	v_mfma_scale_f32_16x16x128_f8f6f4 v[102:105], v[2:9], v[190:197], v[102:105], v187, v187 op_sel_hi:[0,0,0]
	v_mfma_scale_f32_16x16x128_f8f6f4 v[98:101], v[10:17], v[190:197], v[98:101], v187, v187 op_sel_hi:[0,0,0]
	v_mfma_scale_f32_16x16x128_f8f6f4 v[106:109], v[10:17], v[198:205], v[106:109], v187, v187 op_sel_hi:[0,0,0]
	v_mfma_scale_f32_16x16x128_f8f6f4 v[110:113], v[2:9], v[198:205], v[110:113], v187, v187 op_sel_hi:[0,0,0]
	v_mfma_scale_f32_16x16x128_f8f6f4 v[118:121], v[2:9], v[206:213], v[118:121], v187, v187 op_sel_hi:[0,0,0]
	v_mfma_scale_f32_16x16x128_f8f6f4 v[114:117], v[10:17], v[206:213], v[114:117], v187, v187 op_sel_hi:[0,0,0]
	v_mfma_scale_f32_16x16x128_f8f6f4 v[122:125], v[10:17], v[214:221], v[122:125], v187, v187 op_sel_hi:[0,0,0]
	v_mfma_scale_f32_16x16x128_f8f6f4 v[126:129], v[2:9], v[214:221], v[126:129], v187, v187 op_sel_hi:[0,0,0]
	s_setprio 0
	s_setprio 1
	v_mfma_scale_f32_16x16x128_f8f6f4 v[38:41], v[18:25], v[190:197], v[38:41], v187, v187 op_sel_hi:[0,0,0]
	v_mfma_scale_f32_16x16x128_f8f6f4 v[34:37], v[26:33], v[190:197], v[34:37], v187, v187 op_sel_hi:[0,0,0]
	v_mfma_scale_f32_16x16x128_f8f6f4 v[42:45], v[26:33], v[198:205], v[42:45], v187, v187 op_sel_hi:[0,0,0]
	v_mfma_scale_f32_16x16x128_f8f6f4 v[46:49], v[18:25], v[198:205], v[46:49], v187, v187 op_sel_hi:[0,0,0]
	v_mfma_scale_f32_16x16x128_f8f6f4 v[54:57], v[18:25], v[206:213], v[54:57], v187, v187 op_sel_hi:[0,0,0]
	v_mfma_scale_f32_16x16x128_f8f6f4 v[50:53], v[26:33], v[206:213], v[50:53], v187, v187 op_sel_hi:[0,0,0]
	v_mfma_scale_f32_16x16x128_f8f6f4 v[58:61], v[26:33], v[214:221], v[58:61], v187, v187 op_sel_hi:[0,0,0]
	v_mfma_scale_f32_16x16x128_f8f6f4 v[62:65], v[18:25], v[214:221], v[62:65], v187, v187 op_sel_hi:[0,0,0]
	s_setprio 0
	s_barrier
	s_add_i32 vcc_hi, vcc_hi, 2
	s_add_u32 s4, s4, 0x100
	s_addc_u32 s5, s5, 0
	s_cmpk_lt_u32 vcc_hi, 0x54
	s_cbranch_scc1 .LBB0_332
	s_waitcnt vmcnt(0)
	s_mov_b64 s[12:13], s[54:55]
	s_cmpk_gt_u32 s89, 0xff
	s_cbranch_scc1 .LBB0_335
	s_barrier

.LBB0_788:
	v_add_u32_e32 v130, s15, v190
	v_add_u32_e32 v134, s50, v190
	ds_read_b128 v[158:161], v130
	ds_read_b128 v[150:153], v130 offset:1024
	ds_read_b128 v[154:157], v130 offset:2048
	ds_read_b128 v[146:149], v130 offset:3072
	ds_read_b128 v[142:145], v134
	ds_read_b128 v[130:133], v134 offset:1024
	ds_read_b128 v[138:141], v134 offset:2048
	ds_read_b128 v[134:137], v134 offset:3072
	s_add_u32 s36, s34, 0xfff80080
	s_addc_u32 s37, s35, -1
	s_and_b64 s[0:1], s[0:1], exec
	s_cselect_b32 s39, s21, s37
	s_cselect_b32 s38, s60, s36
	s_cselect_b32 s37, s17, s63
	s_cselect_b32 s36, s61, s62
	s_add_i32 m0, s29, 0xc000
	ds_read_b128 v[182:185], v193
	ds_read_b128 v[186:189], v193 offset:1024
	ds_read_b128 v[194:197], v193 offset:2048
	ds_read_b128 v[198:201], v193 offset:3072
	ds_read_b128 v[202:205], v193 offset:4096
	ds_read_b128 v[206:209], v193 offset:5120
	ds_read_b128 v[210:213], v193 offset:6144
	ds_read_b128 v[214:217], v193 offset:7168
	global_load_lds_dwordx4 v172, s[34:35]
	s_add_i32 m0, s29, 0xe000
	s_nop 0
	global_load_lds_dwordx4 v174, s[34:35]
	s_waitcnt vmcnt(8)
	s_waitcnt lgkmcnt(0)
	s_barrier
	s_setprio 1
	s_waitcnt lgkmcnt(0)
	v_mfma_i32_16x16x64_i8 v[126:129], v[158:161], v[182:185], v[126:129]
	v_mfma_i32_16x16x64_i8 v[122:125], v[154:157], v[182:185], v[122:125]
	v_mfma_i32_16x16x64_i8 v[106:109], v[154:157], v[194:197], v[106:109]
	v_mfma_i32_16x16x64_i8 v[114:117], v[158:161], v[194:197], v[114:117]
	v_mfma_i32_16x16x64_i8 v[98:101], v[158:161], v[202:205], v[98:101]
	v_mfma_i32_16x16x64_i8 v[90:93], v[154:157], v[202:205], v[90:93]
	v_mfma_i32_16x16x64_i8 v[74:77], v[154:157], v[210:213], v[74:77]
	v_mfma_i32_16x16x64_i8 v[82:85], v[158:161], v[210:213], v[82:85]
	s_nop 0
	v_mfma_i32_16x16x64_i8 v[126:129], v[150:153], v[186:189], v[126:129]
	v_mfma_i32_16x16x64_i8 v[122:125], v[146:149], v[186:189], v[122:125]
	v_mfma_i32_16x16x64_i8 v[106:109], v[146:149], v[198:201], v[106:109]
	v_mfma_i32_16x16x64_i8 v[114:117], v[150:153], v[198:201], v[114:117]
	v_mfma_i32_16x16x64_i8 v[98:101], v[150:153], v[206:209], v[98:101]
	v_mfma_i32_16x16x64_i8 v[90:93], v[146:149], v[206:209], v[90:93]
	v_mfma_i32_16x16x64_i8 v[74:77], v[146:149], v[214:217], v[74:77]
	v_mfma_i32_16x16x64_i8 v[82:85], v[150:153], v[214:217], v[82:85]
	s_setprio 0
	s_setprio 1
	v_mfma_i32_16x16x64_i8 v[118:121], v[142:145], v[182:185], v[118:121]
	v_mfma_i32_16x16x64_i8 v[110:113], v[138:141], v[182:185], v[110:113]
	v_mfma_i32_16x16x64_i8 v[94:97], v[138:141], v[194:197], v[94:97]
	v_mfma_i32_16x16x64_i8 v[102:105], v[142:145], v[194:197], v[102:105]
	v_mfma_i32_16x16x64_i8 v[86:89], v[142:145], v[202:205], v[86:89]
	v_mfma_i32_16x16x64_i8 v[78:81], v[138:141], v[202:205], v[78:81]
	v_mfma_i32_16x16x64_i8 v[66:69], v[138:141], v[210:213], v[66:69]
	v_mfma_i32_16x16x64_i8 v[70:73], v[142:145], v[210:213], v[70:73]
	s_nop 0
	v_mfma_i32_16x16x64_i8 v[118:121], v[130:133], v[186:189], v[118:121]
	v_mfma_i32_16x16x64_i8 v[110:113], v[134:137], v[186:189], v[110:113]
	v_mfma_i32_16x16x64_i8 v[94:97], v[134:137], v[198:201], v[94:97]
	v_mfma_i32_16x16x64_i8 v[102:105], v[130:133], v[198:201], v[102:105]
	v_mfma_i32_16x16x64_i8 v[86:89], v[130:133], v[206:209], v[86:89]
	v_mfma_i32_16x16x64_i8 v[78:81], v[134:137], v[206:209], v[78:81]
	v_mfma_i32_16x16x64_i8 v[66:69], v[134:137], v[214:217], v[66:69]
	v_mfma_i32_16x16x64_i8 v[70:73], v[130:133], v[214:217], v[70:73]
	s_setprio 0
	s_barrier
	s_add_i32 s0, s15, s40
	s_mov_b32 m0, s0
	ds_read_b128 v[194:197], v193 offset:16384
	ds_read_b128 v[198:201], v193 offset:17408
	ds_read_b128 v[202:205], v193 offset:18432
	ds_read_b128 v[206:209], v193 offset:19456
	ds_read_b128 v[210:213], v193 offset:20480
	ds_read_b128 v[214:217], v193 offset:21504
	ds_read_b128 v[218:221], v193 offset:22528
	ds_read_b128 v[222:225], v193 offset:23552
	global_load_lds_dwordx4 v164, s[36:37]
	s_add_i32 m0, s0, 0x2000
	s_add_u32 s0, s36, 0x80000
	s_addc_u32 s1, s37, 0
	s_add_i32 s66, s50, s40
	global_load_lds_dwordx4 v168, s[36:37]
	s_mov_b32 m0, s66
	s_nop 0
	global_load_lds_dwordx4 v164, s[0:1]
	s_add_i32 m0, s66, 0x2000
	s_nop 0
	global_load_lds_dwordx4 v168, s[0:1]
	s_mov_b32 m0, s29
	s_nop 0
	global_load_lds_dwordx4 v162, s[38:39]
	s_mov_b32 m0, s31
	s_nop 0
	global_load_lds_dwordx4 v166, s[38:39]
	s_waitcnt vmcnt(8)
	s_waitcnt lgkmcnt(0)
	s_barrier
	s_setprio 1
	s_waitcnt lgkmcnt(0)
	v_mfma_i32_16x16x64_i8 v[62:65], v[158:161], v[194:197], v[62:65]
	v_mfma_i32_16x16x64_i8 v[58:61], v[154:157], v[194:197], v[58:61]
	v_mfma_i32_16x16x64_i8 v[42:45], v[154:157], v[202:205], v[42:45]
	v_mfma_i32_16x16x64_i8 v[50:53], v[158:161], v[202:205], v[50:53]
	v_mfma_i32_16x16x64_i8 v[34:37], v[158:161], v[210:213], v[34:37]
	v_mfma_i32_16x16x64_i8 v[26:29], v[154:157], v[210:213], v[26:29]
	v_mfma_i32_16x16x64_i8 v[10:13], v[154:157], v[218:221], v[10:13]
	v_mfma_i32_16x16x64_i8 v[18:21], v[158:161], v[218:221], v[18:21]
	s_nop 0
	v_mfma_i32_16x16x64_i8 v[62:65], v[150:153], v[198:201], v[62:65]
	v_mfma_i32_16x16x64_i8 v[58:61], v[146:149], v[198:201], v[58:61]
	v_mfma_i32_16x16x64_i8 v[42:45], v[146:149], v[206:209], v[42:45]
	v_mfma_i32_16x16x64_i8 v[50:53], v[150:153], v[206:209], v[50:53]
	v_mfma_i32_16x16x64_i8 v[34:37], v[150:153], v[214:217], v[34:37]
	v_mfma_i32_16x16x64_i8 v[26:29], v[146:149], v[214:217], v[26:29]
	v_mfma_i32_16x16x64_i8 v[10:13], v[146:149], v[222:225], v[10:13]
	v_mfma_i32_16x16x64_i8 v[18:21], v[150:153], v[222:225], v[18:21]
	s_setprio 0
	s_setprio 1
	v_mfma_i32_16x16x64_i8 v[54:57], v[142:145], v[194:197], v[54:57]
	v_mfma_i32_16x16x64_i8 v[46:49], v[138:141], v[194:197], v[46:49]
	v_mfma_i32_16x16x64_i8 v[30:33], v[138:141], v[202:205], v[30:33]
	v_mfma_i32_16x16x64_i8 v[38:41], v[142:145], v[202:205], v[38:41]
	v_mfma_i32_16x16x64_i8 v[22:25], v[142:145], v[210:213], v[22:25]
	v_mfma_i32_16x16x64_i8 v[14:17], v[138:141], v[210:213], v[14:17]
	v_mfma_i32_16x16x64_i8 v[2:5], v[138:141], v[218:221], v[2:5]
	v_mfma_i32_16x16x64_i8 v[6:9], v[142:145], v[218:221], v[6:9]
	s_nop 0
	v_mfma_i32_16x16x64_i8 v[54:57], v[130:133], v[198:201], v[54:57]
	v_mfma_i32_16x16x64_i8 v[46:49], v[134:137], v[198:201], v[46:49]
	v_mfma_i32_16x16x64_i8 v[30:33], v[134:137], v[206:209], v[30:33]
	v_mfma_i32_16x16x64_i8 v[38:41], v[130:133], v[206:209], v[38:41]
	v_mfma_i32_16x16x64_i8 v[22:25], v[130:133], v[214:217], v[22:25]
	v_mfma_i32_16x16x64_i8 v[14:17], v[134:137], v[214:217], v[14:17]
	v_mfma_i32_16x16x64_i8 v[2:5], v[134:137], v[222:225], v[2:5]
	v_mfma_i32_16x16x64_i8 v[6:9], v[130:133], v[222:225], v[6:9]
	s_setprio 0
	s_barrier
	s_add_i32 s66, 0, 0x18000
	s_add_i32 s67, 0, 0x1c000
	v_add_u32_e32 v142, s66, v190
	v_add_u32_e32 v158, s67, v190
	ds_read_b128 v[130:133], v142
	ds_read_b128 v[134:137], v142 offset:1024
	ds_read_b128 v[138:141], v142 offset:2048
	ds_read_b128 v[142:145], v142 offset:3072
	ds_read_b128 v[146:149], v158
	ds_read_b128 v[150:153], v158 offset:1024
	ds_read_b128 v[154:157], v158 offset:2048
	ds_read_b128 v[158:161], v158 offset:3072
	s_add_u32 s0, s38, 0x80000
	s_addc_u32 s1, s39, 0
	s_mov_b32 m0, s42
	ds_read_b128 v[194:197], v193 offset:32768
	ds_read_b128 v[198:201], v193 offset:33792
	ds_read_b128 v[202:205], v193 offset:34816
	ds_read_b128 v[206:209], v193 offset:35840
	ds_read_b128 v[210:213], v193 offset:36864
	ds_read_b128 v[214:217], v193 offset:37888
	ds_read_b128 v[218:221], v193 offset:38912
	ds_read_b128 v[222:225], v193 offset:39936
	global_load_lds_dwordx4 v162, s[0:1]
	s_mov_b32 m0, s43
	s_nop 0
	global_load_lds_dwordx4 v166, s[0:1]
	s_waitcnt vmcnt(8)
	s_waitcnt lgkmcnt(0)
	s_barrier
	s_setprio 1
	s_waitcnt lgkmcnt(0)
	v_mfma_i32_16x16x64_i8 v[126:129], v[130:133], v[194:197], v[126:129]
	v_mfma_i32_16x16x64_i8 v[122:125], v[138:141], v[194:197], v[122:125]
	v_mfma_i32_16x16x64_i8 v[106:109], v[138:141], v[202:205], v[106:109]
	v_mfma_i32_16x16x64_i8 v[114:117], v[130:133], v[202:205], v[114:117]
	v_mfma_i32_16x16x64_i8 v[98:101], v[130:133], v[210:213], v[98:101]
	v_mfma_i32_16x16x64_i8 v[90:93], v[138:141], v[210:213], v[90:93]
	v_mfma_i32_16x16x64_i8 v[74:77], v[138:141], v[218:221], v[74:77]
	v_mfma_i32_16x16x64_i8 v[82:85], v[130:133], v[218:221], v[82:85]
	s_nop 0
	v_mfma_i32_16x16x64_i8 v[126:129], v[134:137], v[198:201], v[126:129]
	v_mfma_i32_16x16x64_i8 v[122:125], v[142:145], v[198:201], v[122:125]
	v_mfma_i32_16x16x64_i8 v[106:109], v[142:145], v[206:209], v[106:109]
	v_mfma_i32_16x16x64_i8 v[114:117], v[134:137], v[206:209], v[114:117]
	v_mfma_i32_16x16x64_i8 v[98:101], v[134:137], v[214:217], v[98:101]
	v_mfma_i32_16x16x64_i8 v[90:93], v[142:145], v[214:217], v[90:93]
	v_mfma_i32_16x16x64_i8 v[74:77], v[142:145], v[222:225], v[74:77]
	v_mfma_i32_16x16x64_i8 v[82:85], v[134:137], v[222:225], v[82:85]
	s_setprio 0
	s_setprio 1
	v_mfma_i32_16x16x64_i8 v[118:121], v[146:149], v[194:197], v[118:121]
	v_mfma_i32_16x16x64_i8 v[110:113], v[154:157], v[194:197], v[110:113]
	v_mfma_i32_16x16x64_i8 v[94:97], v[154:157], v[202:205], v[94:97]
	v_mfma_i32_16x16x64_i8 v[102:105], v[146:149], v[202:205], v[102:105]
	v_mfma_i32_16x16x64_i8 v[86:89], v[146:149], v[210:213], v[86:89]
	v_mfma_i32_16x16x64_i8 v[78:81], v[154:157], v[210:213], v[78:81]
	v_mfma_i32_16x16x64_i8 v[66:69], v[154:157], v[218:221], v[66:69]
	v_mfma_i32_16x16x64_i8 v[70:73], v[146:149], v[218:221], v[70:73]
	s_nop 0
	v_mfma_i32_16x16x64_i8 v[118:121], v[150:153], v[198:201], v[118:121]
	v_mfma_i32_16x16x64_i8 v[110:113], v[158:161], v[198:201], v[110:113]
	v_mfma_i32_16x16x64_i8 v[94:97], v[158:161], v[206:209], v[94:97]
	v_mfma_i32_16x16x64_i8 v[102:105], v[150:153], v[206:209], v[102:105]
	v_mfma_i32_16x16x64_i8 v[86:89], v[150:153], v[214:217], v[86:89]
	v_mfma_i32_16x16x64_i8 v[78:81], v[158:161], v[214:217], v[78:81]
	v_mfma_i32_16x16x64_i8 v[66:69], v[158:161], v[222:225], v[66:69]
	v_mfma_i32_16x16x64_i8 v[70:73], v[150:153], v[222:225], v[70:73]
	s_setprio 0
	s_barrier
	s_add_i32 s0, s66, s40
	s_mov_b32 m0, s0
	s_add_u32 s98, s36, 0x80
	s_addc_u32 s99, s37, 0
	s_add_u32 s100, s38, 0x80
	s_addc_u32 s101, s39, 0
	ds_read_b128 v[194:197], v193 offset:49152
	ds_read_b128 v[198:201], v193 offset:50176
	ds_read_b128 v[202:205], v193 offset:51200
	ds_read_b128 v[206:209], v193 offset:52224
	ds_read_b128 v[210:213], v193 offset:53248
	ds_read_b128 v[214:217], v193 offset:54272
	ds_read_b128 v[218:221], v193 offset:55296
	ds_read_b128 v[222:225], v193 offset:56320
	global_load_lds_dwordx4 v164, s[98:99]
	s_add_i32 m0, s0, 0x2000
	s_add_u32 s0, s36, 0x80080
	s_addc_u32 s1, s37, 0
	s_add_i32 s36, s67, s40
	global_load_lds_dwordx4 v168, s[98:99]
	s_mov_b32 m0, s36
	s_nop 0
	global_load_lds_dwordx4 v164, s[0:1]
	s_add_i32 m0, s36, 0x2000
	s_nop 0
	global_load_lds_dwordx4 v168, s[0:1]
	s_mov_b32 m0, s48
	s_nop 0
	global_load_lds_dwordx4 v162, s[100:101]
	s_mov_b32 m0, s49
	s_nop 0
	global_load_lds_dwordx4 v166, s[100:101]
	s_waitcnt vmcnt(8)
	s_waitcnt lgkmcnt(0)
	s_barrier
	s_setprio 1
	s_waitcnt lgkmcnt(0)
	v_mfma_i32_16x16x64_i8 v[62:65], v[130:133], v[194:197], v[62:65]
	v_mfma_i32_16x16x64_i8 v[58:61], v[138:141], v[194:197], v[58:61]
	v_mfma_i32_16x16x64_i8 v[42:45], v[138:141], v[202:205], v[42:45]
	v_mfma_i32_16x16x64_i8 v[50:53], v[130:133], v[202:205], v[50:53]
	v_mfma_i32_16x16x64_i8 v[34:37], v[130:133], v[210:213], v[34:37]
	v_mfma_i32_16x16x64_i8 v[26:29], v[138:141], v[210:213], v[26:29]
	v_mfma_i32_16x16x64_i8 v[10:13], v[138:141], v[218:221], v[10:13]
	v_mfma_i32_16x16x64_i8 v[18:21], v[130:133], v[218:221], v[18:21]
	s_nop 0
	v_mfma_i32_16x16x64_i8 v[62:65], v[134:137], v[198:201], v[62:65]
	v_mfma_i32_16x16x64_i8 v[58:61], v[142:145], v[198:201], v[58:61]
	v_mfma_i32_16x16x64_i8 v[42:45], v[142:145], v[206:209], v[42:45]
	v_mfma_i32_16x16x64_i8 v[50:53], v[134:137], v[206:209], v[50:53]
	v_mfma_i32_16x16x64_i8 v[34:37], v[134:137], v[214:217], v[34:37]
	v_mfma_i32_16x16x64_i8 v[26:29], v[142:145], v[214:217], v[26:29]
	v_mfma_i32_16x16x64_i8 v[10:13], v[142:145], v[222:225], v[10:13]
	v_mfma_i32_16x16x64_i8 v[18:21], v[134:137], v[222:225], v[18:21]
	s_setprio 0
	s_setprio 1
	v_mfma_i32_16x16x64_i8 v[54:57], v[146:149], v[194:197], v[54:57]
	v_mfma_i32_16x16x64_i8 v[46:49], v[154:157], v[194:197], v[46:49]
	v_mfma_i32_16x16x64_i8 v[30:33], v[154:157], v[202:205], v[30:33]
	v_mfma_i32_16x16x64_i8 v[38:41], v[146:149], v[202:205], v[38:41]
	v_mfma_i32_16x16x64_i8 v[22:25], v[146:149], v[210:213], v[22:25]
	v_mfma_i32_16x16x64_i8 v[14:17], v[154:157], v[210:213], v[14:17]
	v_mfma_i32_16x16x64_i8 v[2:5], v[154:157], v[218:221], v[2:5]
	v_mfma_i32_16x16x64_i8 v[6:9], v[146:149], v[218:221], v[6:9]
	s_nop 0
	v_mfma_i32_16x16x64_i8 v[54:57], v[150:153], v[198:201], v[54:57]
	v_mfma_i32_16x16x64_i8 v[46:49], v[158:161], v[198:201], v[46:49]
	v_mfma_i32_16x16x64_i8 v[30:33], v[158:161], v[206:209], v[30:33]
	v_mfma_i32_16x16x64_i8 v[38:41], v[150:153], v[206:209], v[38:41]
	v_mfma_i32_16x16x64_i8 v[22:25], v[150:153], v[214:217], v[22:25]
	v_mfma_i32_16x16x64_i8 v[14:17], v[158:161], v[214:217], v[14:17]
	v_mfma_i32_16x16x64_i8 v[2:5], v[158:161], v[222:225], v[2:5]
	v_mfma_i32_16x16x64_i8 v[6:9], v[150:153], v[222:225], v[6:9]
	s_setprio 0
	s_barrier
	s_add_i32 s64, s64, 2
	s_add_u32 s34, s34, 0x100
	s_addc_u32 s35, s35, 0
	s_add_u32 s62, s62, 0x100
	s_addc_u32 s63, s63, 0
	s_cmp_gt_u32 s64, 29
	s_cbranch_scc1 .LBB0_791

.LBB0_1051:
	s_add_u32 s8, s17, s6
	s_addc_u32 s9, s48, s7
	s_add_u32 s8, s8, 0x32800100
	s_addc_u32 s9, s9, 0
	s_add_u32 s65, s49, s6
	s_addc_u32 s68, s50, s7
	s_add_i32 s69, 0, 0x10000
	s_cmpk_eq_i32 s6, 0xf00
	s_cselect_b32 s41, s5, s9
	s_cselect_b32 s40, s4, s8
	s_cselect_b32 s9, s21, s68
	s_cselect_b32 s8, s20, s65
	s_add_i32 s65, 0, 0x14000
	v_add_u32_e32 v130, s69, v187
	v_add_u32_e32 v134, s65, v187
	ds_read_b128 v[158:161], v130
	ds_read_b128 v[150:153], v130 offset:1024
	ds_read_b128 v[154:157], v130 offset:2048
	ds_read_b128 v[146:149], v130 offset:3072
	ds_read_b128 v[142:145], v134
	ds_read_b128 v[130:133], v134 offset:1024
	ds_read_b128 v[138:141], v134 offset:2048
	ds_read_b128 v[134:137], v134 offset:3072
	v_lshl_add_u64 v[214:215], v[168:169], 0, s[6:7]
	s_add_i32 m0, s43, 0xc000
	ds_read_b128 v[172:175], v188
	ds_read_b128 v[176:179], v188 offset:1024
	ds_read_b128 v[190:193], v188 offset:2048
	ds_read_b128 v[194:197], v188 offset:3072
	ds_read_b128 v[198:201], v188 offset:4096
	ds_read_b128 v[202:205], v188 offset:5120
	ds_read_b128 v[206:209], v188 offset:6144
	ds_read_b128 v[210:213], v188 offset:7168
	global_load_lds_dwordx4 v[214:215], off
	v_lshl_add_u64 v[214:215], v[170:171], 0, s[6:7]
	s_add_i32 m0, s43, 0xe000
	s_nop 0
	global_load_lds_dwordx4 v[214:215], off
	s_waitcnt vmcnt(8)
	s_waitcnt lgkmcnt(0)
	s_barrier
	s_setprio 1
	s_waitcnt lgkmcnt(0)
	v_mfma_i32_16x16x64_i8 v[70:73], v[158:161], v[172:175], v[70:73]
	v_mfma_i32_16x16x64_i8 v[34:37], v[154:157], v[172:175], v[34:37]
	v_mfma_i32_16x16x64_i8 v[54:57], v[154:157], v[190:193], v[54:57]
	v_mfma_i32_16x16x64_i8 v[102:105], v[158:161], v[190:193], v[102:105]
	v_mfma_i32_16x16x64_i8 v[114:117], v[158:161], v[198:201], v[114:117]
	v_mfma_i32_16x16x64_i8 v[86:89], v[154:157], v[198:201], v[86:89]
	v_mfma_i32_16x16x64_i8 v[110:113], v[154:157], v[206:209], v[110:113]
	v_mfma_i32_16x16x64_i8 v[126:129], v[158:161], v[206:209], v[126:129]
	s_nop 0
	v_mfma_i32_16x16x64_i8 v[70:73], v[150:153], v[176:179], v[70:73]
	v_mfma_i32_16x16x64_i8 v[34:37], v[146:149], v[176:179], v[34:37]
	v_mfma_i32_16x16x64_i8 v[54:57], v[146:149], v[194:197], v[54:57]
	v_mfma_i32_16x16x64_i8 v[102:105], v[150:153], v[194:197], v[102:105]
	v_mfma_i32_16x16x64_i8 v[114:117], v[150:153], v[202:205], v[114:117]
	v_mfma_i32_16x16x64_i8 v[86:89], v[146:149], v[202:205], v[86:89]
	v_mfma_i32_16x16x64_i8 v[110:113], v[146:149], v[210:213], v[110:113]
	v_mfma_i32_16x16x64_i8 v[126:129], v[150:153], v[210:213], v[126:129]
	s_setprio 0
	s_setprio 1
	v_mfma_i32_16x16x64_i8 v[18:21], v[142:145], v[172:175], v[18:21]
	v_mfma_i32_16x16x64_i8 v[2:5], v[138:141], v[172:175], v[2:5]
	v_mfma_i32_16x16x64_i8 v[6:9], v[138:141], v[190:193], v[6:9]
	v_mfma_i32_16x16x64_i8 v[38:41], v[142:145], v[190:193], v[38:41]
	v_mfma_i32_16x16x64_i8 v[66:69], v[142:145], v[198:201], v[66:69]
	v_mfma_i32_16x16x64_i8 v[26:29], v[138:141], v[198:201], v[26:29]
	v_mfma_i32_16x16x64_i8 v[50:53], v[138:141], v[206:209], v[50:53]
	v_mfma_i32_16x16x64_i8 v[90:93], v[142:145], v[206:209], v[90:93]
	s_nop 0
	v_mfma_i32_16x16x64_i8 v[18:21], v[130:133], v[176:179], v[18:21]
	v_mfma_i32_16x16x64_i8 v[2:5], v[134:137], v[176:179], v[2:5]
	v_mfma_i32_16x16x64_i8 v[6:9], v[134:137], v[194:197], v[6:9]
	v_mfma_i32_16x16x64_i8 v[38:41], v[130:133], v[194:197], v[38:41]
	v_mfma_i32_16x16x64_i8 v[66:69], v[130:133], v[202:205], v[66:69]
	v_mfma_i32_16x16x64_i8 v[26:29], v[134:137], v[202:205], v[26:29]
	v_mfma_i32_16x16x64_i8 v[50:53], v[134:137], v[210:213], v[50:53]
	v_mfma_i32_16x16x64_i8 v[90:93], v[130:133], v[210:213], v[90:93]
	s_setprio 0
	s_barrier
	s_add_i32 s68, s69, s42
	s_mov_b32 m0, s68
	ds_read_b128 v[190:193], v188 offset:16384
	ds_read_b128 v[194:197], v188 offset:17408
	ds_read_b128 v[198:201], v188 offset:18432
	ds_read_b128 v[202:205], v188 offset:19456
	ds_read_b128 v[206:209], v188 offset:20480
	ds_read_b128 v[210:213], v188 offset:21504
	ds_read_b128 v[214:217], v188 offset:22528
	ds_read_b128 v[218:221], v188 offset:23552
	global_load_lds_dwordx4 v162, s[8:9]
	s_add_i32 m0, s68, 0x2000
	s_add_u32 s68, s8, 0x80000
	s_addc_u32 s69, s9, 0
	s_add_i32 s65, s65, s42
	global_load_lds_dwordx4 v166, s[8:9]
	s_mov_b32 m0, s65
	s_nop 0
	global_load_lds_dwordx4 v162, s[68:69]
	s_add_i32 m0, s65, 0x2000
	s_nop 0
	global_load_lds_dwordx4 v166, s[68:69]
	s_mov_b32 m0, s43
	s_nop 0
	global_load_lds_dwordx4 v162, s[40:41]
	s_mov_b32 m0, s60
	s_nop 0
	global_load_lds_dwordx4 v166, s[40:41]
	s_waitcnt vmcnt(8)
	s_waitcnt lgkmcnt(0)
	s_barrier
	s_setprio 1
	s_waitcnt lgkmcnt(0)
	v_mfma_i32_16x16x64_i8 v[122:125], v[158:161], v[190:193], v[122:125]
	v_mfma_i32_16x16x64_i8 v[118:121], v[154:157], v[190:193], v[118:121]
	v_mfma_i32_16x16x64_i8 v[94:97], v[154:157], v[198:201], v[94:97]
	v_mfma_i32_16x16x64_i8 v[98:101], v[158:161], v[198:201], v[98:101]
	v_mfma_i32_16x16x64_i8 v[62:65], v[158:161], v[206:209], v[62:65]
	v_mfma_i32_16x16x64_i8 v[58:61], v[154:157], v[206:209], v[58:61]
	v_mfma_i32_16x16x64_i8 v[22:25], v[154:157], v[214:217], v[22:25]
	v_mfma_i32_16x16x64_i8 v[30:33], v[158:161], v[214:217], v[30:33]
	s_nop 0
	v_mfma_i32_16x16x64_i8 v[122:125], v[150:153], v[194:197], v[122:125]
	v_mfma_i32_16x16x64_i8 v[118:121], v[146:149], v[194:197], v[118:121]
	v_mfma_i32_16x16x64_i8 v[94:97], v[146:149], v[202:205], v[94:97]
	v_mfma_i32_16x16x64_i8 v[98:101], v[150:153], v[202:205], v[98:101]
	v_mfma_i32_16x16x64_i8 v[62:65], v[150:153], v[210:213], v[62:65]
	v_mfma_i32_16x16x64_i8 v[58:61], v[146:149], v[210:213], v[58:61]
	v_mfma_i32_16x16x64_i8 v[22:25], v[146:149], v[218:221], v[22:25]
	v_mfma_i32_16x16x64_i8 v[30:33], v[150:153], v[218:221], v[30:33]
	s_setprio 0
	s_setprio 1
	v_mfma_i32_16x16x64_i8 v[106:109], v[142:145], v[190:193], v[106:109]
	v_mfma_i32_16x16x64_i8 v[82:85], v[138:141], v[190:193], v[82:85]
	v_mfma_i32_16x16x64_i8 v[74:77], v[138:141], v[198:201], v[74:77]
	v_mfma_i32_16x16x64_i8 v[78:81], v[142:145], v[198:201], v[78:81]
	v_mfma_i32_16x16x64_i8 v[46:49], v[142:145], v[206:209], v[46:49]
	v_mfma_i32_16x16x64_i8 v[42:45], v[138:141], v[206:209], v[42:45]
	v_mfma_i32_16x16x64_i8 v[10:13], v[138:141], v[214:217], v[10:13]
	v_mfma_i32_16x16x64_i8 v[14:17], v[142:145], v[214:217], v[14:17]
	s_nop 0
	v_mfma_i32_16x16x64_i8 v[106:109], v[130:133], v[194:197], v[106:109]
	v_mfma_i32_16x16x64_i8 v[82:85], v[134:137], v[194:197], v[82:85]
	v_mfma_i32_16x16x64_i8 v[74:77], v[134:137], v[202:205], v[74:77]
	v_mfma_i32_16x16x64_i8 v[78:81], v[130:133], v[202:205], v[78:81]
	v_mfma_i32_16x16x64_i8 v[46:49], v[130:133], v[210:213], v[46:49]
	v_mfma_i32_16x16x64_i8 v[42:45], v[134:137], v[210:213], v[42:45]
	v_mfma_i32_16x16x64_i8 v[10:13], v[134:137], v[218:221], v[10:13]
	v_mfma_i32_16x16x64_i8 v[14:17], v[130:133], v[218:221], v[14:17]
	s_setprio 0
	s_barrier
	s_add_i32 s65, 0, 0x18000
	s_add_i32 s68, 0, 0x1c000
	v_add_u32_e32 v142, s65, v187
	v_add_u32_e32 v158, s68, v187
	ds_read_b128 v[130:133], v142
	ds_read_b128 v[134:137], v142 offset:1024
	ds_read_b128 v[138:141], v142 offset:2048
	ds_read_b128 v[142:145], v142 offset:3072
	ds_read_b128 v[146:149], v158
	ds_read_b128 v[150:153], v158 offset:1024
	ds_read_b128 v[154:157], v158 offset:2048
	ds_read_b128 v[158:161], v158 offset:3072
	s_add_u32 s40, s40, 0x80000
	s_addc_u32 s41, s41, 0
	s_add_u32 s100, s40, 0xfff80080
	s_addc_u32 s101, s41, -1
	s_mov_b32 m0, s61
	ds_read_b128 v[190:193], v188 offset:32768
	ds_read_b128 v[194:197], v188 offset:33792
	ds_read_b128 v[198:201], v188 offset:34816
	ds_read_b128 v[202:205], v188 offset:35840
	ds_read_b128 v[206:209], v188 offset:36864
	ds_read_b128 v[210:213], v188 offset:37888
	ds_read_b128 v[214:217], v188 offset:38912
	ds_read_b128 v[218:221], v188 offset:39936
	global_load_lds_dwordx4 v162, s[40:41]
	s_mov_b32 m0, s62
	s_nop 0
	global_load_lds_dwordx4 v166, s[40:41]
	s_waitcnt vmcnt(8)
	s_waitcnt lgkmcnt(0)
	s_barrier
	s_setprio 1
	s_waitcnt lgkmcnt(0)
	v_mfma_i32_16x16x64_i8 v[70:73], v[130:133], v[190:193], v[70:73]
	v_mfma_i32_16x16x64_i8 v[34:37], v[138:141], v[190:193], v[34:37]
	v_mfma_i32_16x16x64_i8 v[54:57], v[138:141], v[198:201], v[54:57]
	v_mfma_i32_16x16x64_i8 v[102:105], v[130:133], v[198:201], v[102:105]
	v_mfma_i32_16x16x64_i8 v[114:117], v[130:133], v[206:209], v[114:117]
	v_mfma_i32_16x16x64_i8 v[86:89], v[138:141], v[206:209], v[86:89]
	v_mfma_i32_16x16x64_i8 v[110:113], v[138:141], v[214:217], v[110:113]
	v_mfma_i32_16x16x64_i8 v[126:129], v[130:133], v[214:217], v[126:129]
	s_nop 0
	v_mfma_i32_16x16x64_i8 v[70:73], v[134:137], v[194:197], v[70:73]
	v_mfma_i32_16x16x64_i8 v[34:37], v[142:145], v[194:197], v[34:37]
	v_mfma_i32_16x16x64_i8 v[54:57], v[142:145], v[202:205], v[54:57]
	v_mfma_i32_16x16x64_i8 v[102:105], v[134:137], v[202:205], v[102:105]
	v_mfma_i32_16x16x64_i8 v[114:117], v[134:137], v[210:213], v[114:117]
	v_mfma_i32_16x16x64_i8 v[86:89], v[142:145], v[210:213], v[86:89]
	v_mfma_i32_16x16x64_i8 v[110:113], v[142:145], v[218:221], v[110:113]
	v_mfma_i32_16x16x64_i8 v[126:129], v[134:137], v[218:221], v[126:129]
	s_setprio 0
	s_setprio 1
	v_mfma_i32_16x16x64_i8 v[18:21], v[146:149], v[190:193], v[18:21]
	v_mfma_i32_16x16x64_i8 v[2:5], v[154:157], v[190:193], v[2:5]
	v_mfma_i32_16x16x64_i8 v[6:9], v[154:157], v[198:201], v[6:9]
	v_mfma_i32_16x16x64_i8 v[38:41], v[146:149], v[198:201], v[38:41]
	v_mfma_i32_16x16x64_i8 v[66:69], v[146:149], v[206:209], v[66:69]
	v_mfma_i32_16x16x64_i8 v[26:29], v[154:157], v[206:209], v[26:29]
	v_mfma_i32_16x16x64_i8 v[50:53], v[154:157], v[214:217], v[50:53]
	v_mfma_i32_16x16x64_i8 v[90:93], v[146:149], v[214:217], v[90:93]
	s_nop 0
	v_mfma_i32_16x16x64_i8 v[18:21], v[150:153], v[194:197], v[18:21]
	v_mfma_i32_16x16x64_i8 v[2:5], v[158:161], v[194:197], v[2:5]
	v_mfma_i32_16x16x64_i8 v[6:9], v[158:161], v[202:205], v[6:9]
	v_mfma_i32_16x16x64_i8 v[38:41], v[150:153], v[202:205], v[38:41]
	v_mfma_i32_16x16x64_i8 v[66:69], v[150:153], v[210:213], v[66:69]
	v_mfma_i32_16x16x64_i8 v[26:29], v[158:161], v[210:213], v[26:29]
	v_mfma_i32_16x16x64_i8 v[50:53], v[158:161], v[218:221], v[50:53]
	v_mfma_i32_16x16x64_i8 v[90:93], v[150:153], v[218:221], v[90:93]
	s_setprio 0
	s_barrier
	s_add_i32 s40, s65, s42
	s_mov_b32 m0, s40
	s_add_u32 s98, s8, 0x80
	s_addc_u32 s99, s9, 0
	ds_read_b128 v[190:193], v188 offset:49152
	ds_read_b128 v[194:197], v188 offset:50176
	ds_read_b128 v[198:201], v188 offset:51200
	ds_read_b128 v[202:205], v188 offset:52224
	ds_read_b128 v[206:209], v188 offset:53248
	ds_read_b128 v[210:213], v188 offset:54272
	ds_read_b128 v[214:217], v188 offset:55296
	ds_read_b128 v[218:221], v188 offset:56320
	global_load_lds_dwordx4 v162, s[98:99]
	s_add_i32 m0, s40, 0x2000
	s_add_u32 s8, s8, 0x80080
	s_addc_u32 s9, s9, 0
	s_add_i32 s40, s68, s42
	global_load_lds_dwordx4 v166, s[98:99]
	s_mov_b32 m0, s40
	s_nop 0
	global_load_lds_dwordx4 v162, s[8:9]
	s_add_i32 m0, s40, 0x2000
	s_nop 0
	global_load_lds_dwordx4 v166, s[8:9]
	s_mov_b32 m0, s66
	s_nop 0
	global_load_lds_dwordx4 v162, s[100:101]
	s_mov_b32 m0, s67
	s_nop 0
	global_load_lds_dwordx4 v166, s[100:101]
	s_waitcnt vmcnt(8)
	s_waitcnt lgkmcnt(0)
	s_barrier
	s_setprio 1
	s_waitcnt lgkmcnt(0)
	v_mfma_i32_16x16x64_i8 v[122:125], v[130:133], v[190:193], v[122:125]
	v_mfma_i32_16x16x64_i8 v[118:121], v[138:141], v[190:193], v[118:121]
	v_mfma_i32_16x16x64_i8 v[94:97], v[138:141], v[198:201], v[94:97]
	v_mfma_i32_16x16x64_i8 v[98:101], v[130:133], v[198:201], v[98:101]
	v_mfma_i32_16x16x64_i8 v[62:65], v[130:133], v[206:209], v[62:65]
	v_mfma_i32_16x16x64_i8 v[58:61], v[138:141], v[206:209], v[58:61]
	v_mfma_i32_16x16x64_i8 v[22:25], v[138:141], v[214:217], v[22:25]
	v_mfma_i32_16x16x64_i8 v[30:33], v[130:133], v[214:217], v[30:33]
	s_nop 0
	v_mfma_i32_16x16x64_i8 v[122:125], v[134:137], v[194:197], v[122:125]
	v_mfma_i32_16x16x64_i8 v[118:121], v[142:145], v[194:197], v[118:121]
	v_mfma_i32_16x16x64_i8 v[94:97], v[142:145], v[202:205], v[94:97]
	v_mfma_i32_16x16x64_i8 v[98:101], v[134:137], v[202:205], v[98:101]
	v_mfma_i32_16x16x64_i8 v[62:65], v[134:137], v[210:213], v[62:65]
	v_mfma_i32_16x16x64_i8 v[58:61], v[142:145], v[210:213], v[58:61]
	v_mfma_i32_16x16x64_i8 v[22:25], v[142:145], v[218:221], v[22:25]
	v_mfma_i32_16x16x64_i8 v[30:33], v[134:137], v[218:221], v[30:33]
	s_setprio 0
	s_setprio 1
	v_mfma_i32_16x16x64_i8 v[106:109], v[146:149], v[190:193], v[106:109]
	v_mfma_i32_16x16x64_i8 v[82:85], v[154:157], v[190:193], v[82:85]
	v_mfma_i32_16x16x64_i8 v[74:77], v[154:157], v[198:201], v[74:77]
	v_mfma_i32_16x16x64_i8 v[78:81], v[146:149], v[198:201], v[78:81]
	v_mfma_i32_16x16x64_i8 v[46:49], v[146:149], v[206:209], v[46:49]
	v_mfma_i32_16x16x64_i8 v[42:45], v[154:157], v[206:209], v[42:45]
	v_mfma_i32_16x16x64_i8 v[10:13], v[154:157], v[214:217], v[10:13]
	v_mfma_i32_16x16x64_i8 v[14:17], v[146:149], v[214:217], v[14:17]
	s_nop 0
	v_mfma_i32_16x16x64_i8 v[106:109], v[150:153], v[194:197], v[106:109]
	v_mfma_i32_16x16x64_i8 v[82:85], v[158:161], v[194:197], v[82:85]
	v_mfma_i32_16x16x64_i8 v[74:77], v[158:161], v[202:205], v[74:77]
	v_mfma_i32_16x16x64_i8 v[78:81], v[150:153], v[202:205], v[78:81]
	v_mfma_i32_16x16x64_i8 v[46:49], v[150:153], v[210:213], v[46:49]
	v_mfma_i32_16x16x64_i8 v[42:45], v[158:161], v[210:213], v[42:45]
	v_mfma_i32_16x16x64_i8 v[10:13], v[158:161], v[218:221], v[10:13]
	v_mfma_i32_16x16x64_i8 v[14:17], v[150:153], v[218:221], v[14:17]
	s_setprio 0
	s_barrier
	s_add_i32 s64, s64, 2
	s_add_u32 s6, s6, 0x100
	s_addc_u32 s7, s7, 0
	s_cmp_gt_u32 s64, 29
	s_cbranch_scc0 .LBB0_1051
	s_waitcnt vmcnt(0)
	s_cmpk_lt_u32 s59, 0x100
	s_cbranch_scc0 .LBB0_1054
	s_barrier

.LBB0_1173:
	ds_read_b128 v[158:161], v184
	ds_read_b128 v[150:153], v184 offset:1024
	ds_read_b128 v[154:157], v184 offset:2048
	ds_read_b128 v[146:149], v184 offset:3072
	ds_read_b128 v[142:145], v185
	ds_read_b128 v[130:133], v185 offset:1024
	ds_read_b128 v[138:141], v185 offset:2048
	ds_read_b128 v[134:137], v185 offset:3072
	s_add_u32 s38, s36, 0xfff80080
	s_addc_u32 s39, s37, -1
	s_cmp_eq_u32 s65, 28
	s_cselect_b32 s41, s18, s39
	s_cselect_b32 s40, s19, s38
	s_cselect_b32 s39, s25, s64
	s_cselect_b32 s38, s27, s63
	v_lshl_add_u64 v[212:213], s[36:37], 0, v[166:167]
	s_add_i32 m0, s35, 0xc000
	ds_read_b128 v[174:177], v186
	ds_read_b128 v[178:181], v186 offset:1024
	ds_read_b128 v[188:191], v186 offset:2048
	ds_read_b128 v[192:195], v186 offset:3072
	ds_read_b128 v[196:199], v186 offset:4096
	ds_read_b128 v[200:203], v186 offset:5120
	ds_read_b128 v[204:207], v186 offset:6144
	ds_read_b128 v[208:211], v186 offset:7168
	global_load_lds_dwordx4 v[212:213], off
	v_lshl_add_u64 v[212:213], s[36:37], 0, v[168:169]
	s_add_i32 m0, s35, 0xe000
	s_nop 0
	global_load_lds_dwordx4 v[212:213], off
	s_waitcnt vmcnt(8)
	s_waitcnt lgkmcnt(0)
	s_barrier
	s_setprio 1
	s_waitcnt lgkmcnt(0)
	v_mfma_i32_16x16x64_i8 v[126:129], v[158:161], v[174:177], v[126:129]
	v_mfma_i32_16x16x64_i8 v[122:125], v[154:157], v[174:177], v[122:125]
	v_mfma_i32_16x16x64_i8 v[106:109], v[154:157], v[188:191], v[106:109]
	v_mfma_i32_16x16x64_i8 v[110:113], v[158:161], v[188:191], v[110:113]
	v_mfma_i32_16x16x64_i8 v[94:97], v[158:161], v[196:199], v[94:97]
	v_mfma_i32_16x16x64_i8 v[90:93], v[154:157], v[196:199], v[90:93]
	v_mfma_i32_16x16x64_i8 v[74:77], v[154:157], v[204:207], v[74:77]
	v_mfma_i32_16x16x64_i8 v[78:81], v[158:161], v[204:207], v[78:81]
	s_nop 0
	v_mfma_i32_16x16x64_i8 v[126:129], v[150:153], v[178:181], v[126:129]
	v_mfma_i32_16x16x64_i8 v[122:125], v[146:149], v[178:181], v[122:125]
	v_mfma_i32_16x16x64_i8 v[106:109], v[146:149], v[192:195], v[106:109]
	v_mfma_i32_16x16x64_i8 v[110:113], v[150:153], v[192:195], v[110:113]
	v_mfma_i32_16x16x64_i8 v[94:97], v[150:153], v[200:203], v[94:97]
	v_mfma_i32_16x16x64_i8 v[90:93], v[146:149], v[200:203], v[90:93]
	v_mfma_i32_16x16x64_i8 v[74:77], v[146:149], v[208:211], v[74:77]
	v_mfma_i32_16x16x64_i8 v[78:81], v[150:153], v[208:211], v[78:81]
	s_setprio 0
	s_setprio 1
	v_mfma_i32_16x16x64_i8 v[118:121], v[142:145], v[174:177], v[118:121]
	v_mfma_i32_16x16x64_i8 v[114:117], v[138:141], v[174:177], v[114:117]
	v_mfma_i32_16x16x64_i8 v[98:101], v[138:141], v[188:191], v[98:101]
	v_mfma_i32_16x16x64_i8 v[102:105], v[142:145], v[188:191], v[102:105]
	v_mfma_i32_16x16x64_i8 v[86:89], v[142:145], v[196:199], v[86:89]
	v_mfma_i32_16x16x64_i8 v[82:85], v[138:141], v[196:199], v[82:85]
	v_mfma_i32_16x16x64_i8 v[66:69], v[138:141], v[204:207], v[66:69]
	v_mfma_i32_16x16x64_i8 v[70:73], v[142:145], v[204:207], v[70:73]
	s_nop 0
	v_mfma_i32_16x16x64_i8 v[118:121], v[130:133], v[178:181], v[118:121]
	v_mfma_i32_16x16x64_i8 v[114:117], v[134:137], v[178:181], v[114:117]
	v_mfma_i32_16x16x64_i8 v[98:101], v[134:137], v[192:195], v[98:101]
	v_mfma_i32_16x16x64_i8 v[102:105], v[130:133], v[192:195], v[102:105]
	v_mfma_i32_16x16x64_i8 v[86:89], v[130:133], v[200:203], v[86:89]
	v_mfma_i32_16x16x64_i8 v[82:85], v[134:137], v[200:203], v[82:85]
	v_mfma_i32_16x16x64_i8 v[66:69], v[134:137], v[208:211], v[66:69]
	v_mfma_i32_16x16x64_i8 v[70:73], v[130:133], v[208:211], v[70:73]
	s_setprio 0
	s_barrier
	s_add_i32 s66, s51, s3
	v_lshl_add_u64 v[174:175], s[38:39], 0, v[164:165]
	s_mov_b32 m0, s66
	ds_read_b128 v[188:191], v186 offset:16384
	ds_read_b128 v[192:195], v186 offset:17408
	ds_read_b128 v[196:199], v186 offset:18432
	ds_read_b128 v[200:203], v186 offset:19456
	ds_read_b128 v[204:207], v186 offset:20480
	ds_read_b128 v[208:211], v186 offset:21504
	ds_read_b128 v[212:215], v186 offset:22528
	ds_read_b128 v[216:219], v186 offset:23552
	global_load_lds_dwordx4 v[174:175], off
	s_add_i32 m0, s66, 0x2000
	s_add_u32 s66, s38, 0x80000
	v_lshl_add_u64 v[176:177], s[38:39], 0, v[162:163]
	s_addc_u32 s67, s39, 0
	s_add_i32 s68, s58, s3
	global_load_lds_dwordx4 v[176:177], off
	v_lshl_add_u64 v[178:179], s[66:67], 0, v[164:165]
	s_mov_b32 m0, s68
	v_lshl_add_u64 v[180:181], s[40:41], 0, v[162:163]
	global_load_lds_dwordx4 v[178:179], off
	v_lshl_add_u64 v[178:179], s[66:67], 0, v[162:163]
	s_add_i32 m0, s68, 0x2000
	s_nop 0
	global_load_lds_dwordx4 v[178:179], off
	v_lshl_add_u64 v[178:179], s[40:41], 0, v[164:165]
	s_mov_b32 m0, s35
	s_nop 0
	global_load_lds_dwordx4 v[178:179], off
	s_mov_b32 m0, s42
	s_nop 0
	global_load_lds_dwordx4 v[180:181], off
	s_waitcnt vmcnt(8)
	s_waitcnt lgkmcnt(0)
	s_barrier
	s_setprio 1
	s_waitcnt lgkmcnt(0)
	v_mfma_i32_16x16x64_i8 v[62:65], v[158:161], v[188:191], v[62:65]
	v_mfma_i32_16x16x64_i8 v[58:61], v[154:157], v[188:191], v[58:61]
	v_mfma_i32_16x16x64_i8 v[42:45], v[154:157], v[196:199], v[42:45]
	v_mfma_i32_16x16x64_i8 v[46:49], v[158:161], v[196:199], v[46:49]
	v_mfma_i32_16x16x64_i8 v[30:33], v[158:161], v[204:207], v[30:33]
	v_mfma_i32_16x16x64_i8 v[26:29], v[154:157], v[204:207], v[26:29]
	v_mfma_i32_16x16x64_i8 v[10:13], v[154:157], v[212:215], v[10:13]
	v_mfma_i32_16x16x64_i8 v[14:17], v[158:161], v[212:215], v[14:17]
	s_nop 0
	v_mfma_i32_16x16x64_i8 v[62:65], v[150:153], v[192:195], v[62:65]
	v_mfma_i32_16x16x64_i8 v[58:61], v[146:149], v[192:195], v[58:61]
	v_mfma_i32_16x16x64_i8 v[42:45], v[146:149], v[200:203], v[42:45]
	v_mfma_i32_16x16x64_i8 v[46:49], v[150:153], v[200:203], v[46:49]
	v_mfma_i32_16x16x64_i8 v[30:33], v[150:153], v[208:211], v[30:33]
	v_mfma_i32_16x16x64_i8 v[26:29], v[146:149], v[208:211], v[26:29]
	v_mfma_i32_16x16x64_i8 v[10:13], v[146:149], v[216:219], v[10:13]
	v_mfma_i32_16x16x64_i8 v[14:17], v[150:153], v[216:219], v[14:17]
	s_setprio 0
	s_setprio 1
	v_mfma_i32_16x16x64_i8 v[54:57], v[142:145], v[188:191], v[54:57]
	v_mfma_i32_16x16x64_i8 v[50:53], v[138:141], v[188:191], v[50:53]
	v_mfma_i32_16x16x64_i8 v[34:37], v[138:141], v[196:199], v[34:37]
	v_mfma_i32_16x16x64_i8 v[38:41], v[142:145], v[196:199], v[38:41]
	v_mfma_i32_16x16x64_i8 v[22:25], v[142:145], v[204:207], v[22:25]
	v_mfma_i32_16x16x64_i8 v[18:21], v[138:141], v[204:207], v[18:21]
	v_mfma_i32_16x16x64_i8 v[2:5], v[138:141], v[212:215], v[2:5]
	v_mfma_i32_16x16x64_i8 v[6:9], v[142:145], v[212:215], v[6:9]
	s_nop 0
	v_mfma_i32_16x16x64_i8 v[54:57], v[130:133], v[192:195], v[54:57]
	v_mfma_i32_16x16x64_i8 v[50:53], v[134:137], v[192:195], v[50:53]
	v_mfma_i32_16x16x64_i8 v[34:37], v[134:137], v[200:203], v[34:37]
	v_mfma_i32_16x16x64_i8 v[38:41], v[130:133], v[200:203], v[38:41]
	v_mfma_i32_16x16x64_i8 v[22:25], v[130:133], v[208:211], v[22:25]
	v_mfma_i32_16x16x64_i8 v[18:21], v[134:137], v[208:211], v[18:21]
	v_mfma_i32_16x16x64_i8 v[2:5], v[134:137], v[216:219], v[2:5]
	v_mfma_i32_16x16x64_i8 v[6:9], v[130:133], v[216:219], v[6:9]
	s_setprio 0
	s_barrier
	s_add_i32 s66, 0, 0x18000
	s_add_i32 s67, 0, 0x1c000
	v_add_u32_e32 v142, s66, v182
	v_add_u32_e32 v158, s67, v182
	ds_read_b128 v[130:133], v142
	ds_read_b128 v[134:137], v142 offset:1024
	ds_read_b128 v[138:141], v142 offset:2048
	ds_read_b128 v[142:145], v142 offset:3072
	ds_read_b128 v[146:149], v158
	ds_read_b128 v[150:153], v158 offset:1024
	ds_read_b128 v[154:157], v158 offset:2048
	ds_read_b128 v[158:161], v158 offset:3072
	s_add_u32 s40, s40, 0x80000
	s_addc_u32 s41, s41, 0
	s_mov_b32 m0, s43
	v_lshl_add_u64 v[220:221], s[40:41], 0, v[164:165]
	ds_read_b128 v[188:191], v186 offset:32768
	ds_read_b128 v[192:195], v186 offset:33792
	ds_read_b128 v[196:199], v186 offset:34816
	ds_read_b128 v[200:203], v186 offset:35840
	ds_read_b128 v[204:207], v186 offset:36864
	ds_read_b128 v[208:211], v186 offset:37888
	ds_read_b128 v[212:215], v186 offset:38912
	ds_read_b128 v[216:219], v186 offset:39936
	global_load_lds_dwordx4 v[220:221], off
	v_lshl_add_u64 v[220:221], s[40:41], 0, v[162:163]
	s_mov_b32 m0, s44
	s_nop 0
	global_load_lds_dwordx4 v[220:221], off
	s_waitcnt vmcnt(8)
	s_waitcnt lgkmcnt(0)
	s_barrier
	s_setprio 1
	s_waitcnt lgkmcnt(0)
	v_mfma_i32_16x16x64_i8 v[126:129], v[130:133], v[188:191], v[126:129]
	v_mfma_i32_16x16x64_i8 v[122:125], v[138:141], v[188:191], v[122:125]
	v_mfma_i32_16x16x64_i8 v[106:109], v[138:141], v[196:199], v[106:109]
	v_mfma_i32_16x16x64_i8 v[110:113], v[130:133], v[196:199], v[110:113]
	v_mfma_i32_16x16x64_i8 v[94:97], v[130:133], v[204:207], v[94:97]
	v_mfma_i32_16x16x64_i8 v[90:93], v[138:141], v[204:207], v[90:93]
	v_mfma_i32_16x16x64_i8 v[74:77], v[138:141], v[212:215], v[74:77]
	v_mfma_i32_16x16x64_i8 v[78:81], v[130:133], v[212:215], v[78:81]
	s_nop 0
	v_mfma_i32_16x16x64_i8 v[126:129], v[134:137], v[192:195], v[126:129]
	v_mfma_i32_16x16x64_i8 v[122:125], v[142:145], v[192:195], v[122:125]
	v_mfma_i32_16x16x64_i8 v[106:109], v[142:145], v[200:203], v[106:109]
	v_mfma_i32_16x16x64_i8 v[110:113], v[134:137], v[200:203], v[110:113]
	v_mfma_i32_16x16x64_i8 v[94:97], v[134:137], v[208:211], v[94:97]
	v_mfma_i32_16x16x64_i8 v[90:93], v[142:145], v[208:211], v[90:93]
	v_mfma_i32_16x16x64_i8 v[74:77], v[142:145], v[216:219], v[74:77]
	v_mfma_i32_16x16x64_i8 v[78:81], v[134:137], v[216:219], v[78:81]
	s_setprio 0
	s_setprio 1
	v_mfma_i32_16x16x64_i8 v[118:121], v[146:149], v[188:191], v[118:121]
	v_mfma_i32_16x16x64_i8 v[114:117], v[154:157], v[188:191], v[114:117]
	v_mfma_i32_16x16x64_i8 v[98:101], v[154:157], v[196:199], v[98:101]
	v_mfma_i32_16x16x64_i8 v[102:105], v[146:149], v[196:199], v[102:105]
	v_mfma_i32_16x16x64_i8 v[86:89], v[146:149], v[204:207], v[86:89]
	v_mfma_i32_16x16x64_i8 v[82:85], v[154:157], v[204:207], v[82:85]
	v_mfma_i32_16x16x64_i8 v[66:69], v[154:157], v[212:215], v[66:69]
	v_mfma_i32_16x16x64_i8 v[70:73], v[146:149], v[212:215], v[70:73]
	s_nop 0
	v_mfma_i32_16x16x64_i8 v[118:121], v[150:153], v[192:195], v[118:121]
	v_mfma_i32_16x16x64_i8 v[114:117], v[158:161], v[192:195], v[114:117]
	v_mfma_i32_16x16x64_i8 v[98:101], v[158:161], v[200:203], v[98:101]
	v_mfma_i32_16x16x64_i8 v[102:105], v[150:153], v[200:203], v[102:105]
	v_mfma_i32_16x16x64_i8 v[86:89], v[150:153], v[208:211], v[86:89]
	v_mfma_i32_16x16x64_i8 v[82:85], v[158:161], v[208:211], v[82:85]
	v_mfma_i32_16x16x64_i8 v[66:69], v[158:161], v[216:219], v[66:69]
	v_mfma_i32_16x16x64_i8 v[70:73], v[150:153], v[216:219], v[70:73]
	s_setprio 0
	s_barrier
	s_add_i32 s40, s66, s3
	v_lshl_add_u64 v[174:175], v[174:175], 0, s[8:9]
	s_mov_b32 m0, s40
	ds_read_b128 v[188:191], v186 offset:49152
	ds_read_b128 v[192:195], v186 offset:50176
	ds_read_b128 v[196:199], v186 offset:51200
	ds_read_b128 v[200:203], v186 offset:52224
	ds_read_b128 v[204:207], v186 offset:53248
	ds_read_b128 v[208:211], v186 offset:54272
	ds_read_b128 v[212:215], v186 offset:55296
	ds_read_b128 v[216:219], v186 offset:56320
	global_load_lds_dwordx4 v[174:175], off
	s_add_i32 m0, s40, 0x2000
	s_add_u32 s38, s38, 0x80080
	v_lshl_add_u64 v[174:175], v[176:177], 0, s[8:9]
	s_addc_u32 s39, s39, 0
	s_add_i32 s40, s67, s3
	global_load_lds_dwordx4 v[174:175], off
	v_lshl_add_u64 v[174:175], s[38:39], 0, v[164:165]
	s_mov_b32 m0, s40
	s_nop 0
	global_load_lds_dwordx4 v[174:175], off
	v_lshl_add_u64 v[174:175], s[38:39], 0, v[162:163]
	s_add_i32 m0, s40, 0x2000
	s_nop 0
	global_load_lds_dwordx4 v[174:175], off
	v_lshl_add_u64 v[174:175], v[178:179], 0, s[8:9]
	s_mov_b32 m0, s49
	s_nop 0
	global_load_lds_dwordx4 v[174:175], off
	v_lshl_add_u64 v[174:175], v[180:181], 0, s[8:9]
	s_mov_b32 m0, s50
	s_nop 0
	global_load_lds_dwordx4 v[174:175], off
	s_waitcnt vmcnt(8)
	s_waitcnt lgkmcnt(0)
	s_barrier
	s_setprio 1
	s_waitcnt lgkmcnt(0)
	v_mfma_i32_16x16x64_i8 v[62:65], v[130:133], v[188:191], v[62:65]
	v_mfma_i32_16x16x64_i8 v[58:61], v[138:141], v[188:191], v[58:61]
	v_mfma_i32_16x16x64_i8 v[42:45], v[138:141], v[196:199], v[42:45]
	v_mfma_i32_16x16x64_i8 v[46:49], v[130:133], v[196:199], v[46:49]
	v_mfma_i32_16x16x64_i8 v[30:33], v[130:133], v[204:207], v[30:33]
	v_mfma_i32_16x16x64_i8 v[26:29], v[138:141], v[204:207], v[26:29]
	v_mfma_i32_16x16x64_i8 v[10:13], v[138:141], v[212:215], v[10:13]
	v_mfma_i32_16x16x64_i8 v[14:17], v[130:133], v[212:215], v[14:17]
	s_nop 0
	v_mfma_i32_16x16x64_i8 v[62:65], v[134:137], v[192:195], v[62:65]
	v_mfma_i32_16x16x64_i8 v[58:61], v[142:145], v[192:195], v[58:61]
	v_mfma_i32_16x16x64_i8 v[42:45], v[142:145], v[200:203], v[42:45]
	v_mfma_i32_16x16x64_i8 v[46:49], v[134:137], v[200:203], v[46:49]
	v_mfma_i32_16x16x64_i8 v[30:33], v[134:137], v[208:211], v[30:33]
	v_mfma_i32_16x16x64_i8 v[26:29], v[142:145], v[208:211], v[26:29]
	v_mfma_i32_16x16x64_i8 v[10:13], v[142:145], v[216:219], v[10:13]
	v_mfma_i32_16x16x64_i8 v[14:17], v[134:137], v[216:219], v[14:17]
	s_setprio 0
	s_setprio 1
	v_mfma_i32_16x16x64_i8 v[54:57], v[146:149], v[188:191], v[54:57]
	v_mfma_i32_16x16x64_i8 v[50:53], v[154:157], v[188:191], v[50:53]
	v_mfma_i32_16x16x64_i8 v[34:37], v[154:157], v[196:199], v[34:37]
	v_mfma_i32_16x16x64_i8 v[38:41], v[146:149], v[196:199], v[38:41]
	v_mfma_i32_16x16x64_i8 v[22:25], v[146:149], v[204:207], v[22:25]
	v_mfma_i32_16x16x64_i8 v[18:21], v[154:157], v[204:207], v[18:21]
	v_mfma_i32_16x16x64_i8 v[2:5], v[154:157], v[212:215], v[2:5]
	v_mfma_i32_16x16x64_i8 v[6:9], v[146:149], v[212:215], v[6:9]
	s_nop 0
	v_mfma_i32_16x16x64_i8 v[54:57], v[150:153], v[192:195], v[54:57]
	v_mfma_i32_16x16x64_i8 v[50:53], v[158:161], v[192:195], v[50:53]
	v_mfma_i32_16x16x64_i8 v[34:37], v[158:161], v[200:203], v[34:37]
	v_mfma_i32_16x16x64_i8 v[38:41], v[150:153], v[200:203], v[38:41]
	v_mfma_i32_16x16x64_i8 v[22:25], v[150:153], v[208:211], v[22:25]
	v_mfma_i32_16x16x64_i8 v[18:21], v[158:161], v[208:211], v[18:21]
	v_mfma_i32_16x16x64_i8 v[2:5], v[158:161], v[216:219], v[2:5]
	v_mfma_i32_16x16x64_i8 v[6:9], v[150:153], v[216:219], v[6:9]
	s_setprio 0
	s_barrier
	s_add_i32 s65, s65, 2
	s_add_u32 s36, s36, 0x100
	s_addc_u32 s37, s37, 0
	s_add_u32 s63, s63, 0x100
	s_addc_u32 s64, s64, 0
	s_cmp_gt_u32 s65, 29
	s_cbranch_scc0 .LBB0_1173
	s_and_b64 vcc, exec, s[12:13]
	s_cbranch_vccz .LBB0_1176
	s_barrier

.LBB0_1291:
	ds_read_b128 v[26:29], v184
	ds_read_b128 v[30:33], v184 offset:1024
	ds_read_b128 v[18:21], v184 offset:2048
	ds_read_b128 v[22:25], v184 offset:3072
	ds_read_b128 v[10:13], v185
	ds_read_b128 v[14:17], v185 offset:1024
	ds_read_b128 v[2:5], v185 offset:2048
	ds_read_b128 v[6:9], v185 offset:3072
	s_add_u32 s20, s14, s16
	s_addc_u32 s21, s15, s17
	s_add_u32 s20, s20, 0x2a800100
	s_addc_u32 s21, s21, 0
	s_add_u32 s48, s31, s16
	s_addc_u32 s49, s34, s17
	s_cmpk_eq_i32 s16, 0x700
	s_cselect_b32 s23, s9, s21
	s_cselect_b32 s22, s8, s20
	s_cselect_b32 s21, s5, s49
	s_cselect_b32 s20, s4, s48
	s_mov_b32 m0, s36
	v_lshl_add_u64 v[214:215], v[170:171], 0, s[16:17]
	ds_read_b128 v[174:177], v186
	ds_read_b128 v[178:181], v186 offset:1024
	ds_read_b128 v[190:193], v186 offset:2048
	ds_read_b128 v[194:197], v186 offset:3072
	ds_read_b128 v[198:201], v186 offset:4096
	ds_read_b128 v[202:205], v186 offset:5120
	ds_read_b128 v[206:209], v186 offset:6144
	ds_read_b128 v[210:213], v186 offset:7168
	global_load_lds_dwordx4 v[214:215], off
	v_lshl_add_u64 v[214:215], v[172:173], 0, s[16:17]
	s_mov_b32 m0, s37
	s_nop 0
	global_load_lds_dwordx4 v[214:215], off
	s_waitcnt vmcnt(8)
	s_waitcnt lgkmcnt(0)
	s_barrier
	s_setprio 1
	s_waitcnt lgkmcnt(0)
	v_mfma_scale_f32_16x16x128_f8f6f4 v[158:161], v[26:33], v[174:181], v[158:161], v1, v1 op_sel_hi:[0,0,0]
	v_mfma_scale_f32_16x16x128_f8f6f4 v[154:157], v[18:25], v[174:181], v[154:157], v1, v1 op_sel_hi:[0,0,0]
	v_mfma_scale_f32_16x16x128_f8f6f4 v[138:141], v[18:25], v[190:197], v[138:141], v1, v1 op_sel_hi:[0,0,0]
	v_mfma_scale_f32_16x16x128_f8f6f4 v[146:149], v[26:33], v[190:197], v[146:149], v1, v1 op_sel_hi:[0,0,0]
	v_mfma_scale_f32_16x16x128_f8f6f4 v[130:133], v[26:33], v[198:205], v[130:133], v1, v1 op_sel_hi:[0,0,0]
	v_mfma_scale_f32_16x16x128_f8f6f4 v[122:125], v[18:25], v[198:205], v[122:125], v1, v1 op_sel_hi:[0,0,0]
	v_mfma_scale_f32_16x16x128_f8f6f4 v[106:109], v[18:25], v[206:213], v[106:109], v1, v1 op_sel_hi:[0,0,0]
	v_mfma_scale_f32_16x16x128_f8f6f4 v[114:117], v[26:33], v[206:213], v[114:117], v1, v1 op_sel_hi:[0,0,0]
	s_setprio 0
	s_setprio 1
	v_mfma_scale_f32_16x16x128_f8f6f4 v[150:153], v[10:17], v[174:181], v[150:153], v1, v1 op_sel_hi:[0,0,0]
	v_mfma_scale_f32_16x16x128_f8f6f4 v[142:145], v[2:9], v[174:181], v[142:145], v1, v1 op_sel_hi:[0,0,0]
	v_mfma_scale_f32_16x16x128_f8f6f4 v[126:129], v[2:9], v[190:197], v[126:129], v1, v1 op_sel_hi:[0,0,0]
	v_mfma_scale_f32_16x16x128_f8f6f4 v[134:137], v[10:17], v[190:197], v[134:137], v1, v1 op_sel_hi:[0,0,0]
	v_mfma_scale_f32_16x16x128_f8f6f4 v[118:121], v[10:17], v[198:205], v[118:121], v1, v1 op_sel_hi:[0,0,0]
	v_mfma_scale_f32_16x16x128_f8f6f4 v[110:113], v[2:9], v[198:205], v[110:113], v1, v1 op_sel_hi:[0,0,0]
	v_mfma_scale_f32_16x16x128_f8f6f4 v[98:101], v[2:9], v[206:213], v[98:101], v1, v1 op_sel_hi:[0,0,0]
	v_mfma_scale_f32_16x16x128_f8f6f4 v[102:105], v[10:17], v[206:213], v[102:105], v1, v1 op_sel_hi:[0,0,0]
	s_setprio 0
	s_barrier
	s_mov_b32 m0, s38
	v_lshl_add_u64 v[174:175], s[20:21], 0, v[164:165]
	s_add_u32 s48, s20, 0x80000
	ds_read_b128 v[190:193], v186 offset:16384
	ds_read_b128 v[194:197], v186 offset:17408
	ds_read_b128 v[198:201], v186 offset:18432
	ds_read_b128 v[202:205], v186 offset:19456
	ds_read_b128 v[206:209], v186 offset:20480
	ds_read_b128 v[210:213], v186 offset:21504
	ds_read_b128 v[214:217], v186 offset:22528
	ds_read_b128 v[218:221], v186 offset:23552
	global_load_lds_dwordx4 v[174:175], off
	v_lshl_add_u64 v[176:177], s[20:21], 0, v[168:169]
	s_mov_b32 m0, s39
	s_addc_u32 s49, s21, 0
	global_load_lds_dwordx4 v[176:177], off
	v_lshl_add_u64 v[178:179], s[48:49], 0, v[164:165]
	s_mov_b32 m0, s40
	v_lshl_add_u64 v[180:181], s[22:23], 0, v[166:167]
	global_load_lds_dwordx4 v[178:179], off
	v_lshl_add_u64 v[178:179], s[48:49], 0, v[168:169]
	s_mov_b32 m0, s41
	s_nop 0
	global_load_lds_dwordx4 v[178:179], off
	v_lshl_add_u64 v[178:179], s[22:23], 0, v[162:163]
	s_mov_b32 m0, s24
	s_nop 0
	global_load_lds_dwordx4 v[178:179], off
	s_mov_b32 m0, s25
	s_nop 0
	global_load_lds_dwordx4 v[180:181], off
	s_waitcnt vmcnt(8)
	s_waitcnt lgkmcnt(0)
	s_barrier
	s_setprio 1
	s_waitcnt lgkmcnt(0)
	v_mfma_scale_f32_16x16x128_f8f6f4 v[94:97], v[26:33], v[190:197], v[94:97], v1, v1 op_sel_hi:[0,0,0]
	v_mfma_scale_f32_16x16x128_f8f6f4 v[90:93], v[18:25], v[190:197], v[90:93], v1, v1 op_sel_hi:[0,0,0]
	v_mfma_scale_f32_16x16x128_f8f6f4 v[74:77], v[18:25], v[198:205], v[74:77], v1, v1 op_sel_hi:[0,0,0]
	v_mfma_scale_f32_16x16x128_f8f6f4 v[82:85], v[26:33], v[198:205], v[82:85], v1, v1 op_sel_hi:[0,0,0]
	v_mfma_scale_f32_16x16x128_f8f6f4 v[66:69], v[26:33], v[206:213], v[66:69], v1, v1 op_sel_hi:[0,0,0]
	v_mfma_scale_f32_16x16x128_f8f6f4 v[58:61], v[18:25], v[206:213], v[58:61], v1, v1 op_sel_hi:[0,0,0]
	v_mfma_scale_f32_16x16x128_f8f6f4 v[42:45], v[18:25], v[214:221], v[42:45], v1, v1 op_sel_hi:[0,0,0]
	v_mfma_scale_f32_16x16x128_f8f6f4 v[50:53], v[26:33], v[214:221], v[50:53], v1, v1 op_sel_hi:[0,0,0]
	s_setprio 0
	s_setprio 1
	v_mfma_scale_f32_16x16x128_f8f6f4 v[86:89], v[10:17], v[190:197], v[86:89], v1, v1 op_sel_hi:[0,0,0]
	v_mfma_scale_f32_16x16x128_f8f6f4 v[78:81], v[2:9], v[190:197], v[78:81], v1, v1 op_sel_hi:[0,0,0]
	v_mfma_scale_f32_16x16x128_f8f6f4 v[62:65], v[2:9], v[198:205], v[62:65], v1, v1 op_sel_hi:[0,0,0]
	v_mfma_scale_f32_16x16x128_f8f6f4 v[70:73], v[10:17], v[198:205], v[70:73], v1, v1 op_sel_hi:[0,0,0]
	v_mfma_scale_f32_16x16x128_f8f6f4 v[54:57], v[10:17], v[206:213], v[54:57], v1, v1 op_sel_hi:[0,0,0]
	v_mfma_scale_f32_16x16x128_f8f6f4 v[46:49], v[2:9], v[206:213], v[46:49], v1, v1 op_sel_hi:[0,0,0]
	v_mfma_scale_f32_16x16x128_f8f6f4 v[34:37], v[2:9], v[214:221], v[34:37], v1, v1 op_sel_hi:[0,0,0]
	v_mfma_scale_f32_16x16x128_f8f6f4 v[38:41], v[10:17], v[214:221], v[38:41], v1, v1 op_sel_hi:[0,0,0]
	s_setprio 0
	s_barrier
	ds_read_b128 v[2:5], v187
	ds_read_b128 v[6:9], v187 offset:1024
	ds_read_b128 v[10:13], v187 offset:2048
	ds_read_b128 v[14:17], v187 offset:3072
	ds_read_b128 v[18:21], v188
	ds_read_b128 v[22:25], v188 offset:1024
	ds_read_b128 v[26:29], v188 offset:2048
	ds_read_b128 v[30:33], v188 offset:3072
	s_add_u32 s22, s22, 0x80000
	s_addc_u32 s23, s23, 0
	s_mov_b32 m0, s26
	v_lshl_add_u64 v[222:223], s[22:23], 0, v[162:163]
	ds_read_b128 v[190:193], v186 offset:32768
	ds_read_b128 v[194:197], v186 offset:33792
	ds_read_b128 v[198:201], v186 offset:34816
	ds_read_b128 v[202:205], v186 offset:35840
	ds_read_b128 v[206:209], v186 offset:36864
	ds_read_b128 v[210:213], v186 offset:37888
	ds_read_b128 v[214:217], v186 offset:38912
	ds_read_b128 v[218:221], v186 offset:39936
	global_load_lds_dwordx4 v[222:223], off
	v_lshl_add_u64 v[222:223], s[22:23], 0, v[166:167]
	s_mov_b32 m0, s27
	s_nop 0
	global_load_lds_dwordx4 v[222:223], off
	s_waitcnt vmcnt(8)
	s_waitcnt lgkmcnt(0)
	s_barrier
	s_setprio 1
	s_waitcnt lgkmcnt(0)
	v_mfma_scale_f32_16x16x128_f8f6f4 v[158:161], v[2:9], v[190:197], v[158:161], v1, v1 op_sel_hi:[0,0,0]
	v_mfma_scale_f32_16x16x128_f8f6f4 v[154:157], v[10:17], v[190:197], v[154:157], v1, v1 op_sel_hi:[0,0,0]
	v_mfma_scale_f32_16x16x128_f8f6f4 v[138:141], v[10:17], v[198:205], v[138:141], v1, v1 op_sel_hi:[0,0,0]
	v_mfma_scale_f32_16x16x128_f8f6f4 v[146:149], v[2:9], v[198:205], v[146:149], v1, v1 op_sel_hi:[0,0,0]
	v_mfma_scale_f32_16x16x128_f8f6f4 v[130:133], v[2:9], v[206:213], v[130:133], v1, v1 op_sel_hi:[0,0,0]
	v_mfma_scale_f32_16x16x128_f8f6f4 v[122:125], v[10:17], v[206:213], v[122:125], v1, v1 op_sel_hi:[0,0,0]
	v_mfma_scale_f32_16x16x128_f8f6f4 v[106:109], v[10:17], v[214:221], v[106:109], v1, v1 op_sel_hi:[0,0,0]
	v_mfma_scale_f32_16x16x128_f8f6f4 v[114:117], v[2:9], v[214:221], v[114:117], v1, v1 op_sel_hi:[0,0,0]
	s_setprio 0
	s_setprio 1
	v_mfma_scale_f32_16x16x128_f8f6f4 v[150:153], v[18:25], v[190:197], v[150:153], v1, v1 op_sel_hi:[0,0,0]
	v_mfma_scale_f32_16x16x128_f8f6f4 v[142:145], v[26:33], v[190:197], v[142:145], v1, v1 op_sel_hi:[0,0,0]
	v_mfma_scale_f32_16x16x128_f8f6f4 v[126:129], v[26:33], v[198:205], v[126:129], v1, v1 op_sel_hi:[0,0,0]
	v_mfma_scale_f32_16x16x128_f8f6f4 v[134:137], v[18:25], v[198:205], v[134:137], v1, v1 op_sel_hi:[0,0,0]
	v_mfma_scale_f32_16x16x128_f8f6f4 v[118:121], v[18:25], v[206:213], v[118:121], v1, v1 op_sel_hi:[0,0,0]
	v_mfma_scale_f32_16x16x128_f8f6f4 v[110:113], v[26:33], v[206:213], v[110:113], v1, v1 op_sel_hi:[0,0,0]
	v_mfma_scale_f32_16x16x128_f8f6f4 v[98:101], v[26:33], v[214:221], v[98:101], v1, v1 op_sel_hi:[0,0,0]
	v_mfma_scale_f32_16x16x128_f8f6f4 v[102:105], v[18:25], v[214:221], v[102:105], v1, v1 op_sel_hi:[0,0,0]
	s_setprio 0
	s_barrier
	s_mov_b32 m0, s42
	v_lshl_add_u64 v[174:175], v[174:175], 0, s[12:13]
	s_add_u32 s20, s20, 0x80080
	ds_read_b128 v[190:193], v186 offset:49152
	ds_read_b128 v[194:197], v186 offset:50176
	ds_read_b128 v[198:201], v186 offset:51200
	ds_read_b128 v[202:205], v186 offset:52224
	ds_read_b128 v[206:209], v186 offset:53248
	ds_read_b128 v[210:213], v186 offset:54272
	ds_read_b128 v[214:217], v186 offset:55296
	ds_read_b128 v[218:221], v186 offset:56320
	global_load_lds_dwordx4 v[174:175], off
	v_lshl_add_u64 v[174:175], v[176:177], 0, s[12:13]
	s_mov_b32 m0, s43
	s_addc_u32 s21, s21, 0
	global_load_lds_dwordx4 v[174:175], off
	v_lshl_add_u64 v[174:175], s[20:21], 0, v[164:165]
	s_mov_b32 m0, s44
	s_nop 0
	global_load_lds_dwordx4 v[174:175], off
	v_lshl_add_u64 v[174:175], s[20:21], 0, v[168:169]
	s_mov_b32 m0, s45
	s_nop 0
	global_load_lds_dwordx4 v[174:175], off
	v_lshl_add_u64 v[174:175], v[178:179], 0, s[12:13]
	s_mov_b32 m0, s29
	s_nop 0
	global_load_lds_dwordx4 v[174:175], off
	v_lshl_add_u64 v[174:175], v[180:181], 0, s[12:13]
	s_mov_b32 m0, s30
	s_nop 0
	global_load_lds_dwordx4 v[174:175], off
	s_waitcnt vmcnt(8)
	s_waitcnt lgkmcnt(0)
	s_barrier
	s_setprio 1
	s_waitcnt lgkmcnt(0)
	v_mfma_scale_f32_16x16x128_f8f6f4 v[94:97], v[2:9], v[190:197], v[94:97], v1, v1 op_sel_hi:[0,0,0]
	v_mfma_scale_f32_16x16x128_f8f6f4 v[90:93], v[10:17], v[190:197], v[90:93], v1, v1 op_sel_hi:[0,0,0]
	v_mfma_scale_f32_16x16x128_f8f6f4 v[74:77], v[10:17], v[198:205], v[74:77], v1, v1 op_sel_hi:[0,0,0]
	v_mfma_scale_f32_16x16x128_f8f6f4 v[82:85], v[2:9], v[198:205], v[82:85], v1, v1 op_sel_hi:[0,0,0]
	v_mfma_scale_f32_16x16x128_f8f6f4 v[66:69], v[2:9], v[206:213], v[66:69], v1, v1 op_sel_hi:[0,0,0]
	v_mfma_scale_f32_16x16x128_f8f6f4 v[58:61], v[10:17], v[206:213], v[58:61], v1, v1 op_sel_hi:[0,0,0]
	v_mfma_scale_f32_16x16x128_f8f6f4 v[42:45], v[10:17], v[214:221], v[42:45], v1, v1 op_sel_hi:[0,0,0]
	v_mfma_scale_f32_16x16x128_f8f6f4 v[50:53], v[2:9], v[214:221], v[50:53], v1, v1 op_sel_hi:[0,0,0]
	s_setprio 0
	s_setprio 1
	v_mfma_scale_f32_16x16x128_f8f6f4 v[86:89], v[18:25], v[190:197], v[86:89], v1, v1 op_sel_hi:[0,0,0]
	v_mfma_scale_f32_16x16x128_f8f6f4 v[78:81], v[26:33], v[190:197], v[78:81], v1, v1 op_sel_hi:[0,0,0]
	v_mfma_scale_f32_16x16x128_f8f6f4 v[62:65], v[26:33], v[198:205], v[62:65], v1, v1 op_sel_hi:[0,0,0]
	v_mfma_scale_f32_16x16x128_f8f6f4 v[70:73], v[18:25], v[198:205], v[70:73], v1, v1 op_sel_hi:[0,0,0]
	v_mfma_scale_f32_16x16x128_f8f6f4 v[54:57], v[18:25], v[206:213], v[54:57], v1, v1 op_sel_hi:[0,0,0]
	v_mfma_scale_f32_16x16x128_f8f6f4 v[46:49], v[26:33], v[206:213], v[46:49], v1, v1 op_sel_hi:[0,0,0]
	v_mfma_scale_f32_16x16x128_f8f6f4 v[34:37], v[26:33], v[214:221], v[34:37], v1, v1 op_sel_hi:[0,0,0]
	v_mfma_scale_f32_16x16x128_f8f6f4 v[38:41], v[18:25], v[214:221], v[38:41], v1, v1 op_sel_hi:[0,0,0]
	s_setprio 0
	s_barrier
	s_add_i32 s35, s35, 2
	s_add_u32 s16, s16, 0x100
	s_addc_u32 s17, s17, 0
	s_cmp_gt_u32 s35, 13
	s_cbranch_scc0 .LBB0_1291
	s_cmpk_lt_u32 s19, 0x100
	s_cbranch_scc0 .LBB0_1294
	s_barrier

.LBB0_1309:
	ds_read_b128 v[26:29], v189
	ds_read_b128 v[30:33], v189 offset:1024
	ds_read_b128 v[18:21], v189 offset:2048
	ds_read_b128 v[22:25], v189 offset:3072
	ds_read_b128 v[10:13], v190
	ds_read_b128 v[14:17], v190 offset:1024
	ds_read_b128 v[2:5], v190 offset:2048
	ds_read_b128 v[6:9], v190 offset:3072
	s_add_u32 s40, s38, 0xfff80080
	s_addc_u32 s41, s39, -1
	s_cmp_eq_u32 s72, 28
	s_cselect_b32 s43, s18, s41
	s_cselect_b32 s42, s19, s40
	s_cselect_b32 s41, s27, s71
	s_cselect_b32 s40, s29, s70
	v_lshl_add_u64 v[216:217], s[38:39], 0, v[170:171]
	s_add_i32 m0, s37, 0xc000
	ds_read_b128 v[178:181], v191
	ds_read_b128 v[182:185], v191 offset:1024
	ds_read_b128 v[192:195], v191 offset:2048
	ds_read_b128 v[196:199], v191 offset:3072
	ds_read_b128 v[200:203], v191 offset:4096
	ds_read_b128 v[204:207], v191 offset:5120
	ds_read_b128 v[208:211], v191 offset:6144
	ds_read_b128 v[212:215], v191 offset:7168
	global_load_lds_dwordx4 v[216:217], off
	v_lshl_add_u64 v[216:217], s[38:39], 0, v[172:173]
	s_add_i32 m0, s37, 0xe000
	s_nop 0
	global_load_lds_dwordx4 v[216:217], off
	s_waitcnt vmcnt(8)
	s_waitcnt lgkmcnt(0)
	s_barrier
	s_setprio 1
	s_waitcnt lgkmcnt(0)
	v_mfma_scale_f32_16x16x128_f8f6f4 v[158:161], v[26:33], v[178:185], v[158:161], v1, v1 op_sel_hi:[0,0,0]
	v_mfma_scale_f32_16x16x128_f8f6f4 v[154:157], v[18:25], v[178:185], v[154:157], v1, v1 op_sel_hi:[0,0,0]
	v_mfma_scale_f32_16x16x128_f8f6f4 v[138:141], v[18:25], v[192:199], v[138:141], v1, v1 op_sel_hi:[0,0,0]
	v_mfma_scale_f32_16x16x128_f8f6f4 v[146:149], v[26:33], v[192:199], v[146:149], v1, v1 op_sel_hi:[0,0,0]
	v_mfma_scale_f32_16x16x128_f8f6f4 v[130:133], v[26:33], v[200:207], v[130:133], v1, v1 op_sel_hi:[0,0,0]
	v_mfma_scale_f32_16x16x128_f8f6f4 v[122:125], v[18:25], v[200:207], v[122:125], v1, v1 op_sel_hi:[0,0,0]
	v_mfma_scale_f32_16x16x128_f8f6f4 v[106:109], v[18:25], v[208:215], v[106:109], v1, v1 op_sel_hi:[0,0,0]
	v_mfma_scale_f32_16x16x128_f8f6f4 v[114:117], v[26:33], v[208:215], v[114:117], v1, v1 op_sel_hi:[0,0,0]
	s_setprio 0
	s_setprio 1
	v_mfma_scale_f32_16x16x128_f8f6f4 v[150:153], v[10:17], v[178:185], v[150:153], v1, v1 op_sel_hi:[0,0,0]
	v_mfma_scale_f32_16x16x128_f8f6f4 v[142:145], v[2:9], v[178:185], v[142:145], v1, v1 op_sel_hi:[0,0,0]
	v_mfma_scale_f32_16x16x128_f8f6f4 v[126:129], v[2:9], v[192:199], v[126:129], v1, v1 op_sel_hi:[0,0,0]
	v_mfma_scale_f32_16x16x128_f8f6f4 v[134:137], v[10:17], v[192:199], v[134:137], v1, v1 op_sel_hi:[0,0,0]
	v_mfma_scale_f32_16x16x128_f8f6f4 v[118:121], v[10:17], v[200:207], v[118:121], v1, v1 op_sel_hi:[0,0,0]
	v_mfma_scale_f32_16x16x128_f8f6f4 v[110:113], v[2:9], v[200:207], v[110:113], v1, v1 op_sel_hi:[0,0,0]
	v_mfma_scale_f32_16x16x128_f8f6f4 v[98:101], v[2:9], v[208:215], v[98:101], v1, v1 op_sel_hi:[0,0,0]
	v_mfma_scale_f32_16x16x128_f8f6f4 v[102:105], v[10:17], v[208:215], v[102:105], v1, v1 op_sel_hi:[0,0,0]
	s_setprio 0
	s_barrier
	s_add_i32 s64, s59, s3
	v_lshl_add_u64 v[178:179], s[40:41], 0, v[166:167]
	s_mov_b32 m0, s64
	ds_read_b128 v[192:195], v191 offset:16384
	ds_read_b128 v[196:199], v191 offset:17408
	ds_read_b128 v[200:203], v191 offset:18432
	ds_read_b128 v[204:207], v191 offset:19456
	ds_read_b128 v[208:211], v191 offset:20480
	ds_read_b128 v[212:215], v191 offset:21504
	ds_read_b128 v[216:219], v191 offset:22528
	ds_read_b128 v[220:223], v191 offset:23552
	global_load_lds_dwordx4 v[178:179], off
	s_add_i32 m0, s64, 0x2000
	s_add_u32 s64, s40, 0x80000
	v_lshl_add_u64 v[180:181], s[40:41], 0, v[162:163]
	s_addc_u32 s65, s41, 0
	s_add_i32 s73, s62, s3
	global_load_lds_dwordx4 v[180:181], off
	v_lshl_add_u64 v[182:183], s[64:65], 0, v[166:167]
	s_mov_b32 m0, s73
	v_lshl_add_u64 v[184:185], s[42:43], 0, v[164:165]
	global_load_lds_dwordx4 v[182:183], off
	v_lshl_add_u64 v[182:183], s[64:65], 0, v[162:163]
	s_add_i32 m0, s73, 0x2000
	s_nop 0
	global_load_lds_dwordx4 v[182:183], off
	v_lshl_add_u64 v[182:183], s[42:43], 0, v[168:169]
	s_mov_b32 m0, s37
	s_nop 0
	global_load_lds_dwordx4 v[182:183], off
	s_mov_b32 m0, s44
	s_nop 0
	global_load_lds_dwordx4 v[184:185], off
	s_waitcnt vmcnt(8)
	s_waitcnt lgkmcnt(0)
	s_barrier
	s_setprio 1
	s_waitcnt lgkmcnt(0)
	v_mfma_scale_f32_16x16x128_f8f6f4 v[94:97], v[26:33], v[192:199], v[94:97], v1, v1 op_sel_hi:[0,0,0]
	v_mfma_scale_f32_16x16x128_f8f6f4 v[90:93], v[18:25], v[192:199], v[90:93], v1, v1 op_sel_hi:[0,0,0]
	v_mfma_scale_f32_16x16x128_f8f6f4 v[74:77], v[18:25], v[200:207], v[74:77], v1, v1 op_sel_hi:[0,0,0]
	v_mfma_scale_f32_16x16x128_f8f6f4 v[82:85], v[26:33], v[200:207], v[82:85], v1, v1 op_sel_hi:[0,0,0]
	v_mfma_scale_f32_16x16x128_f8f6f4 v[66:69], v[26:33], v[208:215], v[66:69], v1, v1 op_sel_hi:[0,0,0]
	v_mfma_scale_f32_16x16x128_f8f6f4 v[58:61], v[18:25], v[208:215], v[58:61], v1, v1 op_sel_hi:[0,0,0]
	v_mfma_scale_f32_16x16x128_f8f6f4 v[42:45], v[18:25], v[216:223], v[42:45], v1, v1 op_sel_hi:[0,0,0]
	v_mfma_scale_f32_16x16x128_f8f6f4 v[50:53], v[26:33], v[216:223], v[50:53], v1, v1 op_sel_hi:[0,0,0]
	s_setprio 0
	s_setprio 1
	v_mfma_scale_f32_16x16x128_f8f6f4 v[86:89], v[10:17], v[192:199], v[86:89], v1, v1 op_sel_hi:[0,0,0]
	v_mfma_scale_f32_16x16x128_f8f6f4 v[78:81], v[2:9], v[192:199], v[78:81], v1, v1 op_sel_hi:[0,0,0]
	v_mfma_scale_f32_16x16x128_f8f6f4 v[62:65], v[2:9], v[200:207], v[62:65], v1, v1 op_sel_hi:[0,0,0]
	v_mfma_scale_f32_16x16x128_f8f6f4 v[70:73], v[10:17], v[200:207], v[70:73], v1, v1 op_sel_hi:[0,0,0]
	v_mfma_scale_f32_16x16x128_f8f6f4 v[54:57], v[10:17], v[208:215], v[54:57], v1, v1 op_sel_hi:[0,0,0]
	v_mfma_scale_f32_16x16x128_f8f6f4 v[46:49], v[2:9], v[208:215], v[46:49], v1, v1 op_sel_hi:[0,0,0]
	v_mfma_scale_f32_16x16x128_f8f6f4 v[34:37], v[2:9], v[216:223], v[34:37], v1, v1 op_sel_hi:[0,0,0]
	v_mfma_scale_f32_16x16x128_f8f6f4 v[38:41], v[10:17], v[216:223], v[38:41], v1, v1 op_sel_hi:[0,0,0]
	s_setprio 0
	s_barrier
	s_add_i32 s64, 0, 0x18000
	s_add_i32 s65, 0, 0x1c000
	v_add_u32_e32 v14, s64, v187
	v_add_u32_e32 v30, s65, v187
	ds_read_b128 v[2:5], v14
	ds_read_b128 v[6:9], v14 offset:1024
	ds_read_b128 v[10:13], v14 offset:2048
	ds_read_b128 v[14:17], v14 offset:3072
	ds_read_b128 v[18:21], v30
	ds_read_b128 v[22:25], v30 offset:1024
	ds_read_b128 v[26:29], v30 offset:2048
	ds_read_b128 v[30:33], v30 offset:3072
	s_add_u32 s42, s42, 0x80000
	s_addc_u32 s43, s43, 0
	s_mov_b32 m0, s45
	v_lshl_add_u64 v[224:225], s[42:43], 0, v[168:169]
	ds_read_b128 v[192:195], v191 offset:32768
	ds_read_b128 v[196:199], v191 offset:33792
	ds_read_b128 v[200:203], v191 offset:34816
	ds_read_b128 v[204:207], v191 offset:35840
	ds_read_b128 v[208:211], v191 offset:36864
	ds_read_b128 v[212:215], v191 offset:37888
	ds_read_b128 v[216:219], v191 offset:38912
	ds_read_b128 v[220:223], v191 offset:39936
	global_load_lds_dwordx4 v[224:225], off
	v_lshl_add_u64 v[224:225], s[42:43], 0, v[164:165]
	s_mov_b32 m0, s48
	s_nop 0
	global_load_lds_dwordx4 v[224:225], off
	s_waitcnt vmcnt(8)
	s_waitcnt lgkmcnt(0)
	s_barrier
	s_setprio 1
	s_waitcnt lgkmcnt(0)
	v_mfma_scale_f32_16x16x128_f8f6f4 v[158:161], v[2:9], v[192:199], v[158:161], v1, v1 op_sel_hi:[0,0,0]
	v_mfma_scale_f32_16x16x128_f8f6f4 v[154:157], v[10:17], v[192:199], v[154:157], v1, v1 op_sel_hi:[0,0,0]
	v_mfma_scale_f32_16x16x128_f8f6f4 v[138:141], v[10:17], v[200:207], v[138:141], v1, v1 op_sel_hi:[0,0,0]
	v_mfma_scale_f32_16x16x128_f8f6f4 v[146:149], v[2:9], v[200:207], v[146:149], v1, v1 op_sel_hi:[0,0,0]
	v_mfma_scale_f32_16x16x128_f8f6f4 v[130:133], v[2:9], v[208:215], v[130:133], v1, v1 op_sel_hi:[0,0,0]
	v_mfma_scale_f32_16x16x128_f8f6f4 v[122:125], v[10:17], v[208:215], v[122:125], v1, v1 op_sel_hi:[0,0,0]
	v_mfma_scale_f32_16x16x128_f8f6f4 v[106:109], v[10:17], v[216:223], v[106:109], v1, v1 op_sel_hi:[0,0,0]
	v_mfma_scale_f32_16x16x128_f8f6f4 v[114:117], v[2:9], v[216:223], v[114:117], v1, v1 op_sel_hi:[0,0,0]
	s_setprio 0
	s_setprio 1
	v_mfma_scale_f32_16x16x128_f8f6f4 v[150:153], v[18:25], v[192:199], v[150:153], v1, v1 op_sel_hi:[0,0,0]
	v_mfma_scale_f32_16x16x128_f8f6f4 v[142:145], v[26:33], v[192:199], v[142:145], v1, v1 op_sel_hi:[0,0,0]
	v_mfma_scale_f32_16x16x128_f8f6f4 v[126:129], v[26:33], v[200:207], v[126:129], v1, v1 op_sel_hi:[0,0,0]
	v_mfma_scale_f32_16x16x128_f8f6f4 v[134:137], v[18:25], v[200:207], v[134:137], v1, v1 op_sel_hi:[0,0,0]
	v_mfma_scale_f32_16x16x128_f8f6f4 v[118:121], v[18:25], v[208:215], v[118:121], v1, v1 op_sel_hi:[0,0,0]
	v_mfma_scale_f32_16x16x128_f8f6f4 v[110:113], v[26:33], v[208:215], v[110:113], v1, v1 op_sel_hi:[0,0,0]
	v_mfma_scale_f32_16x16x128_f8f6f4 v[98:101], v[26:33], v[216:223], v[98:101], v1, v1 op_sel_hi:[0,0,0]
	v_mfma_scale_f32_16x16x128_f8f6f4 v[102:105], v[18:25], v[216:223], v[102:105], v1, v1 op_sel_hi:[0,0,0]
	s_setprio 0
	s_barrier
	s_add_i32 s42, s64, s3
	v_lshl_add_u64 v[178:179], v[178:179], 0, s[12:13]
	s_mov_b32 m0, s42
	ds_read_b128 v[192:195], v191 offset:49152
	ds_read_b128 v[196:199], v191 offset:50176
	ds_read_b128 v[200:203], v191 offset:51200
	ds_read_b128 v[204:207], v191 offset:52224
	ds_read_b128 v[208:211], v191 offset:53248
	ds_read_b128 v[212:215], v191 offset:54272
	ds_read_b128 v[216:219], v191 offset:55296
	ds_read_b128 v[220:223], v191 offset:56320
	global_load_lds_dwordx4 v[178:179], off
	s_add_i32 m0, s42, 0x2000
	s_add_u32 s40, s40, 0x80080
	v_lshl_add_u64 v[178:179], v[180:181], 0, s[12:13]
	s_addc_u32 s41, s41, 0
	s_add_i32 s42, s65, s3
	global_load_lds_dwordx4 v[178:179], off
	v_lshl_add_u64 v[178:179], s[40:41], 0, v[166:167]
	s_mov_b32 m0, s42
	s_nop 0
	global_load_lds_dwordx4 v[178:179], off
	v_lshl_add_u64 v[178:179], s[40:41], 0, v[162:163]
	s_add_i32 m0, s42, 0x2000
	s_nop 0
	global_load_lds_dwordx4 v[178:179], off
	v_lshl_add_u64 v[178:179], v[182:183], 0, s[12:13]
	s_mov_b32 m0, s51
	s_nop 0
	global_load_lds_dwordx4 v[178:179], off
	v_lshl_add_u64 v[178:179], v[184:185], 0, s[12:13]
	s_mov_b32 m0, s58
	s_nop 0
	global_load_lds_dwordx4 v[178:179], off
	s_waitcnt vmcnt(8)
	s_waitcnt lgkmcnt(0)
	s_barrier
	s_setprio 1
	s_waitcnt lgkmcnt(0)
	v_mfma_scale_f32_16x16x128_f8f6f4 v[94:97], v[2:9], v[192:199], v[94:97], v1, v1 op_sel_hi:[0,0,0]
	v_mfma_scale_f32_16x16x128_f8f6f4 v[90:93], v[10:17], v[192:199], v[90:93], v1, v1 op_sel_hi:[0,0,0]
	v_mfma_scale_f32_16x16x128_f8f6f4 v[74:77], v[10:17], v[200:207], v[74:77], v1, v1 op_sel_hi:[0,0,0]
	v_mfma_scale_f32_16x16x128_f8f6f4 v[82:85], v[2:9], v[200:207], v[82:85], v1, v1 op_sel_hi:[0,0,0]
	v_mfma_scale_f32_16x16x128_f8f6f4 v[66:69], v[2:9], v[208:215], v[66:69], v1, v1 op_sel_hi:[0,0,0]
	v_mfma_scale_f32_16x16x128_f8f6f4 v[58:61], v[10:17], v[208:215], v[58:61], v1, v1 op_sel_hi:[0,0,0]
	v_mfma_scale_f32_16x16x128_f8f6f4 v[42:45], v[10:17], v[216:223], v[42:45], v1, v1 op_sel_hi:[0,0,0]
	v_mfma_scale_f32_16x16x128_f8f6f4 v[50:53], v[2:9], v[216:223], v[50:53], v1, v1 op_sel_hi:[0,0,0]
	s_setprio 0
	s_setprio 1
	v_mfma_scale_f32_16x16x128_f8f6f4 v[86:89], v[18:25], v[192:199], v[86:89], v1, v1 op_sel_hi:[0,0,0]
	v_mfma_scale_f32_16x16x128_f8f6f4 v[78:81], v[26:33], v[192:199], v[78:81], v1, v1 op_sel_hi:[0,0,0]
	v_mfma_scale_f32_16x16x128_f8f6f4 v[62:65], v[26:33], v[200:207], v[62:65], v1, v1 op_sel_hi:[0,0,0]
	v_mfma_scale_f32_16x16x128_f8f6f4 v[70:73], v[18:25], v[200:207], v[70:73], v1, v1 op_sel_hi:[0,0,0]
	v_mfma_scale_f32_16x16x128_f8f6f4 v[54:57], v[18:25], v[208:215], v[54:57], v1, v1 op_sel_hi:[0,0,0]
	v_mfma_scale_f32_16x16x128_f8f6f4 v[46:49], v[26:33], v[208:215], v[46:49], v1, v1 op_sel_hi:[0,0,0]
	v_mfma_scale_f32_16x16x128_f8f6f4 v[34:37], v[26:33], v[216:223], v[34:37], v1, v1 op_sel_hi:[0,0,0]
	v_mfma_scale_f32_16x16x128_f8f6f4 v[38:41], v[18:25], v[216:223], v[38:41], v1, v1 op_sel_hi:[0,0,0]
	s_setprio 0
	s_barrier
	s_add_i32 s72, s72, 2
	s_add_u32 s38, s38, 0x100
	s_addc_u32 s39, s39, 0
	s_add_u32 s70, s70, 0x100
	s_addc_u32 s71, s71, 0
	s_cmp_gt_u32 s72, 29
	s_cbranch_scc0 .LBB0_1309
	s_and_b64 vcc, exec, s[14:15]
	s_cbranch_vccz .LBB0_1312
	s_barrier

.LBB0_1437:
	v_and_b32_e32 v188, 15, v189
	v_and_b32_e32 v2, 48, v189
	v_lshlrev_b32_e32 v3, 2, v189
	s_and_b32 s8, s6, 3
	s_lshl_b32 s9, s7, 13
	v_lshl_or_b32 v2, v188, 6, v2
	v_and_b32_e32 v3, 32, v3
	v_bitop3_b32 v4, v2, s9, v3 bitop3:0xde
	s_lshl_b32 s9, s8, 12
	v_lshl_add_u64 v[180:181], s[20:21], 0, v[154:155]
	v_bitop3_b32 v2, v2, s9, v3 bitop3:0xde
	s_add_i32 s9, s60, s72
	v_lshl_add_u64 v[178:179], s[20:21], 0, v[182:183]
	v_lshl_add_u64 v[72:73], v[180:181], 0, s[36:37]
	s_mov_b32 m0, s9
	s_add_i32 s19, s9, 0x2000
	s_waitcnt vmcnt(2)
	s_barrier
	global_load_lds_dwordx4 v[72:73], off
	v_lshl_add_u64 v[158:159], v[178:179], 0, s[36:37]
	s_mov_b32 m0, s19
	s_add_i32 s18, s67, 0x8000
	global_load_lds_dwordx4 v[158:159], off
	v_lshl_add_u64 v[70:71], v[172:173], 0, s[36:37]
	s_mov_b32 m0, s18
	s_add_i32 s43, s67, 0xa000
	global_load_lds_dwordx4 v[70:71], off
	v_lshl_add_u64 v[160:161], v[170:171], 0, s[36:37]
	s_mov_b32 m0, s43
	s_add_i32 s44, s61, s72
	global_load_lds_dwordx4 v[160:161], off
	v_lshl_add_u64 v[162:163], s[24:25], 0, v[154:155]
	s_mov_b32 m0, s44
	s_add_i32 s45, s44, 0x2000
	global_load_lds_dwordx4 v[162:163], off
	v_lshl_add_u64 v[164:165], s[24:25], 0, v[182:183]
	s_mov_b32 m0, s45
	s_add_i32 s73, 0, 0x10000
	global_load_lds_dwordx4 v[164:165], off
	v_add_u32_e32 v195, s73, v2
	s_add_i32 s75, 0, 0x14000
	s_waitcnt vmcnt(6)
	s_barrier
	v_add_u32_e32 v194, s75, v2
	v_add_u32_e32 v191, 0, v4
	v_add_u32_e32 v193, s60, v2
	v_add_u32_e32 v192, s61, v2
	ds_read_b128 v[54:57], v195
	ds_read_b128 v[58:61], v195 offset:1024
	ds_read_b128 v[196:199], v195 offset:2048
	ds_read_b128 v[200:203], v195 offset:3072
	ds_read_b128 v[10:13], v194
	ds_read_b128 v[14:17], v194 offset:1024
	ds_read_b128 v[2:5], v194 offset:2048
	ds_read_b128 v[6:9], v194 offset:3072
	s_lshl_b32 s66, s7, 6
	v_lshl_add_u64 v[176:177], s[22:23], 0, v[154:155]
	v_lshl_add_u64 v[174:175], s[22:23], 0, v[182:183]
	s_add_u32 s70, s4, 0x10080
	s_addc_u32 s71, s5, 0
	s_add_i32 s74, s67, 0xc000
	v_lshl_add_u64 v[30:31], s[70:71], 0, v[154:155]
	s_mov_b32 m0, s74
	s_add_i32 s69, s67, 0xe000
	ds_read_b128 v[22:25], v191
	ds_read_b128 v[26:29], v191 offset:1024
	ds_read_b128 v[34:37], v191 offset:2048
	ds_read_b128 v[38:41], v191 offset:3072
	ds_read_b128 v[82:85], v191 offset:4096
	ds_read_b128 v[86:89], v191 offset:5120
	ds_read_b128 v[94:97], v191 offset:6144
	ds_read_b128 v[98:101], v191 offset:7168
	global_load_lds_dwordx4 v[30:31], off
	v_lshl_add_u64 v[30:31], s[70:71], 0, v[182:183]
	s_mov_b32 m0, s69
	s_nop 0
	global_load_lds_dwordx4 v[30:31], off
	s_waitcnt vmcnt(8)
	s_waitcnt lgkmcnt(0)
	s_barrier
	s_setprio 1
	v_mov_b64_e32 v[32:33], v[20:21]
	v_mov_b64_e32 v[152:153], v[20:21]
	v_mov_b64_e32 v[92:93], v[20:21]
	v_mov_b64_e32 v[44:45], v[20:21]
	v_mov_b64_e32 v[116:117], v[20:21]
	v_mov_b64_e32 v[64:65], v[20:21]
	v_mov_b64_e32 v[80:81], v[20:21]
	v_mov_b64_e32 v[52:53], v[20:21]
	v_mov_b64_e32 v[30:31], v[18:19]
	v_mov_b64_e32 v[150:151], v[18:19]
	v_mov_b64_e32 v[90:91], v[18:19]
	v_mov_b64_e32 v[42:43], v[18:19]
	v_mov_b64_e32 v[114:115], v[18:19]
	v_mov_b64_e32 v[62:63], v[18:19]
	v_mov_b64_e32 v[78:79], v[18:19]
	v_mov_b64_e32 v[50:51], v[18:19]
	s_waitcnt lgkmcnt(0)
	v_mfma_scale_f32_16x16x128_f8f6f4 v[30:33], v[54:61], v[22:29], v[30:33], v190, v190 op_sel_hi:[0,0,0]
	v_mfma_scale_f32_16x16x128_f8f6f4 v[150:153], v[196:203], v[22:29], v[150:153], v190, v190 op_sel_hi:[0,0,0]
	v_mfma_scale_f32_16x16x128_f8f6f4 v[42:45], v[196:203], v[34:41], v[42:45], v190, v190 op_sel_hi:[0,0,0]
	v_mfma_scale_f32_16x16x128_f8f6f4 v[90:93], v[54:61], v[34:41], v[90:93], v190, v190 op_sel_hi:[0,0,0]
	v_mfma_scale_f32_16x16x128_f8f6f4 v[114:117], v[54:61], v[82:89], v[114:117], v190, v190 op_sel_hi:[0,0,0]
	v_mfma_scale_f32_16x16x128_f8f6f4 v[62:65], v[196:203], v[82:89], v[62:65], v190, v190 op_sel_hi:[0,0,0]
	v_mfma_scale_f32_16x16x128_f8f6f4 v[50:53], v[196:203], v[94:101], v[50:53], v190, v190 op_sel_hi:[0,0,0]
	v_mfma_scale_f32_16x16x128_f8f6f4 v[78:81], v[54:61], v[94:101], v[78:81], v190, v190 op_sel_hi:[0,0,0]
	s_setprio 0
	s_setprio 1
	v_mov_b64_e32 v[144:145], v[20:21]
	v_mov_b64_e32 v[148:149], v[20:21]
	v_mov_b64_e32 v[142:143], v[18:19]
	v_mov_b64_e32 v[146:147], v[18:19]
	v_mfma_scale_f32_16x16x128_f8f6f4 v[142:145], v[10:17], v[22:29], v[142:145], v190, v190 op_sel_hi:[0,0,0]
	v_mfma_scale_f32_16x16x128_f8f6f4 v[146:149], v[2:9], v[22:29], v[146:149], v190, v190 op_sel_hi:[0,0,0]
	v_mov_b64_e32 v[28:29], v[20:21]
	v_mov_b64_e32 v[140:141], v[20:21]
	v_mov_b64_e32 v[26:27], v[18:19]
	v_mov_b64_e32 v[138:139], v[18:19]
	v_mfma_scale_f32_16x16x128_f8f6f4 v[26:29], v[10:17], v[34:41], v[26:29], v190, v190 op_sel_hi:[0,0,0]
	v_mfma_scale_f32_16x16x128_f8f6f4 v[138:141], v[2:9], v[34:41], v[138:141], v190, v190 op_sel_hi:[0,0,0]
	v_mov_b64_e32 v[40:41], v[20:21]
	v_mov_b64_e32 v[128:129], v[20:21]
	v_mov_b64_e32 v[24:25], v[20:21]
	v_mov_b64_e32 v[76:77], v[20:21]
	v_mov_b64_e32 v[38:39], v[18:19]
	v_mov_b64_e32 v[126:127], v[18:19]
	v_mov_b64_e32 v[22:23], v[18:19]
	v_mov_b64_e32 v[74:75], v[18:19]
	v_mfma_scale_f32_16x16x128_f8f6f4 v[38:41], v[10:17], v[82:89], v[38:41], v190, v190 op_sel_hi:[0,0,0]
	v_mfma_scale_f32_16x16x128_f8f6f4 v[126:129], v[2:9], v[82:89], v[126:129], v190, v190 op_sel_hi:[0,0,0]
	v_mfma_scale_f32_16x16x128_f8f6f4 v[22:25], v[10:17], v[94:101], v[22:25], v190, v190 op_sel_hi:[0,0,0]
	v_mfma_scale_f32_16x16x128_f8f6f4 v[74:77], v[2:9], v[94:101], v[74:77], v190, v190 op_sel_hi:[0,0,0]
	s_setprio 0
	s_barrier
	s_add_i32 s70, s73, s72
	v_lshl_add_u64 v[34:35], v[180:181], 0, s[14:15]
	s_mov_b32 m0, s70
	s_add_i32 s71, s70, 0x2000
	ds_read_b128 v[204:207], v191 offset:16384
	ds_read_b128 v[208:211], v191 offset:17408
	ds_read_b128 v[212:215], v191 offset:18432
	ds_read_b128 v[216:219], v191 offset:19456
	ds_read_b128 v[220:223], v191 offset:20480
	ds_read_b128 v[224:227], v191 offset:21504
	ds_read_b128 v[228:231], v191 offset:22528
	ds_read_b128 v[232:235], v191 offset:23552
	global_load_lds_dwordx4 v[34:35], off
	v_lshl_add_u64 v[34:35], v[178:179], 0, s[14:15]
	s_mov_b32 m0, s71
	s_add_i32 s72, s75, s72
	global_load_lds_dwordx4 v[34:35], off
	v_lshl_add_u64 v[34:35], s[26:27], 0, v[154:155]
	s_mov_b32 m0, s72
	s_add_i32 s73, s72, 0x2000
	global_load_lds_dwordx4 v[34:35], off
	v_lshl_add_u64 v[34:35], s[26:27], 0, v[182:183]
	s_mov_b32 m0, s73
	s_nop 0
	global_load_lds_dwordx4 v[34:35], off
	v_lshl_add_u64 v[34:35], v[172:173], 0, s[14:15]
	s_mov_b32 m0, s67
	s_nop 0
	global_load_lds_dwordx4 v[34:35], off
	v_lshl_add_u64 v[34:35], v[170:171], 0, s[14:15]
	s_mov_b32 m0, s68
	s_nop 0
	global_load_lds_dwordx4 v[34:35], off
	s_waitcnt vmcnt(8)
	s_waitcnt lgkmcnt(0)
	s_barrier
	s_setprio 1
	v_mov_b64_e32 v[136:137], v[20:21]
	v_mov_b64_e32 v[104:105], v[20:21]
	v_mov_b64_e32 v[124:125], v[20:21]
	v_mov_b64_e32 v[100:101], v[20:21]
	v_mov_b64_e32 v[112:113], v[20:21]
	v_mov_b64_e32 v[108:109], v[20:21]
	v_mov_b64_e32 v[88:89], v[20:21]
	v_mov_b64_e32 v[84:85], v[20:21]
	v_mov_b64_e32 v[134:135], v[18:19]
	v_mov_b64_e32 v[102:103], v[18:19]
	v_mov_b64_e32 v[122:123], v[18:19]
	v_mov_b64_e32 v[98:99], v[18:19]
	v_mov_b64_e32 v[110:111], v[18:19]
	v_mov_b64_e32 v[106:107], v[18:19]
	v_mov_b64_e32 v[86:87], v[18:19]
	v_mov_b64_e32 v[82:83], v[18:19]
	s_waitcnt lgkmcnt(0)
	v_mfma_scale_f32_16x16x128_f8f6f4 v[134:137], v[54:61], v[204:211], v[134:137], v190, v190 op_sel_hi:[0,0,0]
	v_mfma_scale_f32_16x16x128_f8f6f4 v[102:105], v[196:203], v[204:211], v[102:105], v190, v190 op_sel_hi:[0,0,0]
	v_mfma_scale_f32_16x16x128_f8f6f4 v[98:101], v[196:203], v[212:219], v[98:101], v190, v190 op_sel_hi:[0,0,0]
	v_mfma_scale_f32_16x16x128_f8f6f4 v[122:125], v[54:61], v[212:219], v[122:125], v190, v190 op_sel_hi:[0,0,0]
	v_mfma_scale_f32_16x16x128_f8f6f4 v[110:113], v[54:61], v[220:227], v[110:113], v190, v190 op_sel_hi:[0,0,0]
	v_mfma_scale_f32_16x16x128_f8f6f4 v[106:109], v[196:203], v[220:227], v[106:109], v190, v190 op_sel_hi:[0,0,0]
	v_mfma_scale_f32_16x16x128_f8f6f4 v[82:85], v[196:203], v[228:235], v[82:85], v190, v190 op_sel_hi:[0,0,0]
	v_mfma_scale_f32_16x16x128_f8f6f4 v[86:89], v[54:61], v[228:235], v[86:89], v190, v190 op_sel_hi:[0,0,0]
	s_setprio 0
	s_setprio 1
	v_mov_b64_e32 v[36:37], v[20:21]
	v_mov_b64_e32 v[132:133], v[20:21]
	v_mov_b64_e32 v[48:49], v[20:21]
	v_mov_b64_e32 v[120:121], v[20:21]
	v_mov_b64_e32 v[68:69], v[20:21]
	v_mov_b64_e32 v[96:97], v[20:21]
	v_mov_b64_e32 v[56:57], v[20:21]
	v_mov_b64_e32 v[60:61], v[20:21]
	v_mov_b64_e32 v[34:35], v[18:19]
	v_mov_b64_e32 v[130:131], v[18:19]
	v_mov_b64_e32 v[46:47], v[18:19]
	v_mov_b64_e32 v[118:119], v[18:19]
	v_mov_b64_e32 v[66:67], v[18:19]
	v_mov_b64_e32 v[94:95], v[18:19]
	v_mov_b64_e32 v[54:55], v[18:19]
	v_mov_b64_e32 v[58:59], v[18:19]
	v_mfma_scale_f32_16x16x128_f8f6f4 v[34:37], v[10:17], v[204:211], v[34:37], v190, v190 op_sel_hi:[0,0,0]
	v_mfma_scale_f32_16x16x128_f8f6f4 v[130:133], v[2:9], v[204:211], v[130:133], v190, v190 op_sel_hi:[0,0,0]
	v_mfma_scale_f32_16x16x128_f8f6f4 v[118:121], v[2:9], v[212:219], v[118:121], v190, v190 op_sel_hi:[0,0,0]
	v_mfma_scale_f32_16x16x128_f8f6f4 v[46:49], v[10:17], v[212:219], v[46:49], v190, v190 op_sel_hi:[0,0,0]
	v_mfma_scale_f32_16x16x128_f8f6f4 v[66:69], v[10:17], v[220:227], v[66:69], v190, v190 op_sel_hi:[0,0,0]
	v_mfma_scale_f32_16x16x128_f8f6f4 v[94:97], v[2:9], v[220:227], v[94:97], v190, v190 op_sel_hi:[0,0,0]
	v_mfma_scale_f32_16x16x128_f8f6f4 v[58:61], v[2:9], v[228:235], v[58:61], v190, v190 op_sel_hi:[0,0,0]
	v_mfma_scale_f32_16x16x128_f8f6f4 v[54:57], v[10:17], v[228:235], v[54:57], v190, v190 op_sel_hi:[0,0,0]
	s_setprio 0
	s_barrier
	ds_read_b128 v[2:5], v193
	ds_read_b128 v[6:9], v193 offset:1024
	ds_read_b128 v[10:13], v193 offset:2048
	ds_read_b128 v[14:17], v193 offset:3072
	ds_read_b128 v[196:199], v192
	ds_read_b128 v[200:203], v192 offset:1024
	ds_read_b128 v[204:207], v192 offset:2048
	ds_read_b128 v[208:211], v192 offset:3072
	s_add_u32 s76, s4, 0x10100
	s_addc_u32 s77, s5, 0
	s_mov_b32 m0, s48
	v_lshl_add_u64 v[244:245], s[76:77], 0, v[154:155]
	ds_read_b128 v[212:215], v191 offset:32768
	ds_read_b128 v[216:219], v191 offset:33792
	ds_read_b128 v[220:223], v191 offset:34816
	ds_read_b128 v[224:227], v191 offset:35840
	ds_read_b128 v[228:231], v191 offset:36864
	ds_read_b128 v[232:235], v191 offset:37888
	ds_read_b128 v[236:239], v191 offset:38912
	ds_read_b128 v[240:243], v191 offset:39936
	global_load_lds_dwordx4 v[244:245], off
	v_lshl_add_u64 v[244:245], s[76:77], 0, v[182:183]
	s_mov_b32 m0, s49
	s_nop 0
	global_load_lds_dwordx4 v[244:245], off
	s_waitcnt vmcnt(8)
	s_waitcnt lgkmcnt(0)
	s_barrier
	s_setprio 1
	s_waitcnt lgkmcnt(0)
	v_mfma_scale_f32_16x16x128_f8f6f4 v[30:33], v[2:9], v[212:219], v[30:33], v190, v190 op_sel_hi:[0,0,0]
	v_mfma_scale_f32_16x16x128_f8f6f4 v[150:153], v[10:17], v[212:219], v[150:153], v190, v190 op_sel_hi:[0,0,0]
	v_mfma_scale_f32_16x16x128_f8f6f4 v[42:45], v[10:17], v[220:227], v[42:45], v190, v190 op_sel_hi:[0,0,0]
	v_mfma_scale_f32_16x16x128_f8f6f4 v[90:93], v[2:9], v[220:227], v[90:93], v190, v190 op_sel_hi:[0,0,0]
	v_mfma_scale_f32_16x16x128_f8f6f4 v[114:117], v[2:9], v[228:235], v[114:117], v190, v190 op_sel_hi:[0,0,0]
	v_mfma_scale_f32_16x16x128_f8f6f4 v[62:65], v[10:17], v[228:235], v[62:65], v190, v190 op_sel_hi:[0,0,0]
	v_mfma_scale_f32_16x16x128_f8f6f4 v[50:53], v[10:17], v[236:243], v[50:53], v190, v190 op_sel_hi:[0,0,0]
	v_mfma_scale_f32_16x16x128_f8f6f4 v[78:81], v[2:9], v[236:243], v[78:81], v190, v190 op_sel_hi:[0,0,0]
	s_setprio 0
	s_setprio 1
	v_mfma_scale_f32_16x16x128_f8f6f4 v[142:145], v[196:203], v[212:219], v[142:145], v190, v190 op_sel_hi:[0,0,0]
	v_mfma_scale_f32_16x16x128_f8f6f4 v[146:149], v[204:211], v[212:219], v[146:149], v190, v190 op_sel_hi:[0,0,0]
	v_mfma_scale_f32_16x16x128_f8f6f4 v[138:141], v[204:211], v[220:227], v[138:141], v190, v190 op_sel_hi:[0,0,0]
	v_mfma_scale_f32_16x16x128_f8f6f4 v[26:29], v[196:203], v[220:227], v[26:29], v190, v190 op_sel_hi:[0,0,0]
	v_mfma_scale_f32_16x16x128_f8f6f4 v[38:41], v[196:203], v[228:235], v[38:41], v190, v190 op_sel_hi:[0,0,0]
	v_mfma_scale_f32_16x16x128_f8f6f4 v[126:129], v[204:211], v[228:235], v[126:129], v190, v190 op_sel_hi:[0,0,0]
	v_mfma_scale_f32_16x16x128_f8f6f4 v[74:77], v[204:211], v[236:243], v[74:77], v190, v190 op_sel_hi:[0,0,0]
	v_mfma_scale_f32_16x16x128_f8f6f4 v[22:25], v[196:203], v[236:243], v[22:25], v190, v190 op_sel_hi:[0,0,0]
	s_setprio 0
	s_barrier
	s_mov_b32 m0, s9
	v_lshl_add_u64 v[244:245], v[180:181], 0, s[38:39]
	ds_read_b128 v[212:215], v191 offset:49152
	ds_read_b128 v[216:219], v191 offset:50176
	ds_read_b128 v[220:223], v191 offset:51200
	ds_read_b128 v[224:227], v191 offset:52224
	ds_read_b128 v[228:231], v191 offset:53248
	ds_read_b128 v[232:235], v191 offset:54272
	ds_read_b128 v[236:239], v191 offset:55296
	ds_read_b128 v[240:243], v191 offset:56320
	global_load_lds_dwordx4 v[244:245], off
	v_lshl_add_u64 v[244:245], v[178:179], 0, s[38:39]
	s_mov_b32 m0, s19
	s_nop 0
	global_load_lds_dwordx4 v[244:245], off
	v_lshl_add_u64 v[244:245], s[28:29], 0, v[154:155]
	s_mov_b32 m0, s44
	s_nop 0
	global_load_lds_dwordx4 v[244:245], off
	v_lshl_add_u64 v[244:245], s[28:29], 0, v[182:183]
	s_mov_b32 m0, s45
	s_nop 0
	global_load_lds_dwordx4 v[244:245], off
	v_lshl_add_u64 v[244:245], v[172:173], 0, s[38:39]
	s_mov_b32 m0, s18
	s_nop 0
	global_load_lds_dwordx4 v[244:245], off
	v_lshl_add_u64 v[244:245], v[170:171], 0, s[38:39]
	s_mov_b32 m0, s43
	s_nop 0
	global_load_lds_dwordx4 v[244:245], off
	s_waitcnt vmcnt(8)
	s_waitcnt lgkmcnt(0)
	s_barrier
	s_setprio 1
	s_waitcnt lgkmcnt(0)
	v_mfma_scale_f32_16x16x128_f8f6f4 v[134:137], v[2:9], v[212:219], v[134:137], v190, v190 op_sel_hi:[0,0,0]
	v_mfma_scale_f32_16x16x128_f8f6f4 v[102:105], v[10:17], v[212:219], v[102:105], v190, v190 op_sel_hi:[0,0,0]
	v_mfma_scale_f32_16x16x128_f8f6f4 v[98:101], v[10:17], v[220:227], v[98:101], v190, v190 op_sel_hi:[0,0,0]
	v_mfma_scale_f32_16x16x128_f8f6f4 v[122:125], v[2:9], v[220:227], v[122:125], v190, v190 op_sel_hi:[0,0,0]
	v_mfma_scale_f32_16x16x128_f8f6f4 v[110:113], v[2:9], v[228:235], v[110:113], v190, v190 op_sel_hi:[0,0,0]
	v_mfma_scale_f32_16x16x128_f8f6f4 v[106:109], v[10:17], v[228:235], v[106:109], v190, v190 op_sel_hi:[0,0,0]
	v_mfma_scale_f32_16x16x128_f8f6f4 v[82:85], v[10:17], v[236:243], v[82:85], v190, v190 op_sel_hi:[0,0,0]
	v_mfma_scale_f32_16x16x128_f8f6f4 v[86:89], v[2:9], v[236:243], v[86:89], v190, v190 op_sel_hi:[0,0,0]
	s_setprio 0
	s_setprio 1
	v_mfma_scale_f32_16x16x128_f8f6f4 v[34:37], v[196:203], v[212:219], v[34:37], v190, v190 op_sel_hi:[0,0,0]
	v_mfma_scale_f32_16x16x128_f8f6f4 v[130:133], v[204:211], v[212:219], v[130:133], v190, v190 op_sel_hi:[0,0,0]
	v_mfma_scale_f32_16x16x128_f8f6f4 v[118:121], v[204:211], v[220:227], v[118:121], v190, v190 op_sel_hi:[0,0,0]
	v_mfma_scale_f32_16x16x128_f8f6f4 v[46:49], v[196:203], v[220:227], v[46:49], v190, v190 op_sel_hi:[0,0,0]
	v_mfma_scale_f32_16x16x128_f8f6f4 v[66:69], v[196:203], v[228:235], v[66:69], v190, v190 op_sel_hi:[0,0,0]
	v_mfma_scale_f32_16x16x128_f8f6f4 v[94:97], v[204:211], v[228:235], v[94:97], v190, v190 op_sel_hi:[0,0,0]
	v_mfma_scale_f32_16x16x128_f8f6f4 v[58:61], v[204:211], v[236:243], v[58:61], v190, v190 op_sel_hi:[0,0,0]
	v_mfma_scale_f32_16x16x128_f8f6f4 v[54:57], v[196:203], v[236:243], v[54:57], v190, v190 op_sel_hi:[0,0,0]
	s_setprio 0
	s_barrier
	ds_read_b128 v[2:5], v195
	ds_read_b128 v[6:9], v195 offset:1024
	ds_read_b128 v[10:13], v195 offset:2048
	ds_read_b128 v[14:17], v195 offset:3072
	ds_read_b128 v[196:199], v194
	ds_read_b128 v[200:203], v194 offset:1024
	ds_read_b128 v[204:207], v194 offset:2048
	ds_read_b128 v[208:211], v194 offset:3072
	s_add_u32 s4, s4, 0x10180
	s_addc_u32 s5, s5, 0
	s_mov_b32 m0, s74
	v_lshl_add_u64 v[194:195], s[4:5], 0, v[154:155]
	ds_read_b128 v[212:215], v191
	ds_read_b128 v[216:219], v191 offset:1024
	ds_read_b128 v[220:223], v191 offset:2048
	ds_read_b128 v[224:227], v191 offset:3072
	ds_read_b128 v[228:231], v191 offset:4096
	ds_read_b128 v[232:235], v191 offset:5120
	ds_read_b128 v[236:239], v191 offset:6144
	ds_read_b128 v[240:243], v191 offset:7168
	global_load_lds_dwordx4 v[194:195], off
	v_lshl_add_u64 v[182:183], s[4:5], 0, v[182:183]
	s_mov_b32 m0, s69
	s_nop 0
	global_load_lds_dwordx4 v[182:183], off
	s_waitcnt vmcnt(8)
	s_waitcnt lgkmcnt(0)
	s_barrier
	s_setprio 1
	s_waitcnt lgkmcnt(0)
	v_mfma_scale_f32_16x16x128_f8f6f4 v[30:33], v[2:9], v[212:219], v[30:33], v190, v190 op_sel_hi:[0,0,0]
	v_mfma_scale_f32_16x16x128_f8f6f4 v[150:153], v[10:17], v[212:219], v[150:153], v190, v190 op_sel_hi:[0,0,0]
	v_mfma_scale_f32_16x16x128_f8f6f4 v[42:45], v[10:17], v[220:227], v[42:45], v190, v190 op_sel_hi:[0,0,0]
	v_mfma_scale_f32_16x16x128_f8f6f4 v[90:93], v[2:9], v[220:227], v[90:93], v190, v190 op_sel_hi:[0,0,0]
	v_mfma_scale_f32_16x16x128_f8f6f4 v[114:117], v[2:9], v[228:235], v[114:117], v190, v190 op_sel_hi:[0,0,0]
	v_mfma_scale_f32_16x16x128_f8f6f4 v[62:65], v[10:17], v[228:235], v[62:65], v190, v190 op_sel_hi:[0,0,0]
	v_mfma_scale_f32_16x16x128_f8f6f4 v[50:53], v[10:17], v[236:243], v[50:53], v190, v190 op_sel_hi:[0,0,0]
	v_mfma_scale_f32_16x16x128_f8f6f4 v[78:81], v[2:9], v[236:243], v[78:81], v190, v190 op_sel_hi:[0,0,0]
	s_setprio 0
	s_setprio 1
	v_mfma_scale_f32_16x16x128_f8f6f4 v[142:145], v[196:203], v[212:219], v[142:145], v190, v190 op_sel_hi:[0,0,0]
	v_mfma_scale_f32_16x16x128_f8f6f4 v[146:149], v[204:211], v[212:219], v[146:149], v190, v190 op_sel_hi:[0,0,0]
	v_mfma_scale_f32_16x16x128_f8f6f4 v[138:141], v[204:211], v[220:227], v[138:141], v190, v190 op_sel_hi:[0,0,0]
	v_mfma_scale_f32_16x16x128_f8f6f4 v[26:29], v[196:203], v[220:227], v[26:29], v190, v190 op_sel_hi:[0,0,0]
	v_mfma_scale_f32_16x16x128_f8f6f4 v[38:41], v[196:203], v[228:235], v[38:41], v190, v190 op_sel_hi:[0,0,0]
	v_mfma_scale_f32_16x16x128_f8f6f4 v[126:129], v[204:211], v[228:235], v[126:129], v190, v190 op_sel_hi:[0,0,0]
	v_mfma_scale_f32_16x16x128_f8f6f4 v[74:77], v[204:211], v[236:243], v[74:77], v190, v190 op_sel_hi:[0,0,0]
	v_mfma_scale_f32_16x16x128_f8f6f4 v[22:25], v[196:203], v[236:243], v[22:25], v190, v190 op_sel_hi:[0,0,0]
	s_setprio 0
	s_barrier
	s_mov_b32 m0, s70
	ds_read_b128 v[212:215], v191 offset:16384
	ds_read_b128 v[216:219], v191 offset:17408
	ds_read_b128 v[220:223], v191 offset:18432
	ds_read_b128 v[224:227], v191 offset:19456
	ds_read_b128 v[228:231], v191 offset:20480
	ds_read_b128 v[232:235], v191 offset:21504
	ds_read_b128 v[236:239], v191 offset:22528
	ds_read_b128 v[240:243], v191 offset:23552
	global_load_lds_dwordx4 v[180:181], off
	s_mov_b32 m0, s71
	s_nop 0
	global_load_lds_dwordx4 v[178:179], off
	s_mov_b32 m0, s72
	s_nop 0
	global_load_lds_dwordx4 v[176:177], off
	s_mov_b32 m0, s73
	s_nop 0
	global_load_lds_dwordx4 v[174:175], off
	s_mov_b32 m0, s67
	s_nop 0
	global_load_lds_dwordx4 v[172:173], off
	s_mov_b32 m0, s68
	s_nop 0
	global_load_lds_dwordx4 v[170:171], off
	s_waitcnt vmcnt(8)
	s_waitcnt lgkmcnt(0)
	s_barrier
	s_setprio 1
	s_waitcnt lgkmcnt(0)
	v_mfma_scale_f32_16x16x128_f8f6f4 v[134:137], v[2:9], v[212:219], v[134:137], v190, v190 op_sel_hi:[0,0,0]
	v_mfma_scale_f32_16x16x128_f8f6f4 v[102:105], v[10:17], v[212:219], v[102:105], v190, v190 op_sel_hi:[0,0,0]
	v_mfma_scale_f32_16x16x128_f8f6f4 v[98:101], v[10:17], v[220:227], v[98:101], v190, v190 op_sel_hi:[0,0,0]
	v_mfma_scale_f32_16x16x128_f8f6f4 v[122:125], v[2:9], v[220:227], v[122:125], v190, v190 op_sel_hi:[0,0,0]
	v_mfma_scale_f32_16x16x128_f8f6f4 v[110:113], v[2:9], v[228:235], v[110:113], v190, v190 op_sel_hi:[0,0,0]
	v_mfma_scale_f32_16x16x128_f8f6f4 v[106:109], v[10:17], v[228:235], v[106:109], v190, v190 op_sel_hi:[0,0,0]
	v_mfma_scale_f32_16x16x128_f8f6f4 v[82:85], v[10:17], v[236:243], v[82:85], v190, v190 op_sel_hi:[0,0,0]
	v_mfma_scale_f32_16x16x128_f8f6f4 v[86:89], v[2:9], v[236:243], v[86:89], v190, v190 op_sel_hi:[0,0,0]
	s_setprio 0
	s_setprio 1
	v_mfma_scale_f32_16x16x128_f8f6f4 v[34:37], v[196:203], v[212:219], v[34:37], v190, v190 op_sel_hi:[0,0,0]
	v_mfma_scale_f32_16x16x128_f8f6f4 v[130:133], v[204:211], v[212:219], v[130:133], v190, v190 op_sel_hi:[0,0,0]
	v_mfma_scale_f32_16x16x128_f8f6f4 v[118:121], v[204:211], v[220:227], v[118:121], v190, v190 op_sel_hi:[0,0,0]
	v_mfma_scale_f32_16x16x128_f8f6f4 v[46:49], v[196:203], v[220:227], v[46:49], v190, v190 op_sel_hi:[0,0,0]
	v_mfma_scale_f32_16x16x128_f8f6f4 v[66:69], v[196:203], v[228:235], v[66:69], v190, v190 op_sel_hi:[0,0,0]
	v_mfma_scale_f32_16x16x128_f8f6f4 v[94:97], v[204:211], v[228:235], v[94:97], v190, v190 op_sel_hi:[0,0,0]
	v_mfma_scale_f32_16x16x128_f8f6f4 v[58:61], v[204:211], v[236:243], v[58:61], v190, v190 op_sel_hi:[0,0,0]
	v_mfma_scale_f32_16x16x128_f8f6f4 v[54:57], v[196:203], v[236:243], v[54:57], v190, v190 op_sel_hi:[0,0,0]
	s_setprio 0
	s_barrier
	ds_read_b128 v[2:5], v193
	ds_read_b128 v[6:9], v193 offset:1024
	ds_read_b128 v[10:13], v193 offset:2048
	ds_read_b128 v[14:17], v193 offset:3072
	ds_read_b128 v[170:173], v192
	ds_read_b128 v[174:177], v192 offset:1024
	ds_read_b128 v[194:197], v192 offset:2048
	ds_read_b128 v[198:201], v192 offset:3072
	s_mov_b32 m0, s48
	ds_read_b128 v[202:205], v191 offset:32768
	ds_read_b128 v[206:209], v191 offset:33792
	ds_read_b128 v[210:213], v191 offset:34816
	ds_read_b128 v[214:217], v191 offset:35840
	ds_read_b128 v[218:221], v191 offset:36864
	ds_read_b128 v[222:225], v191 offset:37888
	ds_read_b128 v[226:229], v191 offset:38912
	ds_read_b128 v[230:233], v191 offset:39936
	global_load_lds_dwordx4 v[166:167], off
	s_mov_b32 m0, s49
	s_nop 0
	global_load_lds_dwordx4 v[168:169], off
	s_waitcnt vmcnt(8)
	s_waitcnt lgkmcnt(0)
	s_barrier
	s_setprio 1
	s_waitcnt lgkmcnt(0)
	v_mfma_scale_f32_16x16x128_f8f6f4 v[30:33], v[2:9], v[202:209], v[30:33], v190, v190 op_sel_hi:[0,0,0]
	v_mfma_scale_f32_16x16x128_f8f6f4 v[150:153], v[10:17], v[202:209], v[150:153], v190, v190 op_sel_hi:[0,0,0]
	v_mfma_scale_f32_16x16x128_f8f6f4 v[42:45], v[10:17], v[210:217], v[42:45], v190, v190 op_sel_hi:[0,0,0]
	v_mfma_scale_f32_16x16x128_f8f6f4 v[90:93], v[2:9], v[210:217], v[90:93], v190, v190 op_sel_hi:[0,0,0]
	v_mfma_scale_f32_16x16x128_f8f6f4 v[114:117], v[2:9], v[218:225], v[114:117], v190, v190 op_sel_hi:[0,0,0]
	v_mfma_scale_f32_16x16x128_f8f6f4 v[62:65], v[10:17], v[218:225], v[62:65], v190, v190 op_sel_hi:[0,0,0]
	v_mfma_scale_f32_16x16x128_f8f6f4 v[50:53], v[10:17], v[226:233], v[50:53], v190, v190 op_sel_hi:[0,0,0]
	v_mfma_scale_f32_16x16x128_f8f6f4 v[78:81], v[2:9], v[226:233], v[78:81], v190, v190 op_sel_hi:[0,0,0]
	s_setprio 0
	s_setprio 1
	v_mfma_scale_f32_16x16x128_f8f6f4 v[142:145], v[170:177], v[202:209], v[142:145], v190, v190 op_sel_hi:[0,0,0]
	v_mfma_scale_f32_16x16x128_f8f6f4 v[146:149], v[194:201], v[202:209], v[146:149], v190, v190 op_sel_hi:[0,0,0]
	v_mfma_scale_f32_16x16x128_f8f6f4 v[138:141], v[194:201], v[210:217], v[138:141], v190, v190 op_sel_hi:[0,0,0]
	v_mfma_scale_f32_16x16x128_f8f6f4 v[26:29], v[170:177], v[210:217], v[26:29], v190, v190 op_sel_hi:[0,0,0]
	v_mfma_scale_f32_16x16x128_f8f6f4 v[38:41], v[170:177], v[218:225], v[38:41], v190, v190 op_sel_hi:[0,0,0]
	v_mfma_scale_f32_16x16x128_f8f6f4 v[126:129], v[194:201], v[218:225], v[126:129], v190, v190 op_sel_hi:[0,0,0]
	v_mfma_scale_f32_16x16x128_f8f6f4 v[74:77], v[194:201], v[226:233], v[74:77], v190, v190 op_sel_hi:[0,0,0]
	v_mfma_scale_f32_16x16x128_f8f6f4 v[22:25], v[170:177], v[226:233], v[22:25], v190, v190 op_sel_hi:[0,0,0]
	s_setprio 0
	s_barrier
	s_mov_b32 m0, s9
	ds_read_b128 v[202:205], v191 offset:49152
	ds_read_b128 v[206:209], v191 offset:50176
	ds_read_b128 v[210:213], v191 offset:51200
	ds_read_b128 v[214:217], v191 offset:52224
	ds_read_b128 v[218:221], v191 offset:53248
	ds_read_b128 v[222:225], v191 offset:54272
	ds_read_b128 v[226:229], v191 offset:55296
	ds_read_b128 v[230:233], v191 offset:56320
	global_load_lds_dwordx4 v[72:73], off
	s_mov_b32 m0, s19
	s_nop 0
	global_load_lds_dwordx4 v[158:159], off
	s_mov_b32 m0, s44
	s_nop 0
	global_load_lds_dwordx4 v[162:163], off
	s_mov_b32 m0, s45
	s_nop 0
	global_load_lds_dwordx4 v[164:165], off
	s_mov_b32 m0, s18
	s_nop 0
	global_load_lds_dwordx4 v[70:71], off
	s_mov_b32 m0, s43
	s_nop 0
	global_load_lds_dwordx4 v[160:161], off
	s_waitcnt vmcnt(8)
	s_waitcnt lgkmcnt(0)
	s_barrier
	s_setprio 1
	s_waitcnt lgkmcnt(0)
	v_mfma_scale_f32_16x16x128_f8f6f4 v[134:137], v[2:9], v[202:209], v[134:137], v190, v190 op_sel_hi:[0,0,0]
	v_mfma_scale_f32_16x16x128_f8f6f4 v[102:105], v[10:17], v[202:209], v[102:105], v190, v190 op_sel_hi:[0,0,0]
	v_mfma_scale_f32_16x16x128_f8f6f4 v[98:101], v[10:17], v[210:217], v[98:101], v190, v190 op_sel_hi:[0,0,0]
	v_mfma_scale_f32_16x16x128_f8f6f4 v[122:125], v[2:9], v[210:217], v[122:125], v190, v190 op_sel_hi:[0,0,0]
	v_mfma_scale_f32_16x16x128_f8f6f4 v[110:113], v[2:9], v[218:225], v[110:113], v190, v190 op_sel_hi:[0,0,0]
	v_mfma_scale_f32_16x16x128_f8f6f4 v[106:109], v[10:17], v[218:225], v[106:109], v190, v190 op_sel_hi:[0,0,0]
	v_mfma_scale_f32_16x16x128_f8f6f4 v[82:85], v[10:17], v[226:233], v[82:85], v190, v190 op_sel_hi:[0,0,0]
	v_mfma_scale_f32_16x16x128_f8f6f4 v[86:89], v[2:9], v[226:233], v[86:89], v190, v190 op_sel_hi:[0,0,0]
	s_setprio 0
	s_setprio 1
	v_mfma_scale_f32_16x16x128_f8f6f4 v[34:37], v[170:177], v[202:209], v[34:37], v190, v190 op_sel_hi:[0,0,0]
	v_mfma_scale_f32_16x16x128_f8f6f4 v[130:133], v[194:201], v[202:209], v[130:133], v190, v190 op_sel_hi:[0,0,0]
	v_mfma_scale_f32_16x16x128_f8f6f4 v[118:121], v[194:201], v[210:217], v[118:121], v190, v190 op_sel_hi:[0,0,0]
	v_mfma_scale_f32_16x16x128_f8f6f4 v[46:49], v[170:177], v[210:217], v[46:49], v190, v190 op_sel_hi:[0,0,0]
	v_mfma_scale_f32_16x16x128_f8f6f4 v[66:69], v[170:177], v[218:225], v[66:69], v190, v190 op_sel_hi:[0,0,0]
	v_mfma_scale_f32_16x16x128_f8f6f4 v[94:97], v[194:201], v[218:225], v[94:97], v190, v190 op_sel_hi:[0,0,0]
	v_mfma_scale_f32_16x16x128_f8f6f4 v[58:61], v[194:201], v[226:233], v[58:61], v190, v190 op_sel_hi:[0,0,0]
	v_mfma_scale_f32_16x16x128_f8f6f4 v[54:57], v[170:177], v[226:233], v[54:57], v190, v190 op_sel_hi:[0,0,0]
	s_setprio 0
	s_barrier
	s_waitcnt vmcnt(0)
	s_cmpk_gt_u32 s65, 0xff
	s_cbranch_scc1 .LBB0_1439
	s_barrier

.LBB0_1558:
	s_add_u32 s39, s30, s38
	s_addc_u32 s44, s31, 0
	s_add_u32 s42, s39, 0x100
	s_addc_u32 s43, s44, 0
	s_and_b64 s[40:41], s[36:37], exec
	s_cselect_b32 s41, s18, s43
	s_cselect_b32 s40, s19, s42
	s_add_u32 s38, s28, s38
	s_addc_u32 s42, s29, 0
	s_add_u32 s38, s38, 0x100
	s_addc_u32 s42, s42, 0
	s_and_b64 s[36:37], s[36:37], exec
	s_cselect_b32 s43, s17, s42
	s_cselect_b32 s42, s21, s38
	s_add_u32 s76, s39, 0x10080
	ds_read_b128 v[26:29], v181
	ds_read_b128 v[30:33], v181 offset:1024
	ds_read_b128 v[18:21], v181 offset:2048
	ds_read_b128 v[22:25], v181 offset:3072
	ds_read_b128 v[10:13], v182
	ds_read_b128 v[14:17], v182 offset:1024
	ds_read_b128 v[2:5], v182 offset:2048
	ds_read_b128 v[6:9], v182 offset:3072
	s_addc_u32 s77, s44, 0
	s_add_i32 s75, s63, s15
	s_add_i32 m0, s27, 0xc000
	s_add_i32 s78, s27, 0xe000
	s_add_i32 s72, s75, 0x2000
	s_add_u32 s44, s42, 0x10000
	s_addc_u32 s45, s43, 0
	s_add_i32 s74, s64, s15
	s_add_i32 s73, s74, 0x2000
	s_add_i32 s71, 0, 0x18000
	s_add_i32 s70, 0, 0x1c000
	s_add_u32 s38, s40, 0x10000
	s_addc_u32 s39, s41, 0
	s_add_i32 s69, s71, s15
	s_add_i32 s67, s69, 0x2000
	s_add_u32 s36, s42, 0x10080
	s_addc_u32 s37, s43, 0
	s_add_i32 s68, s70, s15
	s_add_i32 s66, s68, 0x2000
	v_lshl_add_u64 v[208:209], s[76:77], 0, v[164:165]
	ds_read_b128 v[170:173], v183
	ds_read_b128 v[174:177], v183 offset:1024
	ds_read_b128 v[184:187], v183 offset:2048
	ds_read_b128 v[188:191], v183 offset:3072
	ds_read_b128 v[192:195], v183 offset:4096
	ds_read_b128 v[196:199], v183 offset:5120
	ds_read_b128 v[200:203], v183 offset:6144
	ds_read_b128 v[204:207], v183 offset:7168
	global_load_lds_dwordx4 v[208:209], off
	v_lshl_add_u64 v[208:209], s[76:77], 0, v[162:163]
	s_mov_b32 m0, s78
	s_nop 0
	global_load_lds_dwordx4 v[208:209], off
	s_waitcnt vmcnt(8)
	s_waitcnt lgkmcnt(0)
	s_barrier
	s_setprio 1
	s_waitcnt lgkmcnt(0)
	v_mfma_scale_f32_16x16x128_f8f6f4 v[158:161], v[26:33], v[170:177], v[158:161], v1, v1 op_sel_hi:[0,0,0]
	v_mfma_scale_f32_16x16x128_f8f6f4 v[154:157], v[18:25], v[170:177], v[154:157], v1, v1 op_sel_hi:[0,0,0]
	v_mfma_scale_f32_16x16x128_f8f6f4 v[138:141], v[18:25], v[184:191], v[138:141], v1, v1 op_sel_hi:[0,0,0]
	v_mfma_scale_f32_16x16x128_f8f6f4 v[142:145], v[26:33], v[184:191], v[142:145], v1, v1 op_sel_hi:[0,0,0]
	v_mfma_scale_f32_16x16x128_f8f6f4 v[126:129], v[26:33], v[192:199], v[126:129], v1, v1 op_sel_hi:[0,0,0]
	v_mfma_scale_f32_16x16x128_f8f6f4 v[122:125], v[18:25], v[192:199], v[122:125], v1, v1 op_sel_hi:[0,0,0]
	v_mfma_scale_f32_16x16x128_f8f6f4 v[106:109], v[18:25], v[200:207], v[106:109], v1, v1 op_sel_hi:[0,0,0]
	v_mfma_scale_f32_16x16x128_f8f6f4 v[110:113], v[26:33], v[200:207], v[110:113], v1, v1 op_sel_hi:[0,0,0]
	s_setprio 0
	s_setprio 1
	v_mfma_scale_f32_16x16x128_f8f6f4 v[150:153], v[10:17], v[170:177], v[150:153], v1, v1 op_sel_hi:[0,0,0]
	v_mfma_scale_f32_16x16x128_f8f6f4 v[146:149], v[2:9], v[170:177], v[146:149], v1, v1 op_sel_hi:[0,0,0]
	v_mfma_scale_f32_16x16x128_f8f6f4 v[130:133], v[2:9], v[184:191], v[130:133], v1, v1 op_sel_hi:[0,0,0]
	v_mfma_scale_f32_16x16x128_f8f6f4 v[134:137], v[10:17], v[184:191], v[134:137], v1, v1 op_sel_hi:[0,0,0]
	v_mfma_scale_f32_16x16x128_f8f6f4 v[118:121], v[10:17], v[192:199], v[118:121], v1, v1 op_sel_hi:[0,0,0]
	v_mfma_scale_f32_16x16x128_f8f6f4 v[114:117], v[2:9], v[192:199], v[114:117], v1, v1 op_sel_hi:[0,0,0]
	v_mfma_scale_f32_16x16x128_f8f6f4 v[98:101], v[2:9], v[200:207], v[98:101], v1, v1 op_sel_hi:[0,0,0]
	v_mfma_scale_f32_16x16x128_f8f6f4 v[102:105], v[10:17], v[200:207], v[102:105], v1, v1 op_sel_hi:[0,0,0]
	s_setprio 0
	s_barrier
	s_mov_b32 m0, s75
	v_lshl_add_u64 v[170:171], s[42:43], 0, v[164:165]
	ds_read_b128 v[184:187], v183 offset:16384
	ds_read_b128 v[188:191], v183 offset:17408
	ds_read_b128 v[192:195], v183 offset:18432
	ds_read_b128 v[196:199], v183 offset:19456
	ds_read_b128 v[200:203], v183 offset:20480
	ds_read_b128 v[204:207], v183 offset:21504
	ds_read_b128 v[208:211], v183 offset:22528
	ds_read_b128 v[212:215], v183 offset:23552
	global_load_lds_dwordx4 v[170:171], off
	v_lshl_add_u64 v[172:173], s[42:43], 0, v[162:163]
	s_mov_b32 m0, s72
	v_lshl_add_u64 v[174:175], s[44:45], 0, v[164:165]
	global_load_lds_dwordx4 v[172:173], off
	s_mov_b32 m0, s74
	v_lshl_add_u64 v[176:177], s[40:41], 0, v[162:163]
	global_load_lds_dwordx4 v[174:175], off
	v_lshl_add_u64 v[174:175], s[44:45], 0, v[162:163]
	s_mov_b32 m0, s73
	s_nop 0
	global_load_lds_dwordx4 v[174:175], off
	v_lshl_add_u64 v[174:175], s[40:41], 0, v[164:165]
	s_mov_b32 m0, s27
	s_nop 0
	global_load_lds_dwordx4 v[174:175], off
	s_mov_b32 m0, s49
	s_nop 0
	global_load_lds_dwordx4 v[176:177], off
	s_waitcnt vmcnt(8)
	s_waitcnt lgkmcnt(0)
	s_barrier
	s_setprio 1
	s_waitcnt lgkmcnt(0)
	v_mfma_scale_f32_16x16x128_f8f6f4 v[94:97], v[26:33], v[184:191], v[94:97], v1, v1 op_sel_hi:[0,0,0]
	v_mfma_scale_f32_16x16x128_f8f6f4 v[90:93], v[18:25], v[184:191], v[90:93], v1, v1 op_sel_hi:[0,0,0]
	v_mfma_scale_f32_16x16x128_f8f6f4 v[74:77], v[18:25], v[192:199], v[74:77], v1, v1 op_sel_hi:[0,0,0]
	v_mfma_scale_f32_16x16x128_f8f6f4 v[78:81], v[26:33], v[192:199], v[78:81], v1, v1 op_sel_hi:[0,0,0]
	v_mfma_scale_f32_16x16x128_f8f6f4 v[62:65], v[26:33], v[200:207], v[62:65], v1, v1 op_sel_hi:[0,0,0]
	v_mfma_scale_f32_16x16x128_f8f6f4 v[58:61], v[18:25], v[200:207], v[58:61], v1, v1 op_sel_hi:[0,0,0]
	v_mfma_scale_f32_16x16x128_f8f6f4 v[42:45], v[18:25], v[208:215], v[42:45], v1, v1 op_sel_hi:[0,0,0]
	v_mfma_scale_f32_16x16x128_f8f6f4 v[54:57], v[26:33], v[208:215], v[54:57], v1, v1 op_sel_hi:[0,0,0]
	s_setprio 0
	s_setprio 1
	v_mfma_scale_f32_16x16x128_f8f6f4 v[86:89], v[10:17], v[184:191], v[86:89], v1, v1 op_sel_hi:[0,0,0]
	v_mfma_scale_f32_16x16x128_f8f6f4 v[82:85], v[2:9], v[184:191], v[82:85], v1, v1 op_sel_hi:[0,0,0]
	v_mfma_scale_f32_16x16x128_f8f6f4 v[66:69], v[2:9], v[192:199], v[66:69], v1, v1 op_sel_hi:[0,0,0]
	v_mfma_scale_f32_16x16x128_f8f6f4 v[70:73], v[10:17], v[192:199], v[70:73], v1, v1 op_sel_hi:[0,0,0]
	v_mfma_scale_f32_16x16x128_f8f6f4 v[50:53], v[10:17], v[200:207], v[50:53], v1, v1 op_sel_hi:[0,0,0]
	v_mfma_scale_f32_16x16x128_f8f6f4 v[46:49], v[2:9], v[200:207], v[46:49], v1, v1 op_sel_hi:[0,0,0]
	v_mfma_scale_f32_16x16x128_f8f6f4 v[34:37], v[2:9], v[208:215], v[34:37], v1, v1 op_sel_hi:[0,0,0]
	v_mfma_scale_f32_16x16x128_f8f6f4 v[38:41], v[10:17], v[208:215], v[38:41], v1, v1 op_sel_hi:[0,0,0]
	s_setprio 0
	s_barrier
	v_add_u32_e32 v14, s71, v179
	v_add_u32_e32 v30, s70, v179
	ds_read_b128 v[2:5], v14
	ds_read_b128 v[6:9], v14 offset:1024
	ds_read_b128 v[10:13], v14 offset:2048
	ds_read_b128 v[14:17], v14 offset:3072
	ds_read_b128 v[18:21], v30
	ds_read_b128 v[22:25], v30 offset:1024
	ds_read_b128 v[26:29], v30 offset:2048
	ds_read_b128 v[30:33], v30 offset:3072
	s_mov_b32 m0, s50
	v_lshl_add_u64 v[216:217], s[38:39], 0, v[164:165]
	ds_read_b128 v[184:187], v183 offset:32768
	ds_read_b128 v[188:191], v183 offset:33792
	ds_read_b128 v[192:195], v183 offset:34816
	ds_read_b128 v[196:199], v183 offset:35840
	ds_read_b128 v[200:203], v183 offset:36864
	ds_read_b128 v[204:207], v183 offset:37888
	ds_read_b128 v[208:211], v183 offset:38912
	ds_read_b128 v[212:215], v183 offset:39936
	global_load_lds_dwordx4 v[216:217], off
	v_lshl_add_u64 v[216:217], s[38:39], 0, v[162:163]
	s_mov_b32 m0, s51
	s_nop 0
	global_load_lds_dwordx4 v[216:217], off
	s_waitcnt vmcnt(8)
	s_waitcnt lgkmcnt(0)
	s_barrier
	s_setprio 1
	s_waitcnt lgkmcnt(0)
	v_mfma_scale_f32_16x16x128_f8f6f4 v[158:161], v[2:9], v[184:191], v[158:161], v1, v1 op_sel_hi:[0,0,0]
	v_mfma_scale_f32_16x16x128_f8f6f4 v[154:157], v[10:17], v[184:191], v[154:157], v1, v1 op_sel_hi:[0,0,0]
	v_mfma_scale_f32_16x16x128_f8f6f4 v[138:141], v[10:17], v[192:199], v[138:141], v1, v1 op_sel_hi:[0,0,0]
	v_mfma_scale_f32_16x16x128_f8f6f4 v[142:145], v[2:9], v[192:199], v[142:145], v1, v1 op_sel_hi:[0,0,0]
	v_mfma_scale_f32_16x16x128_f8f6f4 v[126:129], v[2:9], v[200:207], v[126:129], v1, v1 op_sel_hi:[0,0,0]
	v_mfma_scale_f32_16x16x128_f8f6f4 v[122:125], v[10:17], v[200:207], v[122:125], v1, v1 op_sel_hi:[0,0,0]
	v_mfma_scale_f32_16x16x128_f8f6f4 v[106:109], v[10:17], v[208:215], v[106:109], v1, v1 op_sel_hi:[0,0,0]
	v_mfma_scale_f32_16x16x128_f8f6f4 v[110:113], v[2:9], v[208:215], v[110:113], v1, v1 op_sel_hi:[0,0,0]
	s_setprio 0
	s_setprio 1
	v_mfma_scale_f32_16x16x128_f8f6f4 v[150:153], v[18:25], v[184:191], v[150:153], v1, v1 op_sel_hi:[0,0,0]
	v_mfma_scale_f32_16x16x128_f8f6f4 v[146:149], v[26:33], v[184:191], v[146:149], v1, v1 op_sel_hi:[0,0,0]
	v_mfma_scale_f32_16x16x128_f8f6f4 v[130:133], v[26:33], v[192:199], v[130:133], v1, v1 op_sel_hi:[0,0,0]
	v_mfma_scale_f32_16x16x128_f8f6f4 v[134:137], v[18:25], v[192:199], v[134:137], v1, v1 op_sel_hi:[0,0,0]
	v_mfma_scale_f32_16x16x128_f8f6f4 v[118:121], v[18:25], v[200:207], v[118:121], v1, v1 op_sel_hi:[0,0,0]
	v_mfma_scale_f32_16x16x128_f8f6f4 v[114:117], v[26:33], v[200:207], v[114:117], v1, v1 op_sel_hi:[0,0,0]
	v_mfma_scale_f32_16x16x128_f8f6f4 v[98:101], v[26:33], v[208:215], v[98:101], v1, v1 op_sel_hi:[0,0,0]
	v_mfma_scale_f32_16x16x128_f8f6f4 v[102:105], v[18:25], v[208:215], v[102:105], v1, v1 op_sel_hi:[0,0,0]
	s_setprio 0
	s_barrier
	s_mov_b32 m0, s69
	v_lshl_add_u64 v[170:171], v[170:171], 0, s[8:9]
	ds_read_b128 v[184:187], v183 offset:49152
	ds_read_b128 v[188:191], v183 offset:50176
	ds_read_b128 v[192:195], v183 offset:51200
	ds_read_b128 v[196:199], v183 offset:52224
	ds_read_b128 v[200:203], v183 offset:53248
	ds_read_b128 v[204:207], v183 offset:54272
	ds_read_b128 v[208:211], v183 offset:55296
	ds_read_b128 v[212:215], v183 offset:56320
	global_load_lds_dwordx4 v[170:171], off
	v_lshl_add_u64 v[170:171], v[172:173], 0, s[8:9]
	s_mov_b32 m0, s67
	s_nop 0
	global_load_lds_dwordx4 v[170:171], off
	v_lshl_add_u64 v[170:171], s[36:37], 0, v[164:165]
	s_mov_b32 m0, s68
	s_nop 0
	global_load_lds_dwordx4 v[170:171], off
	v_lshl_add_u64 v[170:171], s[36:37], 0, v[162:163]
	s_mov_b32 m0, s66
	s_nop 0
	global_load_lds_dwordx4 v[170:171], off
	v_lshl_add_u64 v[170:171], v[174:175], 0, s[8:9]
	s_mov_b32 m0, s61
	s_nop 0
	global_load_lds_dwordx4 v[170:171], off
	v_lshl_add_u64 v[170:171], v[176:177], 0, s[8:9]
	s_mov_b32 m0, s62
	s_nop 0
	global_load_lds_dwordx4 v[170:171], off
	s_waitcnt vmcnt(8)
	s_waitcnt lgkmcnt(0)
	s_barrier
	s_setprio 1
	s_waitcnt lgkmcnt(0)
	v_mfma_scale_f32_16x16x128_f8f6f4 v[94:97], v[2:9], v[184:191], v[94:97], v1, v1 op_sel_hi:[0,0,0]
	v_mfma_scale_f32_16x16x128_f8f6f4 v[90:93], v[10:17], v[184:191], v[90:93], v1, v1 op_sel_hi:[0,0,0]
	v_mfma_scale_f32_16x16x128_f8f6f4 v[74:77], v[10:17], v[192:199], v[74:77], v1, v1 op_sel_hi:[0,0,0]
	v_mfma_scale_f32_16x16x128_f8f6f4 v[78:81], v[2:9], v[192:199], v[78:81], v1, v1 op_sel_hi:[0,0,0]
	v_mfma_scale_f32_16x16x128_f8f6f4 v[62:65], v[2:9], v[200:207], v[62:65], v1, v1 op_sel_hi:[0,0,0]
	v_mfma_scale_f32_16x16x128_f8f6f4 v[58:61], v[10:17], v[200:207], v[58:61], v1, v1 op_sel_hi:[0,0,0]
	v_mfma_scale_f32_16x16x128_f8f6f4 v[42:45], v[10:17], v[208:215], v[42:45], v1, v1 op_sel_hi:[0,0,0]
	v_mfma_scale_f32_16x16x128_f8f6f4 v[54:57], v[2:9], v[208:215], v[54:57], v1, v1 op_sel_hi:[0,0,0]
	s_setprio 0
	s_setprio 1
	v_mfma_scale_f32_16x16x128_f8f6f4 v[86:89], v[18:25], v[184:191], v[86:89], v1, v1 op_sel_hi:[0,0,0]
	v_mfma_scale_f32_16x16x128_f8f6f4 v[82:85], v[26:33], v[184:191], v[82:85], v1, v1 op_sel_hi:[0,0,0]
	v_mfma_scale_f32_16x16x128_f8f6f4 v[66:69], v[26:33], v[192:199], v[66:69], v1, v1 op_sel_hi:[0,0,0]
	v_mfma_scale_f32_16x16x128_f8f6f4 v[70:73], v[18:25], v[192:199], v[70:73], v1, v1 op_sel_hi:[0,0,0]
	v_mfma_scale_f32_16x16x128_f8f6f4 v[50:53], v[18:25], v[200:207], v[50:53], v1, v1 op_sel_hi:[0,0,0]
	v_mfma_scale_f32_16x16x128_f8f6f4 v[46:49], v[26:33], v[200:207], v[46:49], v1, v1 op_sel_hi:[0,0,0]
	v_mfma_scale_f32_16x16x128_f8f6f4 v[34:37], v[26:33], v[208:215], v[34:37], v1, v1 op_sel_hi:[0,0,0]
	v_mfma_scale_f32_16x16x128_f8f6f4 v[38:41], v[18:25], v[208:215], v[38:41], v1, v1 op_sel_hi:[0,0,0]
	s_setprio 0
	s_barrier
	s_movk_i32 s38, 0x100
	s_andn2_b64 vcc, exec, s[34:35]
	s_mov_b64 s[36:37], -1
	s_mov_b64 s[34:35], 0
	s_cbranch_vccz .LBB0_1558
	s_and_b64 vcc, exec, s[12:13]
	s_cbranch_vccz .LBB0_1561
	s_barrier

.LBB0_1681:
	ds_read_b128 v[26:29], v189
	ds_read_b128 v[30:33], v189 offset:1024
	ds_read_b128 v[18:21], v189 offset:2048
	ds_read_b128 v[22:25], v189 offset:3072
	ds_read_b128 v[10:13], v190
	ds_read_b128 v[14:17], v190 offset:1024
	ds_read_b128 v[2:5], v190 offset:2048
	ds_read_b128 v[6:9], v190 offset:3072
	s_add_u32 s34, s30, 0xfff80080
	s_addc_u32 s35, s31, -1
	s_cmp_eq_u32 s60, 28
	s_cselect_b32 s37, s18, s35
	s_cselect_b32 s36, s19, s34
	s_cselect_b32 s35, s21, s59
	s_cselect_b32 s34, s23, s58
	s_mov_b32 m0, s43
	s_nop 0
	global_load_lds_dwordx4 v168, s[100:101]
	s_mov_b32 m0, s44
	s_nop 0
	global_load_lds_dwordx4 v164, s[100:101]
	s_add_i32 m0, s29, 0xc000
	ds_read_b128 v[178:181], v191
	ds_read_b128 v[182:185], v191 offset:1024
	ds_read_b128 v[194:197], v191 offset:2048
	ds_read_b128 v[198:201], v191 offset:3072
	ds_read_b128 v[202:205], v191 offset:4096
	ds_read_b128 v[206:209], v191 offset:5120
	ds_read_b128 v[210:213], v191 offset:6144
	ds_read_b128 v[214:217], v191 offset:7168
	global_load_lds_dwordx4 v170, s[30:31]
	s_add_i32 m0, s29, 0xe000
	s_nop 0
	global_load_lds_dwordx4 v172, s[30:31]
	s_waitcnt vmcnt(8)
	s_waitcnt lgkmcnt(0)
	s_barrier
	s_setprio 1
	s_waitcnt lgkmcnt(0)
	v_mfma_scale_f32_16x16x128_f8f6f4 v[158:161], v[26:33], v[178:185], v[158:161], v1, v1 op_sel_hi:[0,0,0]
	v_mfma_scale_f32_16x16x128_f8f6f4 v[154:157], v[18:25], v[178:185], v[154:157], v1, v1 op_sel_hi:[0,0,0]
	v_mfma_scale_f32_16x16x128_f8f6f4 v[138:141], v[18:25], v[194:201], v[138:141], v1, v1 op_sel_hi:[0,0,0]
	v_mfma_scale_f32_16x16x128_f8f6f4 v[142:145], v[26:33], v[194:201], v[142:145], v1, v1 op_sel_hi:[0,0,0]
	v_mfma_scale_f32_16x16x128_f8f6f4 v[126:129], v[26:33], v[202:209], v[126:129], v1, v1 op_sel_hi:[0,0,0]
	v_mfma_scale_f32_16x16x128_f8f6f4 v[122:125], v[18:25], v[202:209], v[122:125], v1, v1 op_sel_hi:[0,0,0]
	v_mfma_scale_f32_16x16x128_f8f6f4 v[106:109], v[18:25], v[210:217], v[106:109], v1, v1 op_sel_hi:[0,0,0]
	v_mfma_scale_f32_16x16x128_f8f6f4 v[110:113], v[26:33], v[210:217], v[110:113], v1, v1 op_sel_hi:[0,0,0]
	s_setprio 0
	s_setprio 1
	v_mfma_scale_f32_16x16x128_f8f6f4 v[150:153], v[10:17], v[178:185], v[150:153], v1, v1 op_sel_hi:[0,0,0]
	v_mfma_scale_f32_16x16x128_f8f6f4 v[146:149], v[2:9], v[178:185], v[146:149], v1, v1 op_sel_hi:[0,0,0]
	v_mfma_scale_f32_16x16x128_f8f6f4 v[130:133], v[2:9], v[194:201], v[130:133], v1, v1 op_sel_hi:[0,0,0]
	v_mfma_scale_f32_16x16x128_f8f6f4 v[134:137], v[10:17], v[194:201], v[134:137], v1, v1 op_sel_hi:[0,0,0]
	v_mfma_scale_f32_16x16x128_f8f6f4 v[118:121], v[10:17], v[202:209], v[118:121], v1, v1 op_sel_hi:[0,0,0]
	v_mfma_scale_f32_16x16x128_f8f6f4 v[114:117], v[2:9], v[202:209], v[114:117], v1, v1 op_sel_hi:[0,0,0]
	v_mfma_scale_f32_16x16x128_f8f6f4 v[98:101], v[2:9], v[210:217], v[98:101], v1, v1 op_sel_hi:[0,0,0]
	v_mfma_scale_f32_16x16x128_f8f6f4 v[102:105], v[10:17], v[210:217], v[102:105], v1, v1 op_sel_hi:[0,0,0]
	s_setprio 0
	s_barrier
	s_add_i32 s61, s45, s3
	s_mov_b32 m0, s61
	ds_read_b128 v[194:197], v191 offset:16384
	ds_read_b128 v[198:201], v191 offset:17408
	ds_read_b128 v[202:205], v191 offset:18432
	ds_read_b128 v[206:209], v191 offset:19456
	ds_read_b128 v[210:213], v191 offset:20480
	ds_read_b128 v[214:217], v191 offset:21504
	ds_read_b128 v[218:221], v191 offset:22528
	ds_read_b128 v[222:225], v191 offset:23552
	global_load_lds_dwordx4 v166, s[34:35]
	s_add_i32 m0, s61, 0x2000
	s_add_u32 s62, s34, 0x80000
	s_addc_u32 s63, s35, 0
	s_add_i32 s61, s48, s3
	global_load_lds_dwordx4 v162, s[34:35]
	s_mov_b32 m0, s61
	s_nop 0
	global_load_lds_dwordx4 v166, s[62:63]
	s_add_i32 m0, s61, 0x2000
	s_nop 0
	global_load_lds_dwordx4 v162, s[62:63]
	s_waitcnt vmcnt(6)
	s_waitcnt lgkmcnt(0)
	s_barrier
	s_setprio 1
	s_waitcnt lgkmcnt(0)
	v_mfma_scale_f32_16x16x128_f8f6f4 v[94:97], v[26:33], v[194:201], v[94:97], v1, v1 op_sel_hi:[0,0,0]
	v_mfma_scale_f32_16x16x128_f8f6f4 v[90:93], v[18:25], v[194:201], v[90:93], v1, v1 op_sel_hi:[0,0,0]
	v_mfma_scale_f32_16x16x128_f8f6f4 v[74:77], v[18:25], v[202:209], v[74:77], v1, v1 op_sel_hi:[0,0,0]
	v_mfma_scale_f32_16x16x128_f8f6f4 v[78:81], v[26:33], v[202:209], v[78:81], v1, v1 op_sel_hi:[0,0,0]
	v_mfma_scale_f32_16x16x128_f8f6f4 v[62:65], v[26:33], v[210:217], v[62:65], v1, v1 op_sel_hi:[0,0,0]
	v_mfma_scale_f32_16x16x128_f8f6f4 v[58:61], v[18:25], v[210:217], v[58:61], v1, v1 op_sel_hi:[0,0,0]
	v_mfma_scale_f32_16x16x128_f8f6f4 v[42:45], v[18:25], v[218:225], v[42:45], v1, v1 op_sel_hi:[0,0,0]
	v_mfma_scale_f32_16x16x128_f8f6f4 v[46:49], v[26:33], v[218:225], v[46:49], v1, v1 op_sel_hi:[0,0,0]
	s_setprio 0
	s_setprio 1
	v_mfma_scale_f32_16x16x128_f8f6f4 v[86:89], v[10:17], v[194:201], v[86:89], v1, v1 op_sel_hi:[0,0,0]
	v_mfma_scale_f32_16x16x128_f8f6f4 v[82:85], v[2:9], v[194:201], v[82:85], v1, v1 op_sel_hi:[0,0,0]
	v_mfma_scale_f32_16x16x128_f8f6f4 v[66:69], v[2:9], v[202:209], v[66:69], v1, v1 op_sel_hi:[0,0,0]
	v_mfma_scale_f32_16x16x128_f8f6f4 v[70:73], v[10:17], v[202:209], v[70:73], v1, v1 op_sel_hi:[0,0,0]
	v_mfma_scale_f32_16x16x128_f8f6f4 v[54:57], v[10:17], v[210:217], v[54:57], v1, v1 op_sel_hi:[0,0,0]
	v_mfma_scale_f32_16x16x128_f8f6f4 v[50:53], v[2:9], v[210:217], v[50:53], v1, v1 op_sel_hi:[0,0,0]
	v_mfma_scale_f32_16x16x128_f8f6f4 v[34:37], v[2:9], v[218:225], v[34:37], v1, v1 op_sel_hi:[0,0,0]
	v_mfma_scale_f32_16x16x128_f8f6f4 v[38:41], v[10:17], v[218:225], v[38:41], v1, v1 op_sel_hi:[0,0,0]
	s_setprio 0
	s_barrier
	s_add_i32 s61, 0, 0x18000
	s_add_i32 s62, 0, 0x1c000
	v_add_u32_e32 v14, s61, v187
	v_add_u32_e32 v30, s62, v187
	ds_read_b128 v[2:5], v14
	ds_read_b128 v[6:9], v14 offset:1024
	ds_read_b128 v[10:13], v14 offset:2048
	ds_read_b128 v[14:17], v14 offset:3072
	ds_read_b128 v[18:21], v30
	ds_read_b128 v[22:25], v30 offset:1024
	ds_read_b128 v[26:29], v30 offset:2048
	ds_read_b128 v[30:33], v30 offset:3072
	s_mov_b32 m0, s29
	s_nop 0
	global_load_lds_dwordx4 v168, s[36:37]
	s_mov_b32 m0, s38
	s_nop 0
	global_load_lds_dwordx4 v164, s[36:37]
	s_add_u32 s36, s36, 0x80000
	s_addc_u32 s37, s37, 0
	s_add_u32 s100, s36, 0xfff80080
	s_addc_u32 s101, s37, -1
	s_mov_b32 m0, s39
	ds_read_b128 v[194:197], v191 offset:32768
	ds_read_b128 v[198:201], v191 offset:33792
	ds_read_b128 v[202:205], v191 offset:34816
	ds_read_b128 v[206:209], v191 offset:35840
	ds_read_b128 v[210:213], v191 offset:36864
	ds_read_b128 v[214:217], v191 offset:37888
	ds_read_b128 v[218:221], v191 offset:38912
	ds_read_b128 v[222:225], v191 offset:39936
	global_load_lds_dwordx4 v168, s[36:37]
	s_mov_b32 m0, s40
	s_nop 0
	global_load_lds_dwordx4 v164, s[36:37]
	s_waitcnt vmcnt(8)
	s_waitcnt lgkmcnt(0)
	s_barrier
	s_setprio 1
	s_waitcnt lgkmcnt(0)
	v_mfma_scale_f32_16x16x128_f8f6f4 v[158:161], v[2:9], v[194:201], v[158:161], v1, v1 op_sel_hi:[0,0,0]
	v_mfma_scale_f32_16x16x128_f8f6f4 v[154:157], v[10:17], v[194:201], v[154:157], v1, v1 op_sel_hi:[0,0,0]
	v_mfma_scale_f32_16x16x128_f8f6f4 v[138:141], v[10:17], v[202:209], v[138:141], v1, v1 op_sel_hi:[0,0,0]
	v_mfma_scale_f32_16x16x128_f8f6f4 v[142:145], v[2:9], v[202:209], v[142:145], v1, v1 op_sel_hi:[0,0,0]
	v_mfma_scale_f32_16x16x128_f8f6f4 v[126:129], v[2:9], v[210:217], v[126:129], v1, v1 op_sel_hi:[0,0,0]
	v_mfma_scale_f32_16x16x128_f8f6f4 v[122:125], v[10:17], v[210:217], v[122:125], v1, v1 op_sel_hi:[0,0,0]
	v_mfma_scale_f32_16x16x128_f8f6f4 v[106:109], v[10:17], v[218:225], v[106:109], v1, v1 op_sel_hi:[0,0,0]
	v_mfma_scale_f32_16x16x128_f8f6f4 v[110:113], v[2:9], v[218:225], v[110:113], v1, v1 op_sel_hi:[0,0,0]
	s_setprio 0
	s_setprio 1
	v_mfma_scale_f32_16x16x128_f8f6f4 v[150:153], v[18:25], v[194:201], v[150:153], v1, v1 op_sel_hi:[0,0,0]
	v_mfma_scale_f32_16x16x128_f8f6f4 v[146:149], v[26:33], v[194:201], v[146:149], v1, v1 op_sel_hi:[0,0,0]
	v_mfma_scale_f32_16x16x128_f8f6f4 v[130:133], v[26:33], v[202:209], v[130:133], v1, v1 op_sel_hi:[0,0,0]
	v_mfma_scale_f32_16x16x128_f8f6f4 v[134:137], v[18:25], v[202:209], v[134:137], v1, v1 op_sel_hi:[0,0,0]
	v_mfma_scale_f32_16x16x128_f8f6f4 v[118:121], v[18:25], v[210:217], v[118:121], v1, v1 op_sel_hi:[0,0,0]
	v_mfma_scale_f32_16x16x128_f8f6f4 v[114:117], v[26:33], v[210:217], v[114:117], v1, v1 op_sel_hi:[0,0,0]
	v_mfma_scale_f32_16x16x128_f8f6f4 v[98:101], v[26:33], v[218:225], v[98:101], v1, v1 op_sel_hi:[0,0,0]
	v_mfma_scale_f32_16x16x128_f8f6f4 v[102:105], v[18:25], v[218:225], v[102:105], v1, v1 op_sel_hi:[0,0,0]
	s_setprio 0
	s_barrier
	s_add_i32 s36, s61, s3
	s_mov_b32 m0, s36
	s_add_u32 s98, s34, 0x80
	s_addc_u32 s99, s35, 0
	ds_read_b128 v[194:197], v191 offset:49152
	ds_read_b128 v[198:201], v191 offset:50176
	ds_read_b128 v[202:205], v191 offset:51200
	ds_read_b128 v[206:209], v191 offset:52224
	ds_read_b128 v[210:213], v191 offset:53248
	ds_read_b128 v[214:217], v191 offset:54272
	ds_read_b128 v[218:221], v191 offset:55296
	ds_read_b128 v[222:225], v191 offset:56320
	global_load_lds_dwordx4 v166, s[98:99]
	s_add_i32 m0, s36, 0x2000
	s_add_u32 s34, s34, 0x80080
	s_addc_u32 s35, s35, 0
	s_add_i32 s36, s62, s3
	global_load_lds_dwordx4 v162, s[98:99]
	s_mov_b32 m0, s36
	s_nop 0
	global_load_lds_dwordx4 v166, s[34:35]
	s_add_i32 m0, s36, 0x2000
	s_nop 0
	global_load_lds_dwordx4 v162, s[34:35]
	s_waitcnt vmcnt(6)
	s_waitcnt lgkmcnt(0)
	s_barrier
	s_setprio 1
	s_waitcnt lgkmcnt(0)
	v_mfma_scale_f32_16x16x128_f8f6f4 v[94:97], v[2:9], v[194:201], v[94:97], v1, v1 op_sel_hi:[0,0,0]
	v_mfma_scale_f32_16x16x128_f8f6f4 v[90:93], v[10:17], v[194:201], v[90:93], v1, v1 op_sel_hi:[0,0,0]
	v_mfma_scale_f32_16x16x128_f8f6f4 v[74:77], v[10:17], v[202:209], v[74:77], v1, v1 op_sel_hi:[0,0,0]
	v_mfma_scale_f32_16x16x128_f8f6f4 v[78:81], v[2:9], v[202:209], v[78:81], v1, v1 op_sel_hi:[0,0,0]
	v_mfma_scale_f32_16x16x128_f8f6f4 v[62:65], v[2:9], v[210:217], v[62:65], v1, v1 op_sel_hi:[0,0,0]
	v_mfma_scale_f32_16x16x128_f8f6f4 v[58:61], v[10:17], v[210:217], v[58:61], v1, v1 op_sel_hi:[0,0,0]
	v_mfma_scale_f32_16x16x128_f8f6f4 v[42:45], v[10:17], v[218:225], v[42:45], v1, v1 op_sel_hi:[0,0,0]
	v_mfma_scale_f32_16x16x128_f8f6f4 v[46:49], v[2:9], v[218:225], v[46:49], v1, v1 op_sel_hi:[0,0,0]
	s_setprio 0
	s_setprio 1
	v_mfma_scale_f32_16x16x128_f8f6f4 v[86:89], v[18:25], v[194:201], v[86:89], v1, v1 op_sel_hi:[0,0,0]
	v_mfma_scale_f32_16x16x128_f8f6f4 v[82:85], v[26:33], v[194:201], v[82:85], v1, v1 op_sel_hi:[0,0,0]
	v_mfma_scale_f32_16x16x128_f8f6f4 v[66:69], v[26:33], v[202:209], v[66:69], v1, v1 op_sel_hi:[0,0,0]
	v_mfma_scale_f32_16x16x128_f8f6f4 v[70:73], v[18:25], v[202:209], v[70:73], v1, v1 op_sel_hi:[0,0,0]
	v_mfma_scale_f32_16x16x128_f8f6f4 v[54:57], v[18:25], v[210:217], v[54:57], v1, v1 op_sel_hi:[0,0,0]
	v_mfma_scale_f32_16x16x128_f8f6f4 v[50:53], v[26:33], v[210:217], v[50:53], v1, v1 op_sel_hi:[0,0,0]
	v_mfma_scale_f32_16x16x128_f8f6f4 v[34:37], v[26:33], v[218:225], v[34:37], v1, v1 op_sel_hi:[0,0,0]
	v_mfma_scale_f32_16x16x128_f8f6f4 v[38:41], v[18:25], v[218:225], v[38:41], v1, v1 op_sel_hi:[0,0,0]
	s_setprio 0
	s_barrier
	s_add_i32 s60, s60, 2
	s_add_u32 s30, s30, 0x100
	s_addc_u32 s31, s31, 0
	s_add_u32 s58, s58, 0x100
	s_addc_u32 s59, s59, 0
	s_cmp_gt_u32 s60, 29
	s_cbranch_scc0 .LBB0_1681
	s_and_b64 vcc, exec, s[12:13]
	s_cbranch_vccz .LBB0_1684
	s_barrier

.LBB0_1745:
	s_add_u32 s8, s49, s6
	s_addc_u32 s9, s50, s7
	s_add_u32 s8, s8, 0x32800100
	s_addc_u32 s9, s9, 0
	s_add_u32 s73, s51, s6
	s_addc_u32 s74, s54, s7
	s_add_i32 s72, 0, 0x10000
	s_cmpk_eq_i32 s6, 0x2a00
	s_cselect_b32 s37, s5, s9
	s_cselect_b32 s36, s4, s8
	s_cselect_b32 s9, s13, s74
	s_cselect_b32 s8, s12, s73
	s_add_i32 s73, 0, 0x14000
	v_add_u32_e32 v2, s72, v188
	v_add_u32_e32 v6, s73, v188
	ds_read_b128 v[26:29], v2
	ds_read_b128 v[30:33], v2 offset:1024
	ds_read_b128 v[18:21], v2 offset:2048
	ds_read_b128 v[22:25], v2 offset:3072
	ds_read_b128 v[10:13], v6
	ds_read_b128 v[14:17], v6 offset:1024
	ds_read_b128 v[2:5], v6 offset:2048
	ds_read_b128 v[6:9], v6 offset:3072
	v_lshl_add_u64 v[214:215], v[168:169], 0, s[6:7]
	s_add_i32 m0, s64, 0xc000
	ds_read_b128 v[172:175], v189
	ds_read_b128 v[176:179], v189 offset:1024
	ds_read_b128 v[190:193], v189 offset:2048
	ds_read_b128 v[194:197], v189 offset:3072
	ds_read_b128 v[198:201], v189 offset:4096
	ds_read_b128 v[202:205], v189 offset:5120
	ds_read_b128 v[206:209], v189 offset:6144
	ds_read_b128 v[210:213], v189 offset:7168
	global_load_lds_dwordx4 v[214:215], off
	v_lshl_add_u64 v[214:215], v[170:171], 0, s[6:7]
	s_add_i32 m0, s64, 0xe000
	s_nop 0
	global_load_lds_dwordx4 v[214:215], off
	s_waitcnt vmcnt(8)
	s_waitcnt lgkmcnt(0)
	s_barrier
	s_setprio 1
	s_waitcnt lgkmcnt(0)
	v_mfma_scale_f32_16x16x128_f8f6f4 v[158:161], v[26:33], v[172:179], v[158:161], v187, v187 op_sel_hi:[0,0,0]
	v_mfma_scale_f32_16x16x128_f8f6f4 v[154:157], v[18:25], v[172:179], v[154:157], v187, v187 op_sel_hi:[0,0,0]
	v_mfma_scale_f32_16x16x128_f8f6f4 v[118:121], v[18:25], v[190:197], v[118:121], v187, v187 op_sel_hi:[0,0,0]
	v_mfma_scale_f32_16x16x128_f8f6f4 v[122:125], v[26:33], v[190:197], v[122:125], v187, v187 op_sel_hi:[0,0,0]
	v_mfma_scale_f32_16x16x128_f8f6f4 v[126:129], v[26:33], v[198:205], v[126:129], v187, v187 op_sel_hi:[0,0,0]
	v_mfma_scale_f32_16x16x128_f8f6f4 v[114:117], v[18:25], v[198:205], v[114:117], v187, v187 op_sel_hi:[0,0,0]
	v_mfma_scale_f32_16x16x128_f8f6f4 v[106:109], v[18:25], v[206:213], v[106:109], v187, v187 op_sel_hi:[0,0,0]
	v_mfma_scale_f32_16x16x128_f8f6f4 v[110:113], v[26:33], v[206:213], v[110:113], v187, v187 op_sel_hi:[0,0,0]
	s_setprio 0
	s_setprio 1
	v_mfma_scale_f32_16x16x128_f8f6f4 v[150:153], v[10:17], v[172:179], v[150:153], v187, v187 op_sel_hi:[0,0,0]
	v_mfma_scale_f32_16x16x128_f8f6f4 v[146:149], v[2:9], v[172:179], v[146:149], v187, v187 op_sel_hi:[0,0,0]
	v_mfma_scale_f32_16x16x128_f8f6f4 v[138:141], v[2:9], v[190:197], v[138:141], v187, v187 op_sel_hi:[0,0,0]
	v_mfma_scale_f32_16x16x128_f8f6f4 v[142:145], v[10:17], v[190:197], v[142:145], v187, v187 op_sel_hi:[0,0,0]
	v_mfma_scale_f32_16x16x128_f8f6f4 v[134:137], v[10:17], v[198:205], v[134:137], v187, v187 op_sel_hi:[0,0,0]
	v_mfma_scale_f32_16x16x128_f8f6f4 v[130:133], v[2:9], v[198:205], v[130:133], v187, v187 op_sel_hi:[0,0,0]
	v_mfma_scale_f32_16x16x128_f8f6f4 v[98:101], v[2:9], v[206:213], v[98:101], v187, v187 op_sel_hi:[0,0,0]
	v_mfma_scale_f32_16x16x128_f8f6f4 v[102:105], v[10:17], v[206:213], v[102:105], v187, v187 op_sel_hi:[0,0,0]
	s_setprio 0
	s_barrier
	s_add_i32 s72, s72, s43
	v_lshl_add_u64 v[172:173], s[8:9], 0, v[162:163]
	s_mov_b32 m0, s72
	ds_read_b128 v[190:193], v189 offset:16384
	ds_read_b128 v[194:197], v189 offset:17408
	ds_read_b128 v[198:201], v189 offset:18432
	ds_read_b128 v[202:205], v189 offset:19456
	ds_read_b128 v[206:209], v189 offset:20480
	ds_read_b128 v[210:213], v189 offset:21504
	ds_read_b128 v[214:217], v189 offset:22528
	ds_read_b128 v[218:221], v189 offset:23552
	global_load_lds_dwordx4 v[172:173], off
	s_add_i32 m0, s72, 0x2000
	s_add_u32 s74, s8, 0x158000
	v_lshl_add_u64 v[174:175], s[8:9], 0, v[166:167]
	s_addc_u32 s75, s9, 0
	s_add_i32 s72, s73, s43
	global_load_lds_dwordx4 v[174:175], off
	v_lshl_add_u64 v[176:177], s[74:75], 0, v[162:163]
	s_mov_b32 m0, s72
	v_lshl_add_u64 v[178:179], s[36:37], 0, v[166:167]
	global_load_lds_dwordx4 v[176:177], off
	v_lshl_add_u64 v[176:177], s[74:75], 0, v[166:167]
	s_add_i32 m0, s72, 0x2000
	s_nop 0
	global_load_lds_dwordx4 v[176:177], off
	v_lshl_add_u64 v[176:177], s[36:37], 0, v[162:163]
	s_mov_b32 m0, s64
	s_nop 0
	global_load_lds_dwordx4 v[176:177], off
	s_mov_b32 m0, s65
	s_nop 0
	global_load_lds_dwordx4 v[178:179], off
	s_waitcnt vmcnt(8)
	s_waitcnt lgkmcnt(0)
	s_barrier
	s_setprio 1
	s_waitcnt lgkmcnt(0)
	v_mfma_scale_f32_16x16x128_f8f6f4 v[94:97], v[26:33], v[190:197], v[94:97], v187, v187 op_sel_hi:[0,0,0]
	v_mfma_scale_f32_16x16x128_f8f6f4 v[90:93], v[18:25], v[190:197], v[90:93], v187, v187 op_sel_hi:[0,0,0]
	v_mfma_scale_f32_16x16x128_f8f6f4 v[74:77], v[18:25], v[198:205], v[74:77], v187, v187 op_sel_hi:[0,0,0]
	v_mfma_scale_f32_16x16x128_f8f6f4 v[78:81], v[26:33], v[198:205], v[78:81], v187, v187 op_sel_hi:[0,0,0]
	v_mfma_scale_f32_16x16x128_f8f6f4 v[62:65], v[26:33], v[206:213], v[62:65], v187, v187 op_sel_hi:[0,0,0]
	v_mfma_scale_f32_16x16x128_f8f6f4 v[58:61], v[18:25], v[206:213], v[58:61], v187, v187 op_sel_hi:[0,0,0]
	v_mfma_scale_f32_16x16x128_f8f6f4 v[42:45], v[18:25], v[214:221], v[42:45], v187, v187 op_sel_hi:[0,0,0]
	v_mfma_scale_f32_16x16x128_f8f6f4 v[46:49], v[26:33], v[214:221], v[46:49], v187, v187 op_sel_hi:[0,0,0]
	s_setprio 0
	s_setprio 1
	v_mfma_scale_f32_16x16x128_f8f6f4 v[86:89], v[10:17], v[190:197], v[86:89], v187, v187 op_sel_hi:[0,0,0]
	v_mfma_scale_f32_16x16x128_f8f6f4 v[82:85], v[2:9], v[190:197], v[82:85], v187, v187 op_sel_hi:[0,0,0]
	v_mfma_scale_f32_16x16x128_f8f6f4 v[66:69], v[2:9], v[198:205], v[66:69], v187, v187 op_sel_hi:[0,0,0]
	v_mfma_scale_f32_16x16x128_f8f6f4 v[70:73], v[10:17], v[198:205], v[70:73], v187, v187 op_sel_hi:[0,0,0]
	v_mfma_scale_f32_16x16x128_f8f6f4 v[54:57], v[10:17], v[206:213], v[54:57], v187, v187 op_sel_hi:[0,0,0]
	v_mfma_scale_f32_16x16x128_f8f6f4 v[50:53], v[2:9], v[206:213], v[50:53], v187, v187 op_sel_hi:[0,0,0]
	v_mfma_scale_f32_16x16x128_f8f6f4 v[34:37], v[2:9], v[214:221], v[34:37], v187, v187 op_sel_hi:[0,0,0]
	v_mfma_scale_f32_16x16x128_f8f6f4 v[38:41], v[10:17], v[214:221], v[38:41], v187, v187 op_sel_hi:[0,0,0]
	s_setprio 0
	s_barrier
	s_add_i32 s72, 0, 0x18000
	s_add_i32 s73, 0, 0x1c000
	v_add_u32_e32 v14, s72, v188
	v_add_u32_e32 v30, s73, v188
	ds_read_b128 v[2:5], v14
	ds_read_b128 v[6:9], v14 offset:1024
	ds_read_b128 v[10:13], v14 offset:2048
	ds_read_b128 v[14:17], v14 offset:3072
	ds_read_b128 v[18:21], v30
	ds_read_b128 v[22:25], v30 offset:1024
	ds_read_b128 v[26:29], v30 offset:2048
	ds_read_b128 v[30:33], v30 offset:3072
	s_add_u32 s36, s36, 0x158000
	s_addc_u32 s37, s37, 0
	s_mov_b32 m0, s66
	v_lshl_add_u64 v[222:223], s[36:37], 0, v[162:163]
	ds_read_b128 v[190:193], v189 offset:32768
	ds_read_b128 v[194:197], v189 offset:33792
	ds_read_b128 v[198:201], v189 offset:34816
	ds_read_b128 v[202:205], v189 offset:35840
	ds_read_b128 v[206:209], v189 offset:36864
	ds_read_b128 v[210:213], v189 offset:37888
	ds_read_b128 v[214:217], v189 offset:38912
	ds_read_b128 v[218:221], v189 offset:39936
	global_load_lds_dwordx4 v[222:223], off
	v_lshl_add_u64 v[222:223], s[36:37], 0, v[166:167]
	s_mov_b32 m0, s67
	s_nop 0
	global_load_lds_dwordx4 v[222:223], off
	s_waitcnt vmcnt(8)
	s_waitcnt lgkmcnt(0)
	s_barrier
	s_setprio 1
	s_waitcnt lgkmcnt(0)
	v_mfma_scale_f32_16x16x128_f8f6f4 v[158:161], v[2:9], v[190:197], v[158:161], v187, v187 op_sel_hi:[0,0,0]
	v_mfma_scale_f32_16x16x128_f8f6f4 v[154:157], v[10:17], v[190:197], v[154:157], v187, v187 op_sel_hi:[0,0,0]
	v_mfma_scale_f32_16x16x128_f8f6f4 v[118:121], v[10:17], v[198:205], v[118:121], v187, v187 op_sel_hi:[0,0,0]
	v_mfma_scale_f32_16x16x128_f8f6f4 v[122:125], v[2:9], v[198:205], v[122:125], v187, v187 op_sel_hi:[0,0,0]
	v_mfma_scale_f32_16x16x128_f8f6f4 v[126:129], v[2:9], v[206:213], v[126:129], v187, v187 op_sel_hi:[0,0,0]
	v_mfma_scale_f32_16x16x128_f8f6f4 v[114:117], v[10:17], v[206:213], v[114:117], v187, v187 op_sel_hi:[0,0,0]
	v_mfma_scale_f32_16x16x128_f8f6f4 v[106:109], v[10:17], v[214:221], v[106:109], v187, v187 op_sel_hi:[0,0,0]
	v_mfma_scale_f32_16x16x128_f8f6f4 v[110:113], v[2:9], v[214:221], v[110:113], v187, v187 op_sel_hi:[0,0,0]
	s_setprio 0
	s_setprio 1
	v_mfma_scale_f32_16x16x128_f8f6f4 v[150:153], v[18:25], v[190:197], v[150:153], v187, v187 op_sel_hi:[0,0,0]
	v_mfma_scale_f32_16x16x128_f8f6f4 v[146:149], v[26:33], v[190:197], v[146:149], v187, v187 op_sel_hi:[0,0,0]
	v_mfma_scale_f32_16x16x128_f8f6f4 v[138:141], v[26:33], v[198:205], v[138:141], v187, v187 op_sel_hi:[0,0,0]
	v_mfma_scale_f32_16x16x128_f8f6f4 v[142:145], v[18:25], v[198:205], v[142:145], v187, v187 op_sel_hi:[0,0,0]
	v_mfma_scale_f32_16x16x128_f8f6f4 v[134:137], v[18:25], v[206:213], v[134:137], v187, v187 op_sel_hi:[0,0,0]
	v_mfma_scale_f32_16x16x128_f8f6f4 v[130:133], v[26:33], v[206:213], v[130:133], v187, v187 op_sel_hi:[0,0,0]
	v_mfma_scale_f32_16x16x128_f8f6f4 v[98:101], v[26:33], v[214:221], v[98:101], v187, v187 op_sel_hi:[0,0,0]
	v_mfma_scale_f32_16x16x128_f8f6f4 v[102:105], v[18:25], v[214:221], v[102:105], v187, v187 op_sel_hi:[0,0,0]
	s_setprio 0
	s_barrier
	s_add_i32 s36, s72, s43
	v_lshl_add_u64 v[172:173], v[172:173], 0, s[22:23]
	s_mov_b32 m0, s36
	ds_read_b128 v[190:193], v189 offset:49152
	ds_read_b128 v[194:197], v189 offset:50176
	ds_read_b128 v[198:201], v189 offset:51200
	ds_read_b128 v[202:205], v189 offset:52224
	ds_read_b128 v[206:209], v189 offset:53248
	ds_read_b128 v[210:213], v189 offset:54272
	ds_read_b128 v[214:217], v189 offset:55296
	ds_read_b128 v[218:221], v189 offset:56320
	global_load_lds_dwordx4 v[172:173], off
	s_add_i32 m0, s36, 0x2000
	s_add_u32 s8, s8, 0x158080
	v_lshl_add_u64 v[172:173], v[174:175], 0, s[22:23]
	s_addc_u32 s9, s9, 0
	s_add_i32 s36, s73, s43
	global_load_lds_dwordx4 v[172:173], off
	v_lshl_add_u64 v[172:173], s[8:9], 0, v[162:163]
	s_mov_b32 m0, s36
	s_nop 0
	global_load_lds_dwordx4 v[172:173], off
	v_lshl_add_u64 v[172:173], s[8:9], 0, v[166:167]
	s_add_i32 m0, s36, 0x2000
	s_nop 0
	global_load_lds_dwordx4 v[172:173], off
	v_lshl_add_u64 v[172:173], v[176:177], 0, s[22:23]
	s_mov_b32 m0, s69
	s_nop 0
	global_load_lds_dwordx4 v[172:173], off
	v_lshl_add_u64 v[172:173], v[178:179], 0, s[22:23]
	s_mov_b32 m0, s70
	s_nop 0
	global_load_lds_dwordx4 v[172:173], off
	s_waitcnt vmcnt(8)
	s_waitcnt lgkmcnt(0)
	s_barrier
	s_setprio 1
	s_waitcnt lgkmcnt(0)
	v_mfma_scale_f32_16x16x128_f8f6f4 v[94:97], v[2:9], v[190:197], v[94:97], v187, v187 op_sel_hi:[0,0,0]
	v_mfma_scale_f32_16x16x128_f8f6f4 v[90:93], v[10:17], v[190:197], v[90:93], v187, v187 op_sel_hi:[0,0,0]
	v_mfma_scale_f32_16x16x128_f8f6f4 v[74:77], v[10:17], v[198:205], v[74:77], v187, v187 op_sel_hi:[0,0,0]
	v_mfma_scale_f32_16x16x128_f8f6f4 v[78:81], v[2:9], v[198:205], v[78:81], v187, v187 op_sel_hi:[0,0,0]
	v_mfma_scale_f32_16x16x128_f8f6f4 v[62:65], v[2:9], v[206:213], v[62:65], v187, v187 op_sel_hi:[0,0,0]
	v_mfma_scale_f32_16x16x128_f8f6f4 v[58:61], v[10:17], v[206:213], v[58:61], v187, v187 op_sel_hi:[0,0,0]
	v_mfma_scale_f32_16x16x128_f8f6f4 v[42:45], v[10:17], v[214:221], v[42:45], v187, v187 op_sel_hi:[0,0,0]
	v_mfma_scale_f32_16x16x128_f8f6f4 v[46:49], v[2:9], v[214:221], v[46:49], v187, v187 op_sel_hi:[0,0,0]
	s_setprio 0
	s_setprio 1
	v_mfma_scale_f32_16x16x128_f8f6f4 v[86:89], v[18:25], v[190:197], v[86:89], v187, v187 op_sel_hi:[0,0,0]
	v_mfma_scale_f32_16x16x128_f8f6f4 v[82:85], v[26:33], v[190:197], v[82:85], v187, v187 op_sel_hi:[0,0,0]
	v_mfma_scale_f32_16x16x128_f8f6f4 v[66:69], v[26:33], v[198:205], v[66:69], v187, v187 op_sel_hi:[0,0,0]
	v_mfma_scale_f32_16x16x128_f8f6f4 v[70:73], v[18:25], v[198:205], v[70:73], v187, v187 op_sel_hi:[0,0,0]
	v_mfma_scale_f32_16x16x128_f8f6f4 v[54:57], v[18:25], v[206:213], v[54:57], v187, v187 op_sel_hi:[0,0,0]
	v_mfma_scale_f32_16x16x128_f8f6f4 v[50:53], v[26:33], v[206:213], v[50:53], v187, v187 op_sel_hi:[0,0,0]
	v_mfma_scale_f32_16x16x128_f8f6f4 v[34:37], v[26:33], v[214:221], v[34:37], v187, v187 op_sel_hi:[0,0,0]
	v_mfma_scale_f32_16x16x128_f8f6f4 v[38:41], v[18:25], v[214:221], v[38:41], v187, v187 op_sel_hi:[0,0,0]
	s_setprio 0
	s_barrier
	s_add_i32 s71, s71, 2
	s_add_u32 s6, s6, 0x100
	s_addc_u32 s7, s7, 0
	s_cmpk_lt_u32 s71, 0x54
	s_cbranch_scc1 .LBB0_1745
	s_waitcnt vmcnt(0)
	s_cmpk_gt_u32 s40, 0xff
	s_cbranch_scc1 .LBB0_1748
	s_barrier

.LBB0_1807:
	ds_read_b128 v[26:29], v185
	ds_read_b128 v[30:33], v185 offset:1024
	ds_read_b128 v[18:21], v185 offset:2048
	ds_read_b128 v[22:25], v185 offset:3072
	ds_read_b128 v[10:13], v186
	ds_read_b128 v[14:17], v186 offset:1024
	ds_read_b128 v[2:5], v186 offset:2048
	ds_read_b128 v[6:9], v186 offset:3072
	s_add_u32 s28, s26, 0xffea8080
	s_addc_u32 s29, s27, -1
	s_cmpk_eq_i32 s58, 0x52
	s_cselect_b32 s31, s5, s29
	s_cselect_b32 s30, s4, s28
	s_cselect_b32 s29, s25, s57
	s_cselect_b32 s28, s24, s56
	v_lshl_add_u64 v[212:213], s[26:27], 0, v[166:167]
	s_add_i32 m0, s34, 0xc000
	ds_read_b128 v[174:177], v187
	ds_read_b128 v[178:181], v187 offset:1024
	ds_read_b128 v[188:191], v187 offset:2048
	ds_read_b128 v[192:195], v187 offset:3072
	ds_read_b128 v[196:199], v187 offset:4096
	ds_read_b128 v[200:203], v187 offset:5120
	ds_read_b128 v[204:207], v187 offset:6144
	ds_read_b128 v[208:211], v187 offset:7168
	global_load_lds_dwordx4 v[212:213], off
	v_lshl_add_u64 v[212:213], s[26:27], 0, v[168:169]
	s_add_i32 m0, s34, 0xe000
	s_nop 0
	global_load_lds_dwordx4 v[212:213], off
	s_waitcnt vmcnt(8)
	s_waitcnt lgkmcnt(0)
	s_barrier
	s_setprio 1
	s_waitcnt lgkmcnt(0)
	v_mfma_scale_f32_16x16x128_f8f6f4 v[158:161], v[26:33], v[174:181], v[158:161], v1, v1 op_sel_hi:[0,0,0]
	v_mfma_scale_f32_16x16x128_f8f6f4 v[154:157], v[18:25], v[174:181], v[154:157], v1, v1 op_sel_hi:[0,0,0]
	v_mfma_scale_f32_16x16x128_f8f6f4 v[138:141], v[18:25], v[188:195], v[138:141], v1, v1 op_sel_hi:[0,0,0]
	v_mfma_scale_f32_16x16x128_f8f6f4 v[142:145], v[26:33], v[188:195], v[142:145], v1, v1 op_sel_hi:[0,0,0]
	v_mfma_scale_f32_16x16x128_f8f6f4 v[126:129], v[26:33], v[196:203], v[126:129], v1, v1 op_sel_hi:[0,0,0]
	v_mfma_scale_f32_16x16x128_f8f6f4 v[122:125], v[18:25], v[196:203], v[122:125], v1, v1 op_sel_hi:[0,0,0]
	v_mfma_scale_f32_16x16x128_f8f6f4 v[106:109], v[18:25], v[204:211], v[106:109], v1, v1 op_sel_hi:[0,0,0]
	v_mfma_scale_f32_16x16x128_f8f6f4 v[110:113], v[26:33], v[204:211], v[110:113], v1, v1 op_sel_hi:[0,0,0]
	s_setprio 0
	s_setprio 1
	v_mfma_scale_f32_16x16x128_f8f6f4 v[150:153], v[10:17], v[174:181], v[150:153], v1, v1 op_sel_hi:[0,0,0]
	v_mfma_scale_f32_16x16x128_f8f6f4 v[146:149], v[2:9], v[174:181], v[146:149], v1, v1 op_sel_hi:[0,0,0]
	v_mfma_scale_f32_16x16x128_f8f6f4 v[130:133], v[2:9], v[188:195], v[130:133], v1, v1 op_sel_hi:[0,0,0]
	v_mfma_scale_f32_16x16x128_f8f6f4 v[134:137], v[10:17], v[188:195], v[134:137], v1, v1 op_sel_hi:[0,0,0]
	v_mfma_scale_f32_16x16x128_f8f6f4 v[118:121], v[10:17], v[196:203], v[118:121], v1, v1 op_sel_hi:[0,0,0]
	v_mfma_scale_f32_16x16x128_f8f6f4 v[114:117], v[2:9], v[196:203], v[114:117], v1, v1 op_sel_hi:[0,0,0]
	v_mfma_scale_f32_16x16x128_f8f6f4 v[98:101], v[2:9], v[204:211], v[98:101], v1, v1 op_sel_hi:[0,0,0]
	v_mfma_scale_f32_16x16x128_f8f6f4 v[102:105], v[10:17], v[204:211], v[102:105], v1, v1 op_sel_hi:[0,0,0]
	s_setprio 0
	s_barrier
	s_add_i32 s59, s42, s3
	v_lshl_add_u64 v[174:175], s[28:29], 0, v[164:165]
	s_mov_b32 m0, s59
	ds_read_b128 v[188:191], v187 offset:16384
	ds_read_b128 v[192:195], v187 offset:17408
	ds_read_b128 v[196:199], v187 offset:18432
	ds_read_b128 v[200:203], v187 offset:19456
	ds_read_b128 v[204:207], v187 offset:20480
	ds_read_b128 v[208:211], v187 offset:21504
	ds_read_b128 v[212:215], v187 offset:22528
	ds_read_b128 v[216:219], v187 offset:23552
	global_load_lds_dwordx4 v[174:175], off
	s_add_i32 m0, s59, 0x2000
	s_add_u32 s60, s28, 0x158000
	v_lshl_add_u64 v[176:177], s[28:29], 0, v[162:163]
	s_addc_u32 s61, s29, 0
	s_add_i32 s59, s43, s3
	global_load_lds_dwordx4 v[176:177], off
	v_lshl_add_u64 v[178:179], s[60:61], 0, v[164:165]
	s_mov_b32 m0, s59
	v_lshl_add_u64 v[180:181], s[30:31], 0, v[162:163]
	global_load_lds_dwordx4 v[178:179], off
	v_lshl_add_u64 v[178:179], s[60:61], 0, v[162:163]
	s_add_i32 m0, s59, 0x2000
	s_nop 0
	global_load_lds_dwordx4 v[178:179], off
	v_lshl_add_u64 v[178:179], s[30:31], 0, v[164:165]
	s_mov_b32 m0, s34
	s_nop 0
	global_load_lds_dwordx4 v[178:179], off
	s_mov_b32 m0, s35
	s_nop 0
	global_load_lds_dwordx4 v[180:181], off
	s_waitcnt vmcnt(8)
	s_waitcnt lgkmcnt(0)
	s_barrier
	s_setprio 1
	s_waitcnt lgkmcnt(0)
	v_mfma_scale_f32_16x16x128_f8f6f4 v[94:97], v[26:33], v[188:195], v[94:97], v1, v1 op_sel_hi:[0,0,0]
	v_mfma_scale_f32_16x16x128_f8f6f4 v[90:93], v[18:25], v[188:195], v[90:93], v1, v1 op_sel_hi:[0,0,0]
	v_mfma_scale_f32_16x16x128_f8f6f4 v[74:77], v[18:25], v[196:203], v[74:77], v1, v1 op_sel_hi:[0,0,0]
	v_mfma_scale_f32_16x16x128_f8f6f4 v[78:81], v[26:33], v[196:203], v[78:81], v1, v1 op_sel_hi:[0,0,0]
	v_mfma_scale_f32_16x16x128_f8f6f4 v[62:65], v[26:33], v[204:211], v[62:65], v1, v1 op_sel_hi:[0,0,0]
	v_mfma_scale_f32_16x16x128_f8f6f4 v[58:61], v[18:25], v[204:211], v[58:61], v1, v1 op_sel_hi:[0,0,0]
	v_mfma_scale_f32_16x16x128_f8f6f4 v[42:45], v[18:25], v[212:219], v[42:45], v1, v1 op_sel_hi:[0,0,0]
	v_mfma_scale_f32_16x16x128_f8f6f4 v[54:57], v[26:33], v[212:219], v[54:57], v1, v1 op_sel_hi:[0,0,0]
	s_setprio 0
	s_setprio 1
	v_mfma_scale_f32_16x16x128_f8f6f4 v[86:89], v[10:17], v[188:195], v[86:89], v1, v1 op_sel_hi:[0,0,0]
	v_mfma_scale_f32_16x16x128_f8f6f4 v[82:85], v[2:9], v[188:195], v[82:85], v1, v1 op_sel_hi:[0,0,0]
	v_mfma_scale_f32_16x16x128_f8f6f4 v[66:69], v[2:9], v[196:203], v[66:69], v1, v1 op_sel_hi:[0,0,0]
	v_mfma_scale_f32_16x16x128_f8f6f4 v[70:73], v[10:17], v[196:203], v[70:73], v1, v1 op_sel_hi:[0,0,0]
	v_mfma_scale_f32_16x16x128_f8f6f4 v[50:53], v[10:17], v[204:211], v[50:53], v1, v1 op_sel_hi:[0,0,0]
	v_mfma_scale_f32_16x16x128_f8f6f4 v[46:49], v[2:9], v[204:211], v[46:49], v1, v1 op_sel_hi:[0,0,0]
	v_mfma_scale_f32_16x16x128_f8f6f4 v[34:37], v[2:9], v[212:219], v[34:37], v1, v1 op_sel_hi:[0,0,0]
	v_mfma_scale_f32_16x16x128_f8f6f4 v[38:41], v[10:17], v[212:219], v[38:41], v1, v1 op_sel_hi:[0,0,0]
	s_setprio 0
	s_barrier
	s_add_i32 s59, 0, 0x18000
	s_add_i32 s60, 0, 0x1c000
	v_add_u32_e32 v14, s59, v183
	v_add_u32_e32 v30, s60, v183
	ds_read_b128 v[2:5], v14
	ds_read_b128 v[6:9], v14 offset:1024
	ds_read_b128 v[10:13], v14 offset:2048
	ds_read_b128 v[14:17], v14 offset:3072
	ds_read_b128 v[18:21], v30
	ds_read_b128 v[22:25], v30 offset:1024
	ds_read_b128 v[26:29], v30 offset:2048
	ds_read_b128 v[30:33], v30 offset:3072
	s_add_u32 s30, s30, 0x158000
	s_addc_u32 s31, s31, 0
	s_mov_b32 m0, s36
	v_lshl_add_u64 v[220:221], s[30:31], 0, v[164:165]
	ds_read_b128 v[188:191], v187 offset:32768
	ds_read_b128 v[192:195], v187 offset:33792
	ds_read_b128 v[196:199], v187 offset:34816
	ds_read_b128 v[200:203], v187 offset:35840
	ds_read_b128 v[204:207], v187 offset:36864
	ds_read_b128 v[208:211], v187 offset:37888
	ds_read_b128 v[212:215], v187 offset:38912
	ds_read_b128 v[216:219], v187 offset:39936
	global_load_lds_dwordx4 v[220:221], off
	v_lshl_add_u64 v[220:221], s[30:31], 0, v[162:163]
	s_mov_b32 m0, s37
	s_nop 0
	global_load_lds_dwordx4 v[220:221], off
	s_waitcnt vmcnt(8)
	s_waitcnt lgkmcnt(0)
	s_barrier
	s_setprio 1
	s_waitcnt lgkmcnt(0)
	v_mfma_scale_f32_16x16x128_f8f6f4 v[158:161], v[2:9], v[188:195], v[158:161], v1, v1 op_sel_hi:[0,0,0]
	v_mfma_scale_f32_16x16x128_f8f6f4 v[154:157], v[10:17], v[188:195], v[154:157], v1, v1 op_sel_hi:[0,0,0]
	v_mfma_scale_f32_16x16x128_f8f6f4 v[138:141], v[10:17], v[196:203], v[138:141], v1, v1 op_sel_hi:[0,0,0]
	v_mfma_scale_f32_16x16x128_f8f6f4 v[142:145], v[2:9], v[196:203], v[142:145], v1, v1 op_sel_hi:[0,0,0]
	v_mfma_scale_f32_16x16x128_f8f6f4 v[126:129], v[2:9], v[204:211], v[126:129], v1, v1 op_sel_hi:[0,0,0]
	v_mfma_scale_f32_16x16x128_f8f6f4 v[122:125], v[10:17], v[204:211], v[122:125], v1, v1 op_sel_hi:[0,0,0]
	v_mfma_scale_f32_16x16x128_f8f6f4 v[106:109], v[10:17], v[212:219], v[106:109], v1, v1 op_sel_hi:[0,0,0]
	v_mfma_scale_f32_16x16x128_f8f6f4 v[110:113], v[2:9], v[212:219], v[110:113], v1, v1 op_sel_hi:[0,0,0]
	s_setprio 0
	s_setprio 1
	v_mfma_scale_f32_16x16x128_f8f6f4 v[150:153], v[18:25], v[188:195], v[150:153], v1, v1 op_sel_hi:[0,0,0]
	v_mfma_scale_f32_16x16x128_f8f6f4 v[146:149], v[26:33], v[188:195], v[146:149], v1, v1 op_sel_hi:[0,0,0]
	v_mfma_scale_f32_16x16x128_f8f6f4 v[130:133], v[26:33], v[196:203], v[130:133], v1, v1 op_sel_hi:[0,0,0]
	v_mfma_scale_f32_16x16x128_f8f6f4 v[134:137], v[18:25], v[196:203], v[134:137], v1, v1 op_sel_hi:[0,0,0]
	v_mfma_scale_f32_16x16x128_f8f6f4 v[118:121], v[18:25], v[204:211], v[118:121], v1, v1 op_sel_hi:[0,0,0]
	v_mfma_scale_f32_16x16x128_f8f6f4 v[114:117], v[26:33], v[204:211], v[114:117], v1, v1 op_sel_hi:[0,0,0]
	v_mfma_scale_f32_16x16x128_f8f6f4 v[98:101], v[26:33], v[212:219], v[98:101], v1, v1 op_sel_hi:[0,0,0]
	v_mfma_scale_f32_16x16x128_f8f6f4 v[102:105], v[18:25], v[212:219], v[102:105], v1, v1 op_sel_hi:[0,0,0]
	s_setprio 0
	s_barrier
	s_add_i32 s30, s59, s3
	v_lshl_add_u64 v[174:175], v[174:175], 0, s[10:11]
	s_mov_b32 m0, s30
	ds_read_b128 v[188:191], v187 offset:49152
	ds_read_b128 v[192:195], v187 offset:50176
	ds_read_b128 v[196:199], v187 offset:51200
	ds_read_b128 v[200:203], v187 offset:52224
	ds_read_b128 v[204:207], v187 offset:53248
	ds_read_b128 v[208:211], v187 offset:54272
	ds_read_b128 v[212:215], v187 offset:55296
	ds_read_b128 v[216:219], v187 offset:56320
	global_load_lds_dwordx4 v[174:175], off
	s_add_i32 m0, s30, 0x2000
	s_add_u32 s28, s28, 0x158080
	v_lshl_add_u64 v[174:175], v[176:177], 0, s[10:11]
	s_addc_u32 s29, s29, 0
	s_add_i32 s30, s60, s3
	global_load_lds_dwordx4 v[174:175], off
	v_lshl_add_u64 v[174:175], s[28:29], 0, v[164:165]
	s_mov_b32 m0, s30
	s_nop 0
	global_load_lds_dwordx4 v[174:175], off
	v_lshl_add_u64 v[174:175], s[28:29], 0, v[162:163]
	s_add_i32 m0, s30, 0x2000
	s_nop 0
	global_load_lds_dwordx4 v[174:175], off
	v_lshl_add_u64 v[174:175], v[178:179], 0, s[10:11]
	s_mov_b32 m0, s40
	s_nop 0
	global_load_lds_dwordx4 v[174:175], off
	v_lshl_add_u64 v[174:175], v[180:181], 0, s[10:11]
	s_mov_b32 m0, s41
	s_nop 0
	global_load_lds_dwordx4 v[174:175], off
	s_waitcnt vmcnt(8)
	s_waitcnt lgkmcnt(0)
	s_barrier
	s_setprio 1
	s_waitcnt lgkmcnt(0)
	v_mfma_scale_f32_16x16x128_f8f6f4 v[94:97], v[2:9], v[188:195], v[94:97], v1, v1 op_sel_hi:[0,0,0]
	v_mfma_scale_f32_16x16x128_f8f6f4 v[90:93], v[10:17], v[188:195], v[90:93], v1, v1 op_sel_hi:[0,0,0]
	v_mfma_scale_f32_16x16x128_f8f6f4 v[74:77], v[10:17], v[196:203], v[74:77], v1, v1 op_sel_hi:[0,0,0]
	v_mfma_scale_f32_16x16x128_f8f6f4 v[78:81], v[2:9], v[196:203], v[78:81], v1, v1 op_sel_hi:[0,0,0]
	v_mfma_scale_f32_16x16x128_f8f6f4 v[62:65], v[2:9], v[204:211], v[62:65], v1, v1 op_sel_hi:[0,0,0]
	v_mfma_scale_f32_16x16x128_f8f6f4 v[58:61], v[10:17], v[204:211], v[58:61], v1, v1 op_sel_hi:[0,0,0]
	v_mfma_scale_f32_16x16x128_f8f6f4 v[42:45], v[10:17], v[212:219], v[42:45], v1, v1 op_sel_hi:[0,0,0]
	v_mfma_scale_f32_16x16x128_f8f6f4 v[54:57], v[2:9], v[212:219], v[54:57], v1, v1 op_sel_hi:[0,0,0]
	s_setprio 0
	s_setprio 1
	v_mfma_scale_f32_16x16x128_f8f6f4 v[86:89], v[18:25], v[188:195], v[86:89], v1, v1 op_sel_hi:[0,0,0]
	v_mfma_scale_f32_16x16x128_f8f6f4 v[82:85], v[26:33], v[188:195], v[82:85], v1, v1 op_sel_hi:[0,0,0]
	v_mfma_scale_f32_16x16x128_f8f6f4 v[66:69], v[26:33], v[196:203], v[66:69], v1, v1 op_sel_hi:[0,0,0]
	v_mfma_scale_f32_16x16x128_f8f6f4 v[70:73], v[18:25], v[196:203], v[70:73], v1, v1 op_sel_hi:[0,0,0]
	v_mfma_scale_f32_16x16x128_f8f6f4 v[50:53], v[18:25], v[204:211], v[50:53], v1, v1 op_sel_hi:[0,0,0]
	v_mfma_scale_f32_16x16x128_f8f6f4 v[46:49], v[26:33], v[204:211], v[46:49], v1, v1 op_sel_hi:[0,0,0]
	v_mfma_scale_f32_16x16x128_f8f6f4 v[34:37], v[26:33], v[212:219], v[34:37], v1, v1 op_sel_hi:[0,0,0]
	v_mfma_scale_f32_16x16x128_f8f6f4 v[38:41], v[18:25], v[212:219], v[38:41], v1, v1 op_sel_hi:[0,0,0]
	s_setprio 0
	s_barrier
	s_add_i32 s58, s58, 2
	s_add_u32 s26, s26, 0x100
	s_addc_u32 s27, s27, 0
	s_add_u32 s56, s56, 0x100
	s_addc_u32 s57, s57, 0
	s_cmpk_gt_u32 s58, 0x53
	s_cbranch_scc0 .LBB0_1807
	s_and_b64 vcc, exec, s[12:13]
	s_cbranch_vccz .LBB0_1810
	s_barrier
